# peeled first K-iteration of every GEMM tile with inline-zero C operand: no per-tile accumulator zeroing; plus saddr LDS-DMA
# speedup vs baseline: 1.0172x; 1.0172x over previous
; #define PG8_STAGE(bufoff, gbase, voff) do { _Pragma("unroll") for (int _i = 0; _i < 2; ++_i) \
;         __builtin_amdgcn_global_load_lds((const unsigned*)((const char*)(gbase) + (voff)[_i]), (PG8_LAS unsigned*)(lds + (bufoff) + ldsw + _i * 8192), 16, 0, 0); } while (0)
; #define PG8_LDA(dst, b, h) do { _Pragma("unroll") for (int m = 0; m < 4; ++m) _Pragma("unroll") for (int k = 0; k < 2; ++k) dst[m][k] = *(const PG8_LAS bf16x8*)(lds + PG8_SA(b, h) + aoff + m * 2048 + k * 1024); } while (0)
; template <class Epi, class Sched, bool ALIGN_EPI = false, bool SP2 = false>
; __device__ __forceinline__ void gemm_phase(PG8_LAS unsigned char* lds, const Gemm g, const Sched& S, const Epi& E) {
;     ...
;         const bool has_next = S.next(ui + 1, nxt);
;         const char* nA = has_next ? (const char*)g.A + (size_t)nxt.pm * tstep : cA; const char* nB = has_next ? (const char*)g.Bt + (size_t)nxt.pn * tstep : cB;
;         for (int t = 0; t < nt; t += 2) {
;             const bool last = (t == nt - 2);
;             const char* a1 = cA + (size_t)(t + 1) * kstep;
;             const char* a2 = last ? nA : cA + (size_t)(t + 2) * kstep; const char* b2 = last ? nB : cB + (size_t)(t + 2) * kstep;
;             const char* a3 = a2 + kstep; const char* b3 = b2 + kstep;
;             if (last && has_next) S.a_ready(nxt);
;             if constexpr (SP2) {
;             PG8_LDB(B0, 0, 0); PG8_LDB(B1, 0, 1); PG8_SCHED; PG8_LDA(At, 0, 0); PG8_STAGE(PG8_SA(1, 1), a1 + hstep, voffA);
;             PG8_WAIT_V(8); PG8_WAIT_L(0); PG8_BAR; PG8_MMA(0, 0, At, B0); PG8_MMA(0, 1, At, B1); PG8_BAR; PG8_SCHED;
;             PG8_LDA(At, 0, 1); PG8_STAGE(PG8_SB(0, 0), b2, voffB); PG8_STAGE(PG8_SB(0, 1), b2 + hstep, voffB); PG8_STAGE(PG8_SA(0, 0), a2, voffA);
;             PG8_WAIT_V(8); PG8_WAIT_L(0); PG8_BAR; PG8_MMA(1, 0, At, B0); PG8_MMA(1, 1, At, B1); PG8_BAR; PG8_SCHED;
;             PG8_LDB(B0, 1, 0); PG8_LDB(B1, 1, 1); PG8_SCHED; PG8_LDA(At, 1, 0); PG8_STAGE(PG8_SA(0, 1), a2 + hstep, voffA);
;             PG8_WAIT_V(8); PG8_WAIT_L(0); PG8_BAR; PG8_MMA(0, 0, At, B0); PG8_MMA(0, 1, At, B1); PG8_BAR; PG8_SCHED;
;             PG8_LDA(At, 1, 1); PG8_STAGE(PG8_SB(1, 0), b3, voffB); PG8_STAGE(PG8_SB(1, 1), b3 + hstep, voffB); PG8_STAGE(PG8_SA(1, 0), a3, voffA);
;             PG8_WAIT_V(8); PG8_WAIT_L(0); PG8_BAR; PG8_MMA(1, 0, At, B0); PG8_MMA(1, 1, At, B1); PG8_BAR; PG8_SCHED;
.LBB0_366:
	s_ashr_i32 s23, s22, 31
	s_lshl_b64 s[24:25], s[22:23], 20
	s_add_u32 s24, s70, s24
	s_addc_u32 s25, s71, s25
	s_and_b64 s[26:27], s[2:3], exec
	s_cselect_b32 s23, s25, s31
	s_cselect_b32 s29, s24, s30
	s_ashr_i32 s21, s20, 31
	s_lshl_b64 s[26:27], s[20:21], 20
	s_add_u32 s26, s33, s26
	s_addc_u32 s27, s38, s27
	s_and_b64 s[36:37], s[2:3], exec
	s_cselect_b32 s21, s27, s35
	s_cselect_b32 s55, s26, s34
	s_add_u32 s30, s30, 0x80080
	s_addc_u32 s31, s31, 0
	s_add_u32 s56, s34, 0x100
	s_addc_u32 s57, s35, 0
	s_mov_b32 s58, -2
	v_add_u32_e32 v248, 0x18000, v154
	v_add_u32_e32 v249, 0x1c000, v154
	ds_read_b128 v[148:151], v156
	ds_read_b128 v[160:163], v156 offset:1024
	ds_read_b128 v[164:167], v156 offset:2048
	ds_read_b128 v[168:171], v156 offset:3072
	ds_read_b128 v[172:175], v157
	ds_read_b128 v[176:179], v157 offset:1024
	ds_read_b128 v[180:183], v157 offset:2048
	ds_read_b128 v[188:191], v157 offset:3072
	s_add_u32 s34, s30, 0xfff80080
	s_addc_u32 s35, s31, -1
	s_cmp_eq_u32 s58, 28
	s_cselect_b32 s37, s23, s35
	s_cselect_b32 s36, s29, s34
	s_cselect_b32 s35, s21, s57
	s_cselect_b32 s34, s55, s56
	s_add_i32 m0, s42, 0xc000
	ds_read_b128 v[192:195], v158
	ds_read_b128 v[196:199], v158 offset:1024
	ds_read_b128 v[200:203], v158 offset:2048
	ds_read_b128 v[204:207], v158 offset:3072
	ds_read_b128 v[212:215], v158 offset:4096
	ds_read_b128 v[216:219], v158 offset:5120
	ds_read_b128 v[220:223], v158 offset:6144
	ds_read_b128 v[224:227], v158 offset:7168
	global_load_lds_dwordx4 v140, s[30:31]
	s_add_i32 m0, s42, 0xe000
	s_nop 0
	global_load_lds_dwordx4 v142, s[30:31]
	s_waitcnt vmcnt(8)
	s_waitcnt lgkmcnt(0)
	s_barrier
	s_setprio 1
	s_waitcnt lgkmcnt(0)
	v_mfma_f32_16x16x32_bf16 v[126:129], v[148:151], v[192:195], 0
	v_mfma_f32_16x16x32_bf16 v[122:125], v[164:167], v[192:195], 0
	v_mfma_f32_16x16x32_bf16 v[118:121], v[148:151], v[200:203], 0
	v_mfma_f32_16x16x32_bf16 v[110:113], v[164:167], v[200:203], 0
	v_mfma_f32_16x16x32_bf16 v[102:105], v[148:151], v[212:215], 0
	v_mfma_f32_16x16x32_bf16 v[94:97], v[164:167], v[212:215], 0
	v_mfma_f32_16x16x32_bf16 v[86:89], v[148:151], v[220:223], 0
	v_mfma_f32_16x16x32_bf16 v[78:81], v[164:167], v[220:223], 0
	v_mfma_f32_16x16x32_bf16 v[126:129], v[160:163], v[196:199], v[126:129]
	v_mfma_f32_16x16x32_bf16 v[122:125], v[168:171], v[196:199], v[122:125]
	v_mfma_f32_16x16x32_bf16 v[118:121], v[160:163], v[204:207], v[118:121]
	v_mfma_f32_16x16x32_bf16 v[110:113], v[168:171], v[204:207], v[110:113]
	v_mfma_f32_16x16x32_bf16 v[102:105], v[160:163], v[216:219], v[102:105]
	v_mfma_f32_16x16x32_bf16 v[94:97], v[168:171], v[216:219], v[94:97]
	v_mfma_f32_16x16x32_bf16 v[86:89], v[160:163], v[224:227], v[86:89]
	v_mfma_f32_16x16x32_bf16 v[78:81], v[168:171], v[224:227], v[78:81]
	s_setprio 0
	s_setprio 1
	v_mfma_f32_16x16x32_bf16 v[114:117], v[172:175], v[192:195], 0
	v_mfma_f32_16x16x32_bf16 v[106:109], v[180:183], v[192:195], 0
	v_mfma_f32_16x16x32_bf16 v[98:101], v[172:175], v[200:203], 0
	v_mfma_f32_16x16x32_bf16 v[90:93], v[180:183], v[200:203], 0
	v_mfma_f32_16x16x32_bf16 v[82:85], v[172:175], v[212:215], 0
	v_mfma_f32_16x16x32_bf16 v[74:77], v[180:183], v[212:215], 0
	v_mfma_f32_16x16x32_bf16 v[70:73], v[172:175], v[220:223], 0
	v_mfma_f32_16x16x32_bf16 v[66:69], v[180:183], v[220:223], 0
	v_mfma_f32_16x16x32_bf16 v[114:117], v[176:179], v[196:199], v[114:117]
	v_mfma_f32_16x16x32_bf16 v[106:109], v[188:191], v[196:199], v[106:109]
	v_mfma_f32_16x16x32_bf16 v[98:101], v[176:179], v[204:207], v[98:101]
	v_mfma_f32_16x16x32_bf16 v[90:93], v[188:191], v[204:207], v[90:93]
	v_mfma_f32_16x16x32_bf16 v[82:85], v[176:179], v[216:219], v[82:85]
	v_mfma_f32_16x16x32_bf16 v[74:77], v[188:191], v[216:219], v[74:77]
	v_mfma_f32_16x16x32_bf16 v[70:73], v[176:179], v[224:227], v[70:73]
	v_mfma_f32_16x16x32_bf16 v[66:69], v[188:191], v[224:227], v[66:69]
	s_setprio 0
	s_barrier
	s_add_i32 s59, s51, s39
	s_mov_b32 m0, s59
	ds_read_b128 v[192:195], v158 offset:16384
	ds_read_b128 v[196:199], v158 offset:17408
	ds_read_b128 v[200:203], v158 offset:18432
	ds_read_b128 v[204:207], v158 offset:19456
	ds_read_b128 v[212:215], v158 offset:20480
	ds_read_b128 v[216:219], v158 offset:21504
	ds_read_b128 v[220:223], v158 offset:22528
	ds_read_b128 v[224:227], v158 offset:23552
	global_load_lds_dwordx4 v134, s[34:35]
	s_add_i32 m0, s59, 0x2000
	s_add_u32 s60, s34, 0x80000
	s_addc_u32 s61, s35, 0
	s_add_i32 s59, s52, s39
	global_load_lds_dwordx4 v130, s[34:35]
	s_mov_b32 m0, s59
	s_nop 0
	global_load_lds_dwordx4 v134, s[60:61]
	s_add_i32 m0, s59, 0x2000
	s_nop 0
	global_load_lds_dwordx4 v130, s[60:61]
	s_mov_b32 m0, s42
	s_nop 0
	global_load_lds_dwordx4 v136, s[36:37]
	s_mov_b32 m0, s43
	s_nop 0
	global_load_lds_dwordx4 v132, s[36:37]
	s_waitcnt vmcnt(8)
	s_waitcnt lgkmcnt(0)
	s_barrier
; #define PG8_STAGE(bufoff, gbase, voff) do { _Pragma("unroll") for (int _i = 0; _i < 2; ++_i) \
;         __builtin_amdgcn_global_load_lds((const unsigned*)((const char*)(gbase) + (voff)[_i]), (PG8_LAS unsigned*)(lds + (bufoff) + ldsw + _i * 8192), 16, 0, 0); } while (0)
; #define PG8_LDA(dst, b, h) do { _Pragma("unroll") for (int m = 0; m < 4; ++m) _Pragma("unroll") for (int k = 0; k < 2; ++k) dst[m][k] = *(const PG8_LAS bf16x8*)(lds + PG8_SA(b, h) + aoff + m * 2048 + k * 1024); } while (0)
; #define PG8_LDB(dst, b, h) do { _Pragma("unroll") for (int n = 0; n < 2; ++n) _Pragma("unroll") for (int k = 0; k < 2; ++k) dst[n][k] = *(const PG8_LAS bf16x8*)(lds + PG8_SB(b, h) + boff + n * 2048 + k * 1024); } while (0)
; #define PG8_WAIT_V(n) asm volatile("s_waitcnt vmcnt(" #n ")" ::: "memory")
; #define PG8_WAIT_L(n) asm volatile("s_waitcnt lgkmcnt(" #n ")" ::: "memory")
; #define PG8_BAR __builtin_amdgcn_s_barrier()
; #define PG8_SCHED __builtin_amdgcn_sched_barrier(0)
; template <class Epi, class Sched, bool ALIGN_EPI = false, bool SP2 = false>
; __device__ __forceinline__ void gemm_phase(PG8_LAS unsigned char* lds, const Gemm g, const Sched& S, const Epi& E) {
;     ...
;             PG8_WAIT_V(8); PG8_WAIT_L(0); PG8_BAR; PG8_MMA(1, 0, At, B0); PG8_MMA(1, 1, At, B1); PG8_BAR; PG8_SCHED;
;             PG8_LDB(B0, 1, 0); PG8_LDB(B1, 1, 1); PG8_SCHED; PG8_LDA(At, 1, 0); PG8_STAGE(PG8_SA(0, 1), a2 + hstep, voffA);
;             PG8_WAIT_V(8); PG8_WAIT_L(0); PG8_BAR; PG8_MMA(0, 0, At, B0); PG8_MMA(0, 1, At, B1); PG8_BAR; PG8_SCHED;
	s_setprio 1
	s_waitcnt lgkmcnt(0)
	v_mfma_f32_16x16x32_bf16 v[62:65], v[148:151], v[192:195], 0
	v_mfma_f32_16x16x32_bf16 v[58:61], v[164:167], v[192:195], 0
	v_mfma_f32_16x16x32_bf16 v[54:57], v[148:151], v[200:203], 0
	v_mfma_f32_16x16x32_bf16 v[46:49], v[164:167], v[200:203], 0
	v_mfma_f32_16x16x32_bf16 v[38:41], v[148:151], v[212:215], 0
	v_mfma_f32_16x16x32_bf16 v[30:33], v[164:167], v[212:215], 0
	v_mfma_f32_16x16x32_bf16 v[22:25], v[148:151], v[220:223], 0
	v_mfma_f32_16x16x32_bf16 v[14:17], v[164:167], v[220:223], 0
	v_mfma_f32_16x16x32_bf16 v[62:65], v[160:163], v[196:199], v[62:65]
	v_mfma_f32_16x16x32_bf16 v[58:61], v[168:171], v[196:199], v[58:61]
	v_mfma_f32_16x16x32_bf16 v[54:57], v[160:163], v[204:207], v[54:57]
	v_mfma_f32_16x16x32_bf16 v[46:49], v[168:171], v[204:207], v[46:49]
	v_mfma_f32_16x16x32_bf16 v[38:41], v[160:163], v[216:219], v[38:41]
	v_mfma_f32_16x16x32_bf16 v[30:33], v[168:171], v[216:219], v[30:33]
	v_mfma_f32_16x16x32_bf16 v[22:25], v[160:163], v[224:227], v[22:25]
	v_mfma_f32_16x16x32_bf16 v[14:17], v[168:171], v[224:227], v[14:17]
	s_setprio 0
	s_setprio 1
	v_mfma_f32_16x16x32_bf16 v[50:53], v[172:175], v[192:195], 0
	v_mfma_f32_16x16x32_bf16 v[42:45], v[180:183], v[192:195], 0
	v_mfma_f32_16x16x32_bf16 v[34:37], v[172:175], v[200:203], 0
	v_mfma_f32_16x16x32_bf16 v[26:29], v[180:183], v[200:203], 0
	v_mfma_f32_16x16x32_bf16 v[18:21], v[172:175], v[212:215], 0
	v_mfma_f32_16x16x32_bf16 v[10:13], v[180:183], v[212:215], 0
	v_mfma_f32_16x16x32_bf16 v[6:9], v[172:175], v[220:223], 0
	v_mfma_f32_16x16x32_bf16 v[2:5], v[180:183], v[220:223], 0
	v_mfma_f32_16x16x32_bf16 v[50:53], v[176:179], v[196:199], v[50:53]
	v_mfma_f32_16x16x32_bf16 v[42:45], v[188:191], v[196:199], v[42:45]
	v_mfma_f32_16x16x32_bf16 v[34:37], v[176:179], v[204:207], v[34:37]
	v_mfma_f32_16x16x32_bf16 v[26:29], v[188:191], v[204:207], v[26:29]
	v_mfma_f32_16x16x32_bf16 v[18:21], v[176:179], v[216:219], v[18:21]
	v_mfma_f32_16x16x32_bf16 v[10:13], v[188:191], v[216:219], v[10:13]
	v_mfma_f32_16x16x32_bf16 v[6:9], v[176:179], v[224:227], v[6:9]
	v_mfma_f32_16x16x32_bf16 v[2:5], v[188:191], v[224:227], v[2:5]
	s_setprio 0
	s_barrier
	s_add_i32 s59, 0, 0x18000
	s_add_i32 s60, 0, 0x1c000
	ds_read_b128 v[148:151], v248
	ds_read_b128 v[160:163], v248 offset:1024
	ds_read_b128 v[164:167], v248 offset:2048
	ds_read_b128 v[168:171], v248 offset:3072
	ds_read_b128 v[172:175], v249
	ds_read_b128 v[176:179], v249 offset:1024
	ds_read_b128 v[180:183], v249 offset:2048
	ds_read_b128 v[188:191], v249 offset:3072
	s_add_u32 s36, s36, 0x80000
	s_addc_u32 s37, s37, 0
	s_mov_b32 m0, s44
	ds_read_b128 v[192:195], v158 offset:32768
	ds_read_b128 v[196:199], v158 offset:33792
	ds_read_b128 v[200:203], v158 offset:34816
	ds_read_b128 v[204:207], v158 offset:35840
	ds_read_b128 v[212:215], v158 offset:36864
	ds_read_b128 v[216:219], v158 offset:37888
	ds_read_b128 v[220:223], v158 offset:38912
	ds_read_b128 v[224:227], v158 offset:39936
	global_load_lds_dwordx4 v136, s[36:37]
	s_mov_b32 m0, s45
	s_nop 0
	global_load_lds_dwordx4 v132, s[36:37]
	s_waitcnt vmcnt(8)
	s_waitcnt lgkmcnt(0)
	s_barrier
	s_setprio 1
	s_waitcnt lgkmcnt(0)
	v_mfma_f32_16x16x32_bf16 v[126:129], v[148:151], v[192:195], v[126:129]
	v_mfma_f32_16x16x32_bf16 v[122:125], v[164:167], v[192:195], v[122:125]
	v_mfma_f32_16x16x32_bf16 v[118:121], v[148:151], v[200:203], v[118:121]
	v_mfma_f32_16x16x32_bf16 v[110:113], v[164:167], v[200:203], v[110:113]
	v_mfma_f32_16x16x32_bf16 v[102:105], v[148:151], v[212:215], v[102:105]
	v_mfma_f32_16x16x32_bf16 v[94:97], v[164:167], v[212:215], v[94:97]
	v_mfma_f32_16x16x32_bf16 v[86:89], v[148:151], v[220:223], v[86:89]
	v_mfma_f32_16x16x32_bf16 v[78:81], v[164:167], v[220:223], v[78:81]
	v_mfma_f32_16x16x32_bf16 v[126:129], v[160:163], v[196:199], v[126:129]
	v_mfma_f32_16x16x32_bf16 v[122:125], v[168:171], v[196:199], v[122:125]
	v_mfma_f32_16x16x32_bf16 v[118:121], v[160:163], v[204:207], v[118:121]
	v_mfma_f32_16x16x32_bf16 v[110:113], v[168:171], v[204:207], v[110:113]
	v_mfma_f32_16x16x32_bf16 v[102:105], v[160:163], v[216:219], v[102:105]
	v_mfma_f32_16x16x32_bf16 v[94:97], v[168:171], v[216:219], v[94:97]
	v_mfma_f32_16x16x32_bf16 v[86:89], v[160:163], v[224:227], v[86:89]
	v_mfma_f32_16x16x32_bf16 v[78:81], v[168:171], v[224:227], v[78:81]
	s_setprio 0
	s_setprio 1
	v_mfma_f32_16x16x32_bf16 v[114:117], v[172:175], v[192:195], v[114:117]
	v_mfma_f32_16x16x32_bf16 v[106:109], v[180:183], v[192:195], v[106:109]
	v_mfma_f32_16x16x32_bf16 v[98:101], v[172:175], v[200:203], v[98:101]
	v_mfma_f32_16x16x32_bf16 v[90:93], v[180:183], v[200:203], v[90:93]
	v_mfma_f32_16x16x32_bf16 v[82:85], v[172:175], v[212:215], v[82:85]
	v_mfma_f32_16x16x32_bf16 v[74:77], v[180:183], v[212:215], v[74:77]
	v_mfma_f32_16x16x32_bf16 v[70:73], v[172:175], v[220:223], v[70:73]
	v_mfma_f32_16x16x32_bf16 v[66:69], v[180:183], v[220:223], v[66:69]
	v_mfma_f32_16x16x32_bf16 v[114:117], v[176:179], v[196:199], v[114:117]
	v_mfma_f32_16x16x32_bf16 v[106:109], v[188:191], v[196:199], v[106:109]
	v_mfma_f32_16x16x32_bf16 v[98:101], v[176:179], v[204:207], v[98:101]
	v_mfma_f32_16x16x32_bf16 v[90:93], v[188:191], v[204:207], v[90:93]
	v_mfma_f32_16x16x32_bf16 v[82:85], v[176:179], v[216:219], v[82:85]
	v_mfma_f32_16x16x32_bf16 v[74:77], v[188:191], v[216:219], v[74:77]
	v_mfma_f32_16x16x32_bf16 v[70:73], v[176:179], v[224:227], v[70:73]
	v_mfma_f32_16x16x32_bf16 v[66:69], v[188:191], v[224:227], v[66:69]
	s_setprio 0
	s_barrier
; #define PG8_STAGE(bufoff, gbase, voff) do { _Pragma("unroll") for (int _i = 0; _i < 2; ++_i) \
;         __builtin_amdgcn_global_load_lds((const unsigned*)((const char*)(gbase) + (voff)[_i]), (PG8_LAS unsigned*)(lds + (bufoff) + ldsw + _i * 8192), 16, 0, 0); } while (0)
; #define PG8_LDA(dst, b, h) do { _Pragma("unroll") for (int m = 0; m < 4; ++m) _Pragma("unroll") for (int k = 0; k < 2; ++k) dst[m][k] = *(const PG8_LAS bf16x8*)(lds + PG8_SA(b, h) + aoff + m * 2048 + k * 1024); } while (0)
; #define PG8_LDB(dst, b, h) do { _Pragma("unroll") for (int n = 0; n < 2; ++n) _Pragma("unroll") for (int k = 0; k < 2; ++k) dst[n][k] = *(const PG8_LAS bf16x8*)(lds + PG8_SB(b, h) + boff + n * 2048 + k * 1024); } while (0)
; #define PG8_WAIT_V(n) asm volatile("s_waitcnt vmcnt(" #n ")" ::: "memory")
; #define PG8_WAIT_L(n) asm volatile("s_waitcnt lgkmcnt(" #n ")" ::: "memory")
; #define PG8_BAR __builtin_amdgcn_s_barrier()
; #define PG8_SCHED __builtin_amdgcn_sched_barrier(0)
; template <class Epi, class Sched, bool ALIGN_EPI = false, bool SP2 = false>
; __device__ __forceinline__ void gemm_phase(PG8_LAS unsigned char* lds, const Gemm g, const Sched& S, const Epi& E) {
;     ...
;         for (int t = 0; t < nt; t += 2) {
;     ...
;             PG8_LDB(B0, 1, 0); PG8_LDB(B1, 1, 1); PG8_SCHED; PG8_LDA(At, 1, 0); PG8_STAGE(PG8_SA(0, 1), a2 + hstep, voffA);
;             PG8_WAIT_V(8); PG8_WAIT_L(0); PG8_BAR; PG8_MMA(0, 0, At, B0); PG8_MMA(0, 1, At, B1); PG8_BAR; PG8_SCHED;
;             PG8_LDA(At, 1, 1); PG8_STAGE(PG8_SB(1, 0), b3, voffB); PG8_STAGE(PG8_SB(1, 1), b3 + hstep, voffB); PG8_STAGE(PG8_SA(1, 0), a3, voffA);
;             PG8_WAIT_V(8); PG8_WAIT_L(0); PG8_BAR; PG8_MMA(1, 0, At, B0); PG8_MMA(1, 1, At, B1); PG8_BAR; PG8_SCHED;
	s_add_u32 s98, s34, 0x80
	s_addc_u32 s99, s35, 0
	s_add_u32 s100, s36, 0xfff80080
	s_addc_u32 s101, s37, -1
	s_add_i32 s36, s59, s39
	s_mov_b32 m0, s36
	ds_read_b128 v[192:195], v158 offset:49152
	ds_read_b128 v[196:199], v158 offset:50176
	ds_read_b128 v[200:203], v158 offset:51200
	ds_read_b128 v[204:207], v158 offset:52224
	ds_read_b128 v[212:215], v158 offset:53248
	ds_read_b128 v[216:219], v158 offset:54272
	ds_read_b128 v[220:223], v158 offset:55296
	ds_read_b128 v[224:227], v158 offset:56320
	global_load_lds_dwordx4 v134, s[98:99]
	s_add_i32 m0, s36, 0x2000
	s_add_u32 s34, s34, 0x80080
	s_addc_u32 s35, s35, 0
	s_add_i32 s36, s60, s39
	global_load_lds_dwordx4 v130, s[98:99]
	s_mov_b32 m0, s36
	s_nop 0
	global_load_lds_dwordx4 v134, s[34:35]
	s_add_i32 m0, s36, 0x2000
	s_nop 0
	global_load_lds_dwordx4 v130, s[34:35]
	s_mov_b32 m0, s48
	s_nop 0
	global_load_lds_dwordx4 v136, s[100:101]
	s_mov_b32 m0, s49
	s_nop 0
	global_load_lds_dwordx4 v132, s[100:101]
	s_waitcnt vmcnt(8)
	s_waitcnt lgkmcnt(0)
	s_barrier
	s_setprio 1
	s_waitcnt lgkmcnt(0)
	v_mfma_f32_16x16x32_bf16 v[62:65], v[148:151], v[192:195], v[62:65]
	v_mfma_f32_16x16x32_bf16 v[58:61], v[164:167], v[192:195], v[58:61]
	v_mfma_f32_16x16x32_bf16 v[54:57], v[148:151], v[200:203], v[54:57]
	v_mfma_f32_16x16x32_bf16 v[46:49], v[164:167], v[200:203], v[46:49]
	v_mfma_f32_16x16x32_bf16 v[38:41], v[148:151], v[212:215], v[38:41]
	v_mfma_f32_16x16x32_bf16 v[30:33], v[164:167], v[212:215], v[30:33]
	v_mfma_f32_16x16x32_bf16 v[22:25], v[148:151], v[220:223], v[22:25]
	v_mfma_f32_16x16x32_bf16 v[14:17], v[164:167], v[220:223], v[14:17]
	v_mfma_f32_16x16x32_bf16 v[62:65], v[160:163], v[196:199], v[62:65]
	v_mfma_f32_16x16x32_bf16 v[58:61], v[168:171], v[196:199], v[58:61]
	v_mfma_f32_16x16x32_bf16 v[54:57], v[160:163], v[204:207], v[54:57]
	v_mfma_f32_16x16x32_bf16 v[46:49], v[168:171], v[204:207], v[46:49]
	v_mfma_f32_16x16x32_bf16 v[38:41], v[160:163], v[216:219], v[38:41]
	v_mfma_f32_16x16x32_bf16 v[30:33], v[168:171], v[216:219], v[30:33]
	v_mfma_f32_16x16x32_bf16 v[22:25], v[160:163], v[224:227], v[22:25]
	v_mfma_f32_16x16x32_bf16 v[14:17], v[168:171], v[224:227], v[14:17]
	s_setprio 0
	s_setprio 1
	v_mfma_f32_16x16x32_bf16 v[50:53], v[172:175], v[192:195], v[50:53]
	v_mfma_f32_16x16x32_bf16 v[42:45], v[180:183], v[192:195], v[42:45]
	v_mfma_f32_16x16x32_bf16 v[34:37], v[172:175], v[200:203], v[34:37]
	v_mfma_f32_16x16x32_bf16 v[26:29], v[180:183], v[200:203], v[26:29]
	v_mfma_f32_16x16x32_bf16 v[18:21], v[172:175], v[212:215], v[18:21]
	v_mfma_f32_16x16x32_bf16 v[10:13], v[180:183], v[212:215], v[10:13]
	v_mfma_f32_16x16x32_bf16 v[6:9], v[172:175], v[220:223], v[6:9]
	v_mfma_f32_16x16x32_bf16 v[2:5], v[180:183], v[220:223], v[2:5]
	v_mfma_f32_16x16x32_bf16 v[50:53], v[176:179], v[196:199], v[50:53]
	v_mfma_f32_16x16x32_bf16 v[42:45], v[188:191], v[196:199], v[42:45]
	v_mfma_f32_16x16x32_bf16 v[34:37], v[176:179], v[204:207], v[34:37]
	v_mfma_f32_16x16x32_bf16 v[26:29], v[188:191], v[204:207], v[26:29]
	v_mfma_f32_16x16x32_bf16 v[18:21], v[176:179], v[216:219], v[18:21]
	v_mfma_f32_16x16x32_bf16 v[10:13], v[188:191], v[216:219], v[10:13]
	v_mfma_f32_16x16x32_bf16 v[6:9], v[176:179], v[224:227], v[6:9]
	v_mfma_f32_16x16x32_bf16 v[2:5], v[188:191], v[224:227], v[2:5]
	s_setprio 0
	s_barrier
	s_add_i32 s58, s58, 2
	s_add_u32 s30, s30, 0x100
	s_addc_u32 s31, s31, 0
	s_add_u32 s56, s56, 0x100
	s_addc_u32 s57, s57, 0
	s_cmp_gt_u32 s58, 29

; #define PG8_STAGE(bufoff, gbase, voff) do { _Pragma("unroll") for (int _i = 0; _i < 2; ++_i) \
;         __builtin_amdgcn_global_load_lds((const unsigned*)((const char*)(gbase) + (voff)[_i]), (PG8_LAS unsigned*)(lds + (bufoff) + ldsw + _i * 8192), 16, 0, 0); } while (0)
; #define PG8_LDA(dst, b, h) do { _Pragma("unroll") for (int m = 0; m < 4; ++m) _Pragma("unroll") for (int k = 0; k < 2; ++k) dst[m][k] = *(const PG8_LAS bf16x8*)(lds + PG8_SA(b, h) + aoff + m * 2048 + k * 1024); } while (0)
; template <class Epi, class Sched, bool ALIGN_EPI = false, bool SP2 = false>
; __device__ __forceinline__ void gemm_phase(PG8_LAS unsigned char* lds, const Gemm g, const Sched& S, const Epi& E) {
;     ...
;         const bool has_next = S.next(ui + 1, nxt);
;         const char* nA = has_next ? (const char*)g.A + (size_t)nxt.pm * tstep : cA; const char* nB = has_next ? (const char*)g.Bt + (size_t)nxt.pn * tstep : cB;
;         for (int t = 0; t < nt; t += 2) {
;             const bool last = (t == nt - 2);
;             const char* a1 = cA + (size_t)(t + 1) * kstep;
;             const char* a2 = last ? nA : cA + (size_t)(t + 2) * kstep; const char* b2 = last ? nB : cB + (size_t)(t + 2) * kstep;
;             const char* a3 = a2 + kstep; const char* b3 = b2 + kstep;
;             if (last && has_next) S.a_ready(nxt);
;             if constexpr (SP2) {
;             PG8_LDB(B0, 0, 0); PG8_LDB(B1, 0, 1); PG8_SCHED; PG8_LDA(At, 0, 0); PG8_STAGE(PG8_SA(1, 1), a1 + hstep, voffA);
;             PG8_WAIT_V(8); PG8_WAIT_L(0); PG8_BAR; PG8_MMA(0, 0, At, B0); PG8_MMA(0, 1, At, B1); PG8_BAR; PG8_SCHED;
;             PG8_LDA(At, 0, 1); PG8_STAGE(PG8_SB(0, 0), b2, voffB); PG8_STAGE(PG8_SB(0, 1), b2 + hstep, voffB); PG8_STAGE(PG8_SA(0, 0), a2, voffA);
;             PG8_WAIT_V(8); PG8_WAIT_L(0); PG8_BAR; PG8_MMA(1, 0, At, B0); PG8_MMA(1, 1, At, B1); PG8_BAR; PG8_SCHED;
;             PG8_LDB(B0, 1, 0); PG8_LDB(B1, 1, 1); PG8_SCHED; PG8_LDA(At, 1, 0); PG8_STAGE(PG8_SA(0, 1), a2 + hstep, voffA);
;             PG8_WAIT_V(8); PG8_WAIT_L(0); PG8_BAR; PG8_MMA(0, 0, At, B0); PG8_MMA(0, 1, At, B1); PG8_BAR; PG8_SCHED;
;             PG8_LDA(At, 1, 1); PG8_STAGE(PG8_SB(1, 0), b3, voffB); PG8_STAGE(PG8_SB(1, 1), b3 + hstep, voffB); PG8_STAGE(PG8_SA(1, 0), a3, voffA);
;             PG8_WAIT_V(8); PG8_WAIT_L(0); PG8_BAR; PG8_MMA(1, 0, At, B0); PG8_MMA(1, 1, At, B1); PG8_BAR; PG8_SCHED;
.LBB0_746:
	s_ashr_i32 s21, s20, 31
	s_lshl_b64 s[22:23], s[20:21], 20
	v_readlane_b32 s24, v247, 17
	v_readlane_b32 s25, v247, 18
	s_add_u32 s22, s24, s22
	s_addc_u32 s23, s25, s23
	s_and_b64 s[24:25], s[2:3], exec
	s_cselect_b32 s21, s23, s29
	s_cselect_b32 s58, s22, s28
	s_ashr_i32 s19, s18, 31
	s_lshl_b64 s[24:25], s[18:19], 20
	s_add_u32 s24, s36, s24
	s_addc_u32 s25, s37, s25
	s_and_b64 s[34:35], s[2:3], exec
	s_cselect_b32 s19, s25, s31
	s_cselect_b32 s59, s24, s30
	s_add_u32 s28, s28, 0x80080
	s_addc_u32 s29, s29, 0
	s_add_u32 s60, s30, 0x100
	s_addc_u32 s61, s31, 0
	s_mov_b32 s62, -2
	v_add_u32_e32 v248, 0x18000, v216
	v_add_u32_e32 v249, 0x1c000, v216
	ds_read_b128 v[130:133], v218
	ds_read_b128 v[134:137], v218 offset:1024
	ds_read_b128 v[138:141], v218 offset:2048
	ds_read_b128 v[142:145], v218 offset:3072
	ds_read_b128 v[146:149], v219
	ds_read_b128 v[150:153], v219 offset:1024
	ds_read_b128 v[154:157], v219 offset:2048
	ds_read_b128 v[158:161], v219 offset:3072
	s_add_u32 s30, s28, 0xfff80080
	s_addc_u32 s31, s29, -1
	s_cmp_eq_u32 s62, 28
	s_cselect_b32 s35, s21, s31
	s_cselect_b32 s34, s58, s30
	s_cselect_b32 s31, s19, s61
	s_cselect_b32 s30, s59, s60
	s_add_i32 m0, s27, 0xc000
	ds_read_b128 v[162:165], v220
	ds_read_b128 v[166:169], v220 offset:1024
	ds_read_b128 v[170:173], v220 offset:2048
	ds_read_b128 v[174:177], v220 offset:3072
	ds_read_b128 v[178:181], v220 offset:4096
	ds_read_b128 v[182:185], v220 offset:5120
	ds_read_b128 v[206:209], v220 offset:6144
	ds_read_b128 v[222:225], v220 offset:7168
	global_load_lds_dwordx4 v198, s[28:29]
	s_add_i32 m0, s27, 0xe000
	s_nop 0
	global_load_lds_dwordx4 v200, s[28:29]
	s_waitcnt vmcnt(8)
	s_waitcnt lgkmcnt(0)
	s_barrier
	s_setprio 1
	s_waitcnt lgkmcnt(0)
	v_mfma_f32_16x16x32_bf16 v[126:129], v[130:133], v[162:165], 0
	v_mfma_f32_16x16x32_bf16 v[122:125], v[138:141], v[162:165], 0
	v_mfma_f32_16x16x32_bf16 v[118:121], v[130:133], v[170:173], 0
	v_mfma_f32_16x16x32_bf16 v[110:113], v[138:141], v[170:173], 0
	v_mfma_f32_16x16x32_bf16 v[94:97], v[130:133], v[178:181], 0
	v_mfma_f32_16x16x32_bf16 v[90:93], v[138:141], v[178:181], 0
	v_mfma_f32_16x16x32_bf16 v[82:85], v[130:133], v[206:209], 0
	v_mfma_f32_16x16x32_bf16 v[74:77], v[138:141], v[206:209], 0
	v_mfma_f32_16x16x32_bf16 v[126:129], v[134:137], v[166:169], v[126:129]
	v_mfma_f32_16x16x32_bf16 v[122:125], v[142:145], v[166:169], v[122:125]
	v_mfma_f32_16x16x32_bf16 v[118:121], v[134:137], v[174:177], v[118:121]
	v_mfma_f32_16x16x32_bf16 v[110:113], v[142:145], v[174:177], v[110:113]
	v_mfma_f32_16x16x32_bf16 v[94:97], v[134:137], v[182:185], v[94:97]
	v_mfma_f32_16x16x32_bf16 v[90:93], v[142:145], v[182:185], v[90:93]
	v_mfma_f32_16x16x32_bf16 v[82:85], v[134:137], v[222:225], v[82:85]
	v_mfma_f32_16x16x32_bf16 v[74:77], v[142:145], v[222:225], v[74:77]
	s_setprio 0
	s_setprio 1
	v_mfma_f32_16x16x32_bf16 v[114:117], v[146:149], v[162:165], 0
	v_mfma_f32_16x16x32_bf16 v[106:109], v[154:157], v[162:165], 0
	v_mfma_f32_16x16x32_bf16 v[102:105], v[146:149], v[170:173], 0
	v_mfma_f32_16x16x32_bf16 v[98:101], v[154:157], v[170:173], 0
	v_mfma_f32_16x16x32_bf16 v[86:89], v[146:149], v[178:181], 0
	v_mfma_f32_16x16x32_bf16 v[78:81], v[154:157], v[178:181], 0
	v_mfma_f32_16x16x32_bf16 v[70:73], v[146:149], v[206:209], 0
	v_mfma_f32_16x16x32_bf16 v[66:69], v[154:157], v[206:209], 0
	v_mfma_f32_16x16x32_bf16 v[114:117], v[150:153], v[166:169], v[114:117]
	v_mfma_f32_16x16x32_bf16 v[106:109], v[158:161], v[166:169], v[106:109]
	v_mfma_f32_16x16x32_bf16 v[102:105], v[150:153], v[174:177], v[102:105]
	v_mfma_f32_16x16x32_bf16 v[98:101], v[158:161], v[174:177], v[98:101]
	v_mfma_f32_16x16x32_bf16 v[86:89], v[150:153], v[182:185], v[86:89]
	v_mfma_f32_16x16x32_bf16 v[78:81], v[158:161], v[182:185], v[78:81]
	v_mfma_f32_16x16x32_bf16 v[70:73], v[150:153], v[222:225], v[70:73]
	v_mfma_f32_16x16x32_bf16 v[66:69], v[158:161], v[222:225], v[66:69]
	s_setprio 0
	s_barrier
	s_add_i32 s63, s48, s38
	s_mov_b32 m0, s63
	ds_read_b128 v[162:165], v220 offset:16384
	ds_read_b128 v[166:169], v220 offset:17408
	ds_read_b128 v[170:173], v220 offset:18432
	ds_read_b128 v[174:177], v220 offset:19456
	ds_read_b128 v[178:181], v220 offset:20480
	ds_read_b128 v[182:185], v220 offset:21504
	ds_read_b128 v[206:209], v220 offset:22528
	ds_read_b128 v[222:225], v220 offset:23552
	global_load_lds_dwordx4 v192, s[30:31]
	s_add_i32 m0, s63, 0x2000
	s_add_u32 s64, s30, 0x80000
	s_addc_u32 s65, s31, 0
	s_add_i32 s63, s49, s38
	global_load_lds_dwordx4 v196, s[30:31]
	s_mov_b32 m0, s63
	s_nop 0
	global_load_lds_dwordx4 v192, s[64:65]
	s_add_i32 m0, s63, 0x2000
	s_nop 0
	global_load_lds_dwordx4 v196, s[64:65]
	s_mov_b32 m0, s27
	s_nop 0
	global_load_lds_dwordx4 v190, s[34:35]
	s_mov_b32 m0, s39
	s_nop 0
	global_load_lds_dwordx4 v194, s[34:35]
	s_waitcnt vmcnt(8)
	s_waitcnt lgkmcnt(0)
	s_barrier
; #define PG8_STAGE(bufoff, gbase, voff) do { _Pragma("unroll") for (int _i = 0; _i < 2; ++_i) \
;         __builtin_amdgcn_global_load_lds((const unsigned*)((const char*)(gbase) + (voff)[_i]), (PG8_LAS unsigned*)(lds + (bufoff) + ldsw + _i * 8192), 16, 0, 0); } while (0)
; #define PG8_LDA(dst, b, h) do { _Pragma("unroll") for (int m = 0; m < 4; ++m) _Pragma("unroll") for (int k = 0; k < 2; ++k) dst[m][k] = *(const PG8_LAS bf16x8*)(lds + PG8_SA(b, h) + aoff + m * 2048 + k * 1024); } while (0)
; #define PG8_LDB(dst, b, h) do { _Pragma("unroll") for (int n = 0; n < 2; ++n) _Pragma("unroll") for (int k = 0; k < 2; ++k) dst[n][k] = *(const PG8_LAS bf16x8*)(lds + PG8_SB(b, h) + boff + n * 2048 + k * 1024); } while (0)
; #define PG8_WAIT_V(n) asm volatile("s_waitcnt vmcnt(" #n ")" ::: "memory")
; #define PG8_WAIT_L(n) asm volatile("s_waitcnt lgkmcnt(" #n ")" ::: "memory")
; #define PG8_BAR __builtin_amdgcn_s_barrier()
; #define PG8_SCHED __builtin_amdgcn_sched_barrier(0)
; template <class Epi, class Sched, bool ALIGN_EPI = false, bool SP2 = false>
; __device__ __forceinline__ void gemm_phase(PG8_LAS unsigned char* lds, const Gemm g, const Sched& S, const Epi& E) {
;     ...
;             PG8_WAIT_V(8); PG8_WAIT_L(0); PG8_BAR; PG8_MMA(1, 0, At, B0); PG8_MMA(1, 1, At, B1); PG8_BAR; PG8_SCHED;
;             PG8_LDB(B0, 1, 0); PG8_LDB(B1, 1, 1); PG8_SCHED; PG8_LDA(At, 1, 0); PG8_STAGE(PG8_SA(0, 1), a2 + hstep, voffA);
;             PG8_WAIT_V(8); PG8_WAIT_L(0); PG8_BAR; PG8_MMA(0, 0, At, B0); PG8_MMA(0, 1, At, B1); PG8_BAR; PG8_SCHED;
	s_setprio 1
	s_waitcnt lgkmcnt(0)
	v_mfma_f32_16x16x32_bf16 v[62:65], v[130:133], v[162:165], 0
	v_mfma_f32_16x16x32_bf16 v[58:61], v[138:141], v[162:165], 0
	v_mfma_f32_16x16x32_bf16 v[50:53], v[130:133], v[170:173], 0
	v_mfma_f32_16x16x32_bf16 v[42:45], v[138:141], v[170:173], 0
	v_mfma_f32_16x16x32_bf16 v[34:37], v[130:133], v[178:181], 0
	v_mfma_f32_16x16x32_bf16 v[26:29], v[138:141], v[178:181], 0
	v_mfma_f32_16x16x32_bf16 v[18:21], v[130:133], v[206:209], 0
	v_mfma_f32_16x16x32_bf16 v[10:13], v[138:141], v[206:209], 0
	v_mfma_f32_16x16x32_bf16 v[62:65], v[134:137], v[166:169], v[62:65]
	v_mfma_f32_16x16x32_bf16 v[58:61], v[142:145], v[166:169], v[58:61]
	v_mfma_f32_16x16x32_bf16 v[50:53], v[134:137], v[174:177], v[50:53]
	v_mfma_f32_16x16x32_bf16 v[42:45], v[142:145], v[174:177], v[42:45]
	v_mfma_f32_16x16x32_bf16 v[34:37], v[134:137], v[182:185], v[34:37]
	v_mfma_f32_16x16x32_bf16 v[26:29], v[142:145], v[182:185], v[26:29]
	v_mfma_f32_16x16x32_bf16 v[18:21], v[134:137], v[222:225], v[18:21]
	v_mfma_f32_16x16x32_bf16 v[10:13], v[142:145], v[222:225], v[10:13]
	s_setprio 0
	s_setprio 1
	v_mfma_f32_16x16x32_bf16 v[54:57], v[146:149], v[162:165], 0
	v_mfma_f32_16x16x32_bf16 v[46:49], v[154:157], v[162:165], 0
	v_mfma_f32_16x16x32_bf16 v[38:41], v[146:149], v[170:173], 0
	v_mfma_f32_16x16x32_bf16 v[30:33], v[154:157], v[170:173], 0
	v_mfma_f32_16x16x32_bf16 v[22:25], v[146:149], v[178:181], 0
	v_mfma_f32_16x16x32_bf16 v[14:17], v[154:157], v[178:181], 0
	v_mfma_f32_16x16x32_bf16 v[6:9], v[146:149], v[206:209], 0
	v_mfma_f32_16x16x32_bf16 v[2:5], v[154:157], v[206:209], 0
	v_mfma_f32_16x16x32_bf16 v[54:57], v[150:153], v[166:169], v[54:57]
	v_mfma_f32_16x16x32_bf16 v[46:49], v[158:161], v[166:169], v[46:49]
	v_mfma_f32_16x16x32_bf16 v[38:41], v[150:153], v[174:177], v[38:41]
	v_mfma_f32_16x16x32_bf16 v[30:33], v[158:161], v[174:177], v[30:33]
	v_mfma_f32_16x16x32_bf16 v[22:25], v[150:153], v[182:185], v[22:25]
	v_mfma_f32_16x16x32_bf16 v[14:17], v[158:161], v[182:185], v[14:17]
	v_mfma_f32_16x16x32_bf16 v[6:9], v[150:153], v[222:225], v[6:9]
	v_mfma_f32_16x16x32_bf16 v[2:5], v[158:161], v[222:225], v[2:5]
	s_setprio 0
	s_barrier
	s_add_i32 s63, 0, 0x18000
	s_add_i32 s64, 0, 0x1c000
	ds_read_b128 v[130:133], v248
	ds_read_b128 v[134:137], v248 offset:1024
	ds_read_b128 v[138:141], v248 offset:2048
	ds_read_b128 v[142:145], v248 offset:3072
	ds_read_b128 v[146:149], v249
	ds_read_b128 v[150:153], v249 offset:1024
	ds_read_b128 v[154:157], v249 offset:2048
	ds_read_b128 v[158:161], v249 offset:3072
	s_add_u32 s34, s34, 0x80000
	s_addc_u32 s35, s35, 0
	s_mov_b32 m0, s40
	ds_read_b128 v[162:165], v220 offset:32768
	ds_read_b128 v[166:169], v220 offset:33792
	ds_read_b128 v[170:173], v220 offset:34816
	ds_read_b128 v[174:177], v220 offset:35840
	ds_read_b128 v[178:181], v220 offset:36864
	ds_read_b128 v[182:185], v220 offset:37888
	ds_read_b128 v[206:209], v220 offset:38912
	ds_read_b128 v[222:225], v220 offset:39936
	global_load_lds_dwordx4 v190, s[34:35]
	s_mov_b32 m0, s41
	s_nop 0
	global_load_lds_dwordx4 v194, s[34:35]
	s_waitcnt vmcnt(8)
	s_waitcnt lgkmcnt(0)
	s_barrier
	s_setprio 1
	s_waitcnt lgkmcnt(0)
	v_mfma_f32_16x16x32_bf16 v[126:129], v[130:133], v[162:165], v[126:129]
	v_mfma_f32_16x16x32_bf16 v[122:125], v[138:141], v[162:165], v[122:125]
	v_mfma_f32_16x16x32_bf16 v[118:121], v[130:133], v[170:173], v[118:121]
	v_mfma_f32_16x16x32_bf16 v[110:113], v[138:141], v[170:173], v[110:113]
	v_mfma_f32_16x16x32_bf16 v[94:97], v[130:133], v[178:181], v[94:97]
	v_mfma_f32_16x16x32_bf16 v[90:93], v[138:141], v[178:181], v[90:93]
	v_mfma_f32_16x16x32_bf16 v[82:85], v[130:133], v[206:209], v[82:85]
	v_mfma_f32_16x16x32_bf16 v[74:77], v[138:141], v[206:209], v[74:77]
	v_mfma_f32_16x16x32_bf16 v[126:129], v[134:137], v[166:169], v[126:129]
	v_mfma_f32_16x16x32_bf16 v[122:125], v[142:145], v[166:169], v[122:125]
	v_mfma_f32_16x16x32_bf16 v[118:121], v[134:137], v[174:177], v[118:121]
	v_mfma_f32_16x16x32_bf16 v[110:113], v[142:145], v[174:177], v[110:113]
	v_mfma_f32_16x16x32_bf16 v[94:97], v[134:137], v[182:185], v[94:97]
	v_mfma_f32_16x16x32_bf16 v[90:93], v[142:145], v[182:185], v[90:93]
	v_mfma_f32_16x16x32_bf16 v[82:85], v[134:137], v[222:225], v[82:85]
	v_mfma_f32_16x16x32_bf16 v[74:77], v[142:145], v[222:225], v[74:77]
	s_setprio 0
	s_setprio 1
	v_mfma_f32_16x16x32_bf16 v[114:117], v[146:149], v[162:165], v[114:117]
	v_mfma_f32_16x16x32_bf16 v[106:109], v[154:157], v[162:165], v[106:109]
	v_mfma_f32_16x16x32_bf16 v[102:105], v[146:149], v[170:173], v[102:105]
	v_mfma_f32_16x16x32_bf16 v[98:101], v[154:157], v[170:173], v[98:101]
	v_mfma_f32_16x16x32_bf16 v[86:89], v[146:149], v[178:181], v[86:89]
	v_mfma_f32_16x16x32_bf16 v[78:81], v[154:157], v[178:181], v[78:81]
	v_mfma_f32_16x16x32_bf16 v[70:73], v[146:149], v[206:209], v[70:73]
	v_mfma_f32_16x16x32_bf16 v[66:69], v[154:157], v[206:209], v[66:69]
	v_mfma_f32_16x16x32_bf16 v[114:117], v[150:153], v[166:169], v[114:117]
	v_mfma_f32_16x16x32_bf16 v[106:109], v[158:161], v[166:169], v[106:109]
	v_mfma_f32_16x16x32_bf16 v[102:105], v[150:153], v[174:177], v[102:105]
	v_mfma_f32_16x16x32_bf16 v[98:101], v[158:161], v[174:177], v[98:101]
	v_mfma_f32_16x16x32_bf16 v[86:89], v[150:153], v[182:185], v[86:89]
	v_mfma_f32_16x16x32_bf16 v[78:81], v[158:161], v[182:185], v[78:81]
	v_mfma_f32_16x16x32_bf16 v[70:73], v[150:153], v[222:225], v[70:73]
	v_mfma_f32_16x16x32_bf16 v[66:69], v[158:161], v[222:225], v[66:69]
	s_setprio 0
	s_barrier
; #define PG8_STAGE(bufoff, gbase, voff) do { _Pragma("unroll") for (int _i = 0; _i < 2; ++_i) \
;         __builtin_amdgcn_global_load_lds((const unsigned*)((const char*)(gbase) + (voff)[_i]), (PG8_LAS unsigned*)(lds + (bufoff) + ldsw + _i * 8192), 16, 0, 0); } while (0)
; #define PG8_LDA(dst, b, h) do { _Pragma("unroll") for (int m = 0; m < 4; ++m) _Pragma("unroll") for (int k = 0; k < 2; ++k) dst[m][k] = *(const PG8_LAS bf16x8*)(lds + PG8_SA(b, h) + aoff + m * 2048 + k * 1024); } while (0)
; #define PG8_LDB(dst, b, h) do { _Pragma("unroll") for (int n = 0; n < 2; ++n) _Pragma("unroll") for (int k = 0; k < 2; ++k) dst[n][k] = *(const PG8_LAS bf16x8*)(lds + PG8_SB(b, h) + boff + n * 2048 + k * 1024); } while (0)
; #define PG8_WAIT_V(n) asm volatile("s_waitcnt vmcnt(" #n ")" ::: "memory")
; #define PG8_WAIT_L(n) asm volatile("s_waitcnt lgkmcnt(" #n ")" ::: "memory")
; #define PG8_BAR __builtin_amdgcn_s_barrier()
; #define PG8_SCHED __builtin_amdgcn_sched_barrier(0)
; template <class Epi, class Sched, bool ALIGN_EPI = false, bool SP2 = false>
; __device__ __forceinline__ void gemm_phase(PG8_LAS unsigned char* lds, const Gemm g, const Sched& S, const Epi& E) {
;     ...
;         for (int t = 0; t < nt; t += 2) {
;     ...
;             PG8_LDB(B0, 1, 0); PG8_LDB(B1, 1, 1); PG8_SCHED; PG8_LDA(At, 1, 0); PG8_STAGE(PG8_SA(0, 1), a2 + hstep, voffA);
;             PG8_WAIT_V(8); PG8_WAIT_L(0); PG8_BAR; PG8_MMA(0, 0, At, B0); PG8_MMA(0, 1, At, B1); PG8_BAR; PG8_SCHED;
;             PG8_LDA(At, 1, 1); PG8_STAGE(PG8_SB(1, 0), b3, voffB); PG8_STAGE(PG8_SB(1, 1), b3 + hstep, voffB); PG8_STAGE(PG8_SA(1, 0), a3, voffA);
;             PG8_WAIT_V(8); PG8_WAIT_L(0); PG8_BAR; PG8_MMA(1, 0, At, B0); PG8_MMA(1, 1, At, B1); PG8_BAR; PG8_SCHED;
	s_add_u32 s98, s30, 0x80
	s_addc_u32 s99, s31, 0
	s_add_u32 s100, s34, 0xfff80080
	s_addc_u32 s101, s35, -1
	s_add_i32 s34, s63, s38
	s_mov_b32 m0, s34
	ds_read_b128 v[162:165], v220 offset:49152
	ds_read_b128 v[166:169], v220 offset:50176
	ds_read_b128 v[170:173], v220 offset:51200
	ds_read_b128 v[174:177], v220 offset:52224
	ds_read_b128 v[178:181], v220 offset:53248
	ds_read_b128 v[182:185], v220 offset:54272
	ds_read_b128 v[206:209], v220 offset:55296
	ds_read_b128 v[222:225], v220 offset:56320
	global_load_lds_dwordx4 v192, s[98:99]
	s_add_i32 m0, s34, 0x2000
	s_add_u32 s30, s30, 0x80080
	s_addc_u32 s31, s31, 0
	s_add_i32 s34, s64, s38
	global_load_lds_dwordx4 v196, s[98:99]
	s_mov_b32 m0, s34
	s_nop 0
	global_load_lds_dwordx4 v192, s[30:31]
	s_add_i32 m0, s34, 0x2000
	s_nop 0
	global_load_lds_dwordx4 v196, s[30:31]
	s_mov_b32 m0, s45
	s_nop 0
	global_load_lds_dwordx4 v190, s[100:101]
	s_mov_b32 m0, s46
	s_nop 0
	global_load_lds_dwordx4 v194, s[100:101]
	s_waitcnt vmcnt(8)
	s_waitcnt lgkmcnt(0)
	s_barrier
	s_setprio 1
	s_waitcnt lgkmcnt(0)
	v_mfma_f32_16x16x32_bf16 v[62:65], v[130:133], v[162:165], v[62:65]
	v_mfma_f32_16x16x32_bf16 v[58:61], v[138:141], v[162:165], v[58:61]
	v_mfma_f32_16x16x32_bf16 v[50:53], v[130:133], v[170:173], v[50:53]
	v_mfma_f32_16x16x32_bf16 v[42:45], v[138:141], v[170:173], v[42:45]
	v_mfma_f32_16x16x32_bf16 v[34:37], v[130:133], v[178:181], v[34:37]
	v_mfma_f32_16x16x32_bf16 v[26:29], v[138:141], v[178:181], v[26:29]
	v_mfma_f32_16x16x32_bf16 v[18:21], v[130:133], v[206:209], v[18:21]
	v_mfma_f32_16x16x32_bf16 v[10:13], v[138:141], v[206:209], v[10:13]
	v_mfma_f32_16x16x32_bf16 v[62:65], v[134:137], v[166:169], v[62:65]
	v_mfma_f32_16x16x32_bf16 v[58:61], v[142:145], v[166:169], v[58:61]
	v_mfma_f32_16x16x32_bf16 v[50:53], v[134:137], v[174:177], v[50:53]
	v_mfma_f32_16x16x32_bf16 v[42:45], v[142:145], v[174:177], v[42:45]
	v_mfma_f32_16x16x32_bf16 v[34:37], v[134:137], v[182:185], v[34:37]
	v_mfma_f32_16x16x32_bf16 v[26:29], v[142:145], v[182:185], v[26:29]
	v_mfma_f32_16x16x32_bf16 v[18:21], v[134:137], v[222:225], v[18:21]
	v_mfma_f32_16x16x32_bf16 v[10:13], v[142:145], v[222:225], v[10:13]
	s_setprio 0
	s_setprio 1
	v_mfma_f32_16x16x32_bf16 v[54:57], v[146:149], v[162:165], v[54:57]
	v_mfma_f32_16x16x32_bf16 v[46:49], v[154:157], v[162:165], v[46:49]
	v_mfma_f32_16x16x32_bf16 v[38:41], v[146:149], v[170:173], v[38:41]
	v_mfma_f32_16x16x32_bf16 v[30:33], v[154:157], v[170:173], v[30:33]
	v_mfma_f32_16x16x32_bf16 v[22:25], v[146:149], v[178:181], v[22:25]
	v_mfma_f32_16x16x32_bf16 v[14:17], v[154:157], v[178:181], v[14:17]
	v_mfma_f32_16x16x32_bf16 v[6:9], v[146:149], v[206:209], v[6:9]
	v_mfma_f32_16x16x32_bf16 v[2:5], v[154:157], v[206:209], v[2:5]
	v_mfma_f32_16x16x32_bf16 v[54:57], v[150:153], v[166:169], v[54:57]
	v_mfma_f32_16x16x32_bf16 v[46:49], v[158:161], v[166:169], v[46:49]
	v_mfma_f32_16x16x32_bf16 v[38:41], v[150:153], v[174:177], v[38:41]
	v_mfma_f32_16x16x32_bf16 v[30:33], v[158:161], v[174:177], v[30:33]
	v_mfma_f32_16x16x32_bf16 v[22:25], v[150:153], v[182:185], v[22:25]
	v_mfma_f32_16x16x32_bf16 v[14:17], v[158:161], v[182:185], v[14:17]
	v_mfma_f32_16x16x32_bf16 v[6:9], v[150:153], v[222:225], v[6:9]
	v_mfma_f32_16x16x32_bf16 v[2:5], v[158:161], v[222:225], v[2:5]
	s_setprio 0
	s_barrier
	s_add_i32 s62, s62, 2
	s_add_u32 s28, s28, 0x100
	s_addc_u32 s29, s29, 0
	s_add_u32 s60, s60, 0x100
	s_addc_u32 s61, s61, 0
	s_cmp_gt_u32 s62, 29

; #define PG8_STAGE(bufoff, gbase, voff) do { _Pragma("unroll") for (int _i = 0; _i < 2; ++_i) \
;         __builtin_amdgcn_global_load_lds((const unsigned*)((const char*)(gbase) + (voff)[_i]), (PG8_LAS unsigned*)(lds + (bufoff) + ldsw + _i * 8192), 16, 0, 0); } while (0)
; #define PG8_LDA(dst, b, h) do { _Pragma("unroll") for (int m = 0; m < 4; ++m) _Pragma("unroll") for (int k = 0; k < 2; ++k) dst[m][k] = *(const PG8_LAS bf16x8*)(lds + PG8_SA(b, h) + aoff + m * 2048 + k * 1024); } while (0)
; template <class Epi, class Sched, bool ALIGN_EPI = false, bool SP2 = false>
; __device__ __forceinline__ void gemm_phase(PG8_LAS unsigned char* lds, const Gemm g, const Sched& S, const Epi& E) {
;     ...
;         const bool has_next = S.next(ui + 1, nxt);
;         const char* nA = has_next ? (const char*)g.A + (size_t)nxt.pm * tstep : cA; const char* nB = has_next ? (const char*)g.Bt + (size_t)nxt.pn * tstep : cB;
;         for (int t = 0; t < nt; t += 2) {
;             const bool last = (t == nt - 2);
;             const char* a1 = cA + (size_t)(t + 1) * kstep;
;             const char* a2 = last ? nA : cA + (size_t)(t + 2) * kstep; const char* b2 = last ? nB : cB + (size_t)(t + 2) * kstep;
;             const char* a3 = a2 + kstep; const char* b3 = b2 + kstep;
;             if (last && has_next) S.a_ready(nxt);
;             if constexpr (SP2) {
;             PG8_LDB(B0, 0, 0); PG8_LDB(B1, 0, 1); PG8_SCHED; PG8_LDA(At, 0, 0); PG8_STAGE(PG8_SA(1, 1), a1 + hstep, voffA);
;             PG8_WAIT_V(8); PG8_WAIT_L(0); PG8_BAR; PG8_MMA(0, 0, At, B0); PG8_MMA(0, 1, At, B1); PG8_BAR; PG8_SCHED;
;             PG8_LDA(At, 0, 1); PG8_STAGE(PG8_SB(0, 0), b2, voffB); PG8_STAGE(PG8_SB(0, 1), b2 + hstep, voffB); PG8_STAGE(PG8_SA(0, 0), a2, voffA);
;             PG8_WAIT_V(8); PG8_WAIT_L(0); PG8_BAR; PG8_MMA(1, 0, At, B0); PG8_MMA(1, 1, At, B1); PG8_BAR; PG8_SCHED;
;             PG8_LDB(B0, 1, 0); PG8_LDB(B1, 1, 1); PG8_SCHED; PG8_LDA(At, 1, 0); PG8_STAGE(PG8_SA(0, 1), a2 + hstep, voffA);
;             PG8_WAIT_V(8); PG8_WAIT_L(0); PG8_BAR; PG8_MMA(0, 0, At, B0); PG8_MMA(0, 1, At, B1); PG8_BAR; PG8_SCHED;
;             PG8_LDA(At, 1, 1); PG8_STAGE(PG8_SB(1, 0), b3, voffB); PG8_STAGE(PG8_SB(1, 1), b3 + hstep, voffB); PG8_STAGE(PG8_SA(1, 0), a3, voffA);
;             PG8_WAIT_V(8); PG8_WAIT_L(0); PG8_BAR; PG8_MMA(1, 0, At, B0); PG8_MMA(1, 1, At, B1); PG8_BAR; PG8_SCHED;
.LBB0_871:
	s_ashr_i32 s15, s14, 31
	s_lshl_b64 s[16:17], s[14:15], 20
	s_add_u32 s16, s70, s16
	s_addc_u32 s17, s71, s17
	s_and_b64 s[18:19], s[2:3], exec
	s_cselect_b32 s15, s17, s23
	s_cselect_b32 s44, s16, s22
	s_ashr_i32 s13, s12, 31
	s_lshl_b64 s[18:19], s[12:13], 20
	s_add_u32 s18, s11, s18
	s_addc_u32 s19, s28, s19
	s_and_b64 s[26:27], s[2:3], exec
	s_cselect_b32 s13, s19, s25
	s_cselect_b32 s45, s18, s24
	s_add_u32 s22, s22, 0x80080
	s_addc_u32 s23, s23, 0
	s_add_u32 s46, s24, 0x100
	s_addc_u32 s47, s25, 0
	s_mov_b32 s48, -2
	v_add_u32_e32 v248, 0x18000, v151
	v_add_u32_e32 v249, 0x1c000, v151
	ds_read_b128 v[146:149], v153
	ds_read_b128 v[156:159], v153 offset:1024
	ds_read_b128 v[160:163], v153 offset:2048
	ds_read_b128 v[164:167], v153 offset:3072
	ds_read_b128 v[168:171], v154
	ds_read_b128 v[172:175], v154 offset:1024
	ds_read_b128 v[176:179], v154 offset:2048
	ds_read_b128 v[180:183], v154 offset:3072
	s_add_u32 s24, s22, 0xfff80080
	s_addc_u32 s25, s23, -1
	s_cmp_eq_u32 s48, 28
	s_cselect_b32 s27, s15, s25
	s_cselect_b32 s26, s44, s24
	s_cselect_b32 s25, s13, s47
	s_cselect_b32 s24, s45, s46
	s_add_i32 m0, s21, 0xc000
	ds_read_b128 v[190:193], v155
	ds_read_b128 v[194:197], v155 offset:1024
	ds_read_b128 v[198:201], v155 offset:2048
	ds_read_b128 v[202:205], v155 offset:3072
	ds_read_b128 v[206:209], v155 offset:4096
	ds_read_b128 v[216:219], v155 offset:5120
	ds_read_b128 v[220:223], v155 offset:6144
	ds_read_b128 v[224:227], v155 offset:7168
	global_load_lds_dwordx4 v138, s[22:23]
	s_add_i32 m0, s21, 0xe000
	s_nop 0
	global_load_lds_dwordx4 v140, s[22:23]
	s_waitcnt vmcnt(8)
	s_waitcnt lgkmcnt(0)
	s_barrier
	s_setprio 1
	s_waitcnt lgkmcnt(0)
	v_mfma_f32_16x16x32_bf16 v[126:129], v[146:149], v[190:193], 0
	v_mfma_f32_16x16x32_bf16 v[122:125], v[160:163], v[190:193], 0
	v_mfma_f32_16x16x32_bf16 v[110:113], v[146:149], v[198:201], 0
	v_mfma_f32_16x16x32_bf16 v[106:109], v[160:163], v[198:201], 0
	v_mfma_f32_16x16x32_bf16 v[94:97], v[146:149], v[206:209], 0
	v_mfma_f32_16x16x32_bf16 v[90:93], v[160:163], v[206:209], 0
	v_mfma_f32_16x16x32_bf16 v[78:81], v[146:149], v[220:223], 0
	v_mfma_f32_16x16x32_bf16 v[74:77], v[160:163], v[220:223], 0
	v_mfma_f32_16x16x32_bf16 v[126:129], v[156:159], v[194:197], v[126:129]
	v_mfma_f32_16x16x32_bf16 v[122:125], v[164:167], v[194:197], v[122:125]
	v_mfma_f32_16x16x32_bf16 v[110:113], v[156:159], v[202:205], v[110:113]
	v_mfma_f32_16x16x32_bf16 v[106:109], v[164:167], v[202:205], v[106:109]
	v_mfma_f32_16x16x32_bf16 v[94:97], v[156:159], v[216:219], v[94:97]
	v_mfma_f32_16x16x32_bf16 v[90:93], v[164:167], v[216:219], v[90:93]
	v_mfma_f32_16x16x32_bf16 v[78:81], v[156:159], v[224:227], v[78:81]
	v_mfma_f32_16x16x32_bf16 v[74:77], v[164:167], v[224:227], v[74:77]
	s_setprio 0
	s_setprio 1
	v_mfma_f32_16x16x32_bf16 v[118:121], v[168:171], v[190:193], 0
	v_mfma_f32_16x16x32_bf16 v[114:117], v[176:179], v[190:193], 0
	v_mfma_f32_16x16x32_bf16 v[102:105], v[168:171], v[198:201], 0
	v_mfma_f32_16x16x32_bf16 v[98:101], v[176:179], v[198:201], 0
	v_mfma_f32_16x16x32_bf16 v[86:89], v[168:171], v[206:209], 0
	v_mfma_f32_16x16x32_bf16 v[82:85], v[176:179], v[206:209], 0
	v_mfma_f32_16x16x32_bf16 v[70:73], v[168:171], v[220:223], 0
	v_mfma_f32_16x16x32_bf16 v[66:69], v[176:179], v[220:223], 0
	v_mfma_f32_16x16x32_bf16 v[118:121], v[172:175], v[194:197], v[118:121]
	v_mfma_f32_16x16x32_bf16 v[114:117], v[180:183], v[194:197], v[114:117]
	v_mfma_f32_16x16x32_bf16 v[102:105], v[172:175], v[202:205], v[102:105]
	v_mfma_f32_16x16x32_bf16 v[98:101], v[180:183], v[202:205], v[98:101]
	v_mfma_f32_16x16x32_bf16 v[86:89], v[172:175], v[216:219], v[86:89]
	v_mfma_f32_16x16x32_bf16 v[82:85], v[180:183], v[216:219], v[82:85]
	v_mfma_f32_16x16x32_bf16 v[70:73], v[172:175], v[224:227], v[70:73]
	v_mfma_f32_16x16x32_bf16 v[66:69], v[180:183], v[224:227], v[66:69]
	s_setprio 0
	s_barrier
	s_add_i32 s49, s40, s29
	s_mov_b32 m0, s49
	ds_read_b128 v[190:193], v155 offset:16384
	ds_read_b128 v[194:197], v155 offset:17408
	ds_read_b128 v[198:201], v155 offset:18432
	ds_read_b128 v[202:205], v155 offset:19456
	ds_read_b128 v[206:209], v155 offset:20480
	ds_read_b128 v[216:219], v155 offset:21504
	ds_read_b128 v[220:223], v155 offset:22528
	ds_read_b128 v[224:227], v155 offset:23552
	global_load_lds_dwordx4 v134, s[24:25]
	s_add_i32 m0, s49, 0x2000
	s_add_u32 s50, s24, 0x80000
	s_addc_u32 s51, s25, 0
	s_add_i32 s49, s41, s29
	global_load_lds_dwordx4 v130, s[24:25]
	s_mov_b32 m0, s49
	s_nop 0
	global_load_lds_dwordx4 v134, s[50:51]
	s_add_i32 m0, s49, 0x2000
	s_nop 0
	global_load_lds_dwordx4 v130, s[50:51]
	s_mov_b32 m0, s21
	s_nop 0
	global_load_lds_dwordx4 v136, s[26:27]
	s_mov_b32 m0, s33
	s_nop 0
	global_load_lds_dwordx4 v132, s[26:27]
	s_waitcnt vmcnt(8)
	s_waitcnt lgkmcnt(0)
	s_barrier
; #define PG8_STAGE(bufoff, gbase, voff) do { _Pragma("unroll") for (int _i = 0; _i < 2; ++_i) \
;         __builtin_amdgcn_global_load_lds((const unsigned*)((const char*)(gbase) + (voff)[_i]), (PG8_LAS unsigned*)(lds + (bufoff) + ldsw + _i * 8192), 16, 0, 0); } while (0)
; #define PG8_LDA(dst, b, h) do { _Pragma("unroll") for (int m = 0; m < 4; ++m) _Pragma("unroll") for (int k = 0; k < 2; ++k) dst[m][k] = *(const PG8_LAS bf16x8*)(lds + PG8_SA(b, h) + aoff + m * 2048 + k * 1024); } while (0)
; #define PG8_LDB(dst, b, h) do { _Pragma("unroll") for (int n = 0; n < 2; ++n) _Pragma("unroll") for (int k = 0; k < 2; ++k) dst[n][k] = *(const PG8_LAS bf16x8*)(lds + PG8_SB(b, h) + boff + n * 2048 + k * 1024); } while (0)
; #define PG8_WAIT_V(n) asm volatile("s_waitcnt vmcnt(" #n ")" ::: "memory")
; #define PG8_WAIT_L(n) asm volatile("s_waitcnt lgkmcnt(" #n ")" ::: "memory")
; #define PG8_BAR __builtin_amdgcn_s_barrier()
; #define PG8_SCHED __builtin_amdgcn_sched_barrier(0)
; template <class Epi, class Sched, bool ALIGN_EPI = false, bool SP2 = false>
; __device__ __forceinline__ void gemm_phase(PG8_LAS unsigned char* lds, const Gemm g, const Sched& S, const Epi& E) {
;     ...
;             PG8_WAIT_V(8); PG8_WAIT_L(0); PG8_BAR; PG8_MMA(1, 0, At, B0); PG8_MMA(1, 1, At, B1); PG8_BAR; PG8_SCHED;
;             PG8_LDB(B0, 1, 0); PG8_LDB(B1, 1, 1); PG8_SCHED; PG8_LDA(At, 1, 0); PG8_STAGE(PG8_SA(0, 1), a2 + hstep, voffA);
;             PG8_WAIT_V(8); PG8_WAIT_L(0); PG8_BAR; PG8_MMA(0, 0, At, B0); PG8_MMA(0, 1, At, B1); PG8_BAR; PG8_SCHED;
	s_setprio 1
	s_waitcnt lgkmcnt(0)
	v_mfma_f32_16x16x32_bf16 v[62:65], v[146:149], v[190:193], 0
	v_mfma_f32_16x16x32_bf16 v[58:61], v[160:163], v[190:193], 0
	v_mfma_f32_16x16x32_bf16 v[46:49], v[146:149], v[198:201], 0
	v_mfma_f32_16x16x32_bf16 v[42:45], v[160:163], v[198:201], 0
	v_mfma_f32_16x16x32_bf16 v[30:33], v[146:149], v[206:209], 0
	v_mfma_f32_16x16x32_bf16 v[26:29], v[160:163], v[206:209], 0
	v_mfma_f32_16x16x32_bf16 v[14:17], v[146:149], v[220:223], 0
	v_mfma_f32_16x16x32_bf16 v[10:13], v[160:163], v[220:223], 0
	v_mfma_f32_16x16x32_bf16 v[62:65], v[156:159], v[194:197], v[62:65]
	v_mfma_f32_16x16x32_bf16 v[58:61], v[164:167], v[194:197], v[58:61]
	v_mfma_f32_16x16x32_bf16 v[46:49], v[156:159], v[202:205], v[46:49]
	v_mfma_f32_16x16x32_bf16 v[42:45], v[164:167], v[202:205], v[42:45]
	v_mfma_f32_16x16x32_bf16 v[30:33], v[156:159], v[216:219], v[30:33]
	v_mfma_f32_16x16x32_bf16 v[26:29], v[164:167], v[216:219], v[26:29]
	v_mfma_f32_16x16x32_bf16 v[14:17], v[156:159], v[224:227], v[14:17]
	v_mfma_f32_16x16x32_bf16 v[10:13], v[164:167], v[224:227], v[10:13]
	s_setprio 0
	s_setprio 1
	v_mfma_f32_16x16x32_bf16 v[54:57], v[168:171], v[190:193], 0
	v_mfma_f32_16x16x32_bf16 v[50:53], v[176:179], v[190:193], 0
	v_mfma_f32_16x16x32_bf16 v[38:41], v[168:171], v[198:201], 0
	v_mfma_f32_16x16x32_bf16 v[34:37], v[176:179], v[198:201], 0
	v_mfma_f32_16x16x32_bf16 v[22:25], v[168:171], v[206:209], 0
	v_mfma_f32_16x16x32_bf16 v[18:21], v[176:179], v[206:209], 0
	v_mfma_f32_16x16x32_bf16 v[6:9], v[168:171], v[220:223], 0
	v_mfma_f32_16x16x32_bf16 v[2:5], v[176:179], v[220:223], 0
	v_mfma_f32_16x16x32_bf16 v[54:57], v[172:175], v[194:197], v[54:57]
	v_mfma_f32_16x16x32_bf16 v[50:53], v[180:183], v[194:197], v[50:53]
	v_mfma_f32_16x16x32_bf16 v[38:41], v[172:175], v[202:205], v[38:41]
	v_mfma_f32_16x16x32_bf16 v[34:37], v[180:183], v[202:205], v[34:37]
	v_mfma_f32_16x16x32_bf16 v[22:25], v[172:175], v[216:219], v[22:25]
	v_mfma_f32_16x16x32_bf16 v[18:21], v[180:183], v[216:219], v[18:21]
	v_mfma_f32_16x16x32_bf16 v[6:9], v[172:175], v[224:227], v[6:9]
	v_mfma_f32_16x16x32_bf16 v[2:5], v[180:183], v[224:227], v[2:5]
	s_setprio 0
	s_barrier
	s_add_i32 s49, 0, 0x18000
	s_add_i32 s50, 0, 0x1c000
	ds_read_b128 v[146:149], v248
	ds_read_b128 v[156:159], v248 offset:1024
	ds_read_b128 v[160:163], v248 offset:2048
	ds_read_b128 v[164:167], v248 offset:3072
	ds_read_b128 v[168:171], v249
	ds_read_b128 v[172:175], v249 offset:1024
	ds_read_b128 v[176:179], v249 offset:2048
	ds_read_b128 v[180:183], v249 offset:3072
	s_add_u32 s26, s26, 0x80000
	s_addc_u32 s27, s27, 0
	s_mov_b32 m0, s34
	ds_read_b128 v[190:193], v155 offset:32768
	ds_read_b128 v[194:197], v155 offset:33792
	ds_read_b128 v[198:201], v155 offset:34816
	ds_read_b128 v[202:205], v155 offset:35840
	ds_read_b128 v[206:209], v155 offset:36864
	ds_read_b128 v[216:219], v155 offset:37888
	ds_read_b128 v[220:223], v155 offset:38912
	ds_read_b128 v[224:227], v155 offset:39936
	global_load_lds_dwordx4 v136, s[26:27]
	s_mov_b32 m0, s35
	s_nop 0
	global_load_lds_dwordx4 v132, s[26:27]
	s_waitcnt vmcnt(8)
	s_waitcnt lgkmcnt(0)
	s_barrier
	s_setprio 1
	s_waitcnt lgkmcnt(0)
	v_mfma_f32_16x16x32_bf16 v[126:129], v[146:149], v[190:193], v[126:129]
	v_mfma_f32_16x16x32_bf16 v[122:125], v[160:163], v[190:193], v[122:125]
	v_mfma_f32_16x16x32_bf16 v[110:113], v[146:149], v[198:201], v[110:113]
	v_mfma_f32_16x16x32_bf16 v[106:109], v[160:163], v[198:201], v[106:109]
	v_mfma_f32_16x16x32_bf16 v[94:97], v[146:149], v[206:209], v[94:97]
	v_mfma_f32_16x16x32_bf16 v[90:93], v[160:163], v[206:209], v[90:93]
	v_mfma_f32_16x16x32_bf16 v[78:81], v[146:149], v[220:223], v[78:81]
	v_mfma_f32_16x16x32_bf16 v[74:77], v[160:163], v[220:223], v[74:77]
	v_mfma_f32_16x16x32_bf16 v[126:129], v[156:159], v[194:197], v[126:129]
	v_mfma_f32_16x16x32_bf16 v[122:125], v[164:167], v[194:197], v[122:125]
	v_mfma_f32_16x16x32_bf16 v[110:113], v[156:159], v[202:205], v[110:113]
	v_mfma_f32_16x16x32_bf16 v[106:109], v[164:167], v[202:205], v[106:109]
	v_mfma_f32_16x16x32_bf16 v[94:97], v[156:159], v[216:219], v[94:97]
	v_mfma_f32_16x16x32_bf16 v[90:93], v[164:167], v[216:219], v[90:93]
	v_mfma_f32_16x16x32_bf16 v[78:81], v[156:159], v[224:227], v[78:81]
	v_mfma_f32_16x16x32_bf16 v[74:77], v[164:167], v[224:227], v[74:77]
	s_setprio 0
	s_setprio 1
	v_mfma_f32_16x16x32_bf16 v[118:121], v[168:171], v[190:193], v[118:121]
	v_mfma_f32_16x16x32_bf16 v[114:117], v[176:179], v[190:193], v[114:117]
	v_mfma_f32_16x16x32_bf16 v[102:105], v[168:171], v[198:201], v[102:105]
	v_mfma_f32_16x16x32_bf16 v[98:101], v[176:179], v[198:201], v[98:101]
	v_mfma_f32_16x16x32_bf16 v[86:89], v[168:171], v[206:209], v[86:89]
	v_mfma_f32_16x16x32_bf16 v[82:85], v[176:179], v[206:209], v[82:85]
	v_mfma_f32_16x16x32_bf16 v[70:73], v[168:171], v[220:223], v[70:73]
	v_mfma_f32_16x16x32_bf16 v[66:69], v[176:179], v[220:223], v[66:69]
	v_mfma_f32_16x16x32_bf16 v[118:121], v[172:175], v[194:197], v[118:121]
	v_mfma_f32_16x16x32_bf16 v[114:117], v[180:183], v[194:197], v[114:117]
	v_mfma_f32_16x16x32_bf16 v[102:105], v[172:175], v[202:205], v[102:105]
	v_mfma_f32_16x16x32_bf16 v[98:101], v[180:183], v[202:205], v[98:101]
	v_mfma_f32_16x16x32_bf16 v[86:89], v[172:175], v[216:219], v[86:89]
	v_mfma_f32_16x16x32_bf16 v[82:85], v[180:183], v[216:219], v[82:85]
	v_mfma_f32_16x16x32_bf16 v[70:73], v[172:175], v[224:227], v[70:73]
	v_mfma_f32_16x16x32_bf16 v[66:69], v[180:183], v[224:227], v[66:69]
	s_setprio 0
	s_barrier
; #define PG8_STAGE(bufoff, gbase, voff) do { _Pragma("unroll") for (int _i = 0; _i < 2; ++_i) \
;         __builtin_amdgcn_global_load_lds((const unsigned*)((const char*)(gbase) + (voff)[_i]), (PG8_LAS unsigned*)(lds + (bufoff) + ldsw + _i * 8192), 16, 0, 0); } while (0)
; #define PG8_LDA(dst, b, h) do { _Pragma("unroll") for (int m = 0; m < 4; ++m) _Pragma("unroll") for (int k = 0; k < 2; ++k) dst[m][k] = *(const PG8_LAS bf16x8*)(lds + PG8_SA(b, h) + aoff + m * 2048 + k * 1024); } while (0)
; #define PG8_LDB(dst, b, h) do { _Pragma("unroll") for (int n = 0; n < 2; ++n) _Pragma("unroll") for (int k = 0; k < 2; ++k) dst[n][k] = *(const PG8_LAS bf16x8*)(lds + PG8_SB(b, h) + boff + n * 2048 + k * 1024); } while (0)
; #define PG8_WAIT_V(n) asm volatile("s_waitcnt vmcnt(" #n ")" ::: "memory")
; #define PG8_WAIT_L(n) asm volatile("s_waitcnt lgkmcnt(" #n ")" ::: "memory")
; #define PG8_BAR __builtin_amdgcn_s_barrier()
; #define PG8_SCHED __builtin_amdgcn_sched_barrier(0)
; template <class Epi, class Sched, bool ALIGN_EPI = false, bool SP2 = false>
; __device__ __forceinline__ void gemm_phase(PG8_LAS unsigned char* lds, const Gemm g, const Sched& S, const Epi& E) {
;     ...
;         for (int t = 0; t < nt; t += 2) {
;     ...
;             PG8_LDB(B0, 1, 0); PG8_LDB(B1, 1, 1); PG8_SCHED; PG8_LDA(At, 1, 0); PG8_STAGE(PG8_SA(0, 1), a2 + hstep, voffA);
;             PG8_WAIT_V(8); PG8_WAIT_L(0); PG8_BAR; PG8_MMA(0, 0, At, B0); PG8_MMA(0, 1, At, B1); PG8_BAR; PG8_SCHED;
;             PG8_LDA(At, 1, 1); PG8_STAGE(PG8_SB(1, 0), b3, voffB); PG8_STAGE(PG8_SB(1, 1), b3 + hstep, voffB); PG8_STAGE(PG8_SA(1, 0), a3, voffA);
;             PG8_WAIT_V(8); PG8_WAIT_L(0); PG8_BAR; PG8_MMA(1, 0, At, B0); PG8_MMA(1, 1, At, B1); PG8_BAR; PG8_SCHED;
	s_add_u32 s98, s24, 0x80
	s_addc_u32 s99, s25, 0
	s_add_u32 s100, s26, 0xfff80080
	s_addc_u32 s101, s27, -1
	s_add_i32 s26, s49, s29
	s_mov_b32 m0, s26
	ds_read_b128 v[190:193], v155 offset:49152
	ds_read_b128 v[194:197], v155 offset:50176
	ds_read_b128 v[198:201], v155 offset:51200
	ds_read_b128 v[202:205], v155 offset:52224
	ds_read_b128 v[206:209], v155 offset:53248
	ds_read_b128 v[216:219], v155 offset:54272
	ds_read_b128 v[220:223], v155 offset:55296
	ds_read_b128 v[224:227], v155 offset:56320
	global_load_lds_dwordx4 v134, s[98:99]
	s_add_i32 m0, s26, 0x2000
	s_add_u32 s24, s24, 0x80080
	s_addc_u32 s25, s25, 0
	s_add_i32 s26, s50, s29
	global_load_lds_dwordx4 v130, s[98:99]
	s_mov_b32 m0, s26
	s_nop 0
	global_load_lds_dwordx4 v134, s[24:25]
	s_add_i32 m0, s26, 0x2000
	s_nop 0
	global_load_lds_dwordx4 v130, s[24:25]
	s_mov_b32 m0, s37
	s_nop 0
	global_load_lds_dwordx4 v136, s[100:101]
	s_mov_b32 m0, s38
	s_nop 0
	global_load_lds_dwordx4 v132, s[100:101]
	s_waitcnt vmcnt(8)
	s_waitcnt lgkmcnt(0)
	s_barrier
	s_setprio 1
	s_waitcnt lgkmcnt(0)
	v_mfma_f32_16x16x32_bf16 v[62:65], v[146:149], v[190:193], v[62:65]
	v_mfma_f32_16x16x32_bf16 v[58:61], v[160:163], v[190:193], v[58:61]
	v_mfma_f32_16x16x32_bf16 v[46:49], v[146:149], v[198:201], v[46:49]
	v_mfma_f32_16x16x32_bf16 v[42:45], v[160:163], v[198:201], v[42:45]
	v_mfma_f32_16x16x32_bf16 v[30:33], v[146:149], v[206:209], v[30:33]
	v_mfma_f32_16x16x32_bf16 v[26:29], v[160:163], v[206:209], v[26:29]
	v_mfma_f32_16x16x32_bf16 v[14:17], v[146:149], v[220:223], v[14:17]
	v_mfma_f32_16x16x32_bf16 v[10:13], v[160:163], v[220:223], v[10:13]
	v_mfma_f32_16x16x32_bf16 v[62:65], v[156:159], v[194:197], v[62:65]
	v_mfma_f32_16x16x32_bf16 v[58:61], v[164:167], v[194:197], v[58:61]
	v_mfma_f32_16x16x32_bf16 v[46:49], v[156:159], v[202:205], v[46:49]
	v_mfma_f32_16x16x32_bf16 v[42:45], v[164:167], v[202:205], v[42:45]
	v_mfma_f32_16x16x32_bf16 v[30:33], v[156:159], v[216:219], v[30:33]
	v_mfma_f32_16x16x32_bf16 v[26:29], v[164:167], v[216:219], v[26:29]
	v_mfma_f32_16x16x32_bf16 v[14:17], v[156:159], v[224:227], v[14:17]
	v_mfma_f32_16x16x32_bf16 v[10:13], v[164:167], v[224:227], v[10:13]
	s_setprio 0
	s_setprio 1
	v_mfma_f32_16x16x32_bf16 v[54:57], v[168:171], v[190:193], v[54:57]
	v_mfma_f32_16x16x32_bf16 v[50:53], v[176:179], v[190:193], v[50:53]
	v_mfma_f32_16x16x32_bf16 v[38:41], v[168:171], v[198:201], v[38:41]
	v_mfma_f32_16x16x32_bf16 v[34:37], v[176:179], v[198:201], v[34:37]
	v_mfma_f32_16x16x32_bf16 v[22:25], v[168:171], v[206:209], v[22:25]
	v_mfma_f32_16x16x32_bf16 v[18:21], v[176:179], v[206:209], v[18:21]
	v_mfma_f32_16x16x32_bf16 v[6:9], v[168:171], v[220:223], v[6:9]
	v_mfma_f32_16x16x32_bf16 v[2:5], v[176:179], v[220:223], v[2:5]
	v_mfma_f32_16x16x32_bf16 v[54:57], v[172:175], v[194:197], v[54:57]
	v_mfma_f32_16x16x32_bf16 v[50:53], v[180:183], v[194:197], v[50:53]
	v_mfma_f32_16x16x32_bf16 v[38:41], v[172:175], v[202:205], v[38:41]
	v_mfma_f32_16x16x32_bf16 v[34:37], v[180:183], v[202:205], v[34:37]
	v_mfma_f32_16x16x32_bf16 v[22:25], v[172:175], v[216:219], v[22:25]
	v_mfma_f32_16x16x32_bf16 v[18:21], v[180:183], v[216:219], v[18:21]
	v_mfma_f32_16x16x32_bf16 v[6:9], v[172:175], v[224:227], v[6:9]
	v_mfma_f32_16x16x32_bf16 v[2:5], v[180:183], v[224:227], v[2:5]
	s_setprio 0
	s_barrier
	s_add_i32 s48, s48, 2
	s_add_u32 s22, s22, 0x100
	s_addc_u32 s23, s23, 0
	s_add_u32 s46, s46, 0x100
	s_addc_u32 s47, s47, 0
	s_cmp_gt_u32 s48, 29

; #define PG8_STAGE(bufoff, gbase, voff) do { _Pragma("unroll") for (int _i = 0; _i < 2; ++_i) \
;         __builtin_amdgcn_global_load_lds((const unsigned*)((const char*)(gbase) + (voff)[_i]), (PG8_LAS unsigned*)(lds + (bufoff) + ldsw + _i * 8192), 16, 0, 0); } while (0)
; #define PG8_LDA(dst, b, h) do { _Pragma("unroll") for (int m = 0; m < 4; ++m) _Pragma("unroll") for (int k = 0; k < 2; ++k) dst[m][k] = *(const PG8_LAS bf16x8*)(lds + PG8_SA(b, h) + aoff + m * 2048 + k * 1024); } while (0)
; #define PG8_BAR __builtin_amdgcn_s_barrier()
; template <class Epi, class Sched, bool ALIGN_EPI = false, bool SP2 = false>
; __device__ __forceinline__ void gemm_phase(PG8_LAS unsigned char* lds, const Gemm g, const Sched& S, const Epi& E) {
;     ...
;         const char* nA = has_next ? (const char*)g.A + (size_t)nxt.pm * tstep : cA; const char* nB = has_next ? (const char*)g.Bt + (size_t)nxt.pn * tstep : cB;
;         for (int t = 0; t < nt; t += 2) {
;             const bool last = (t == nt - 2);
;             const char* a1 = cA + (size_t)(t + 1) * kstep;
;             const char* a2 = last ? nA : cA + (size_t)(t + 2) * kstep; const char* b2 = last ? nB : cB + (size_t)(t + 2) * kstep;
;             const char* a3 = a2 + kstep; const char* b3 = b2 + kstep;
;             if (last && has_next) S.a_ready(nxt);
;             if constexpr (SP2) {
;             PG8_LDB(B0, 0, 0); PG8_LDB(B1, 0, 1); PG8_SCHED; PG8_LDA(At, 0, 0); PG8_STAGE(PG8_SA(1, 1), a1 + hstep, voffA);
;             PG8_WAIT_V(8); PG8_WAIT_L(0); PG8_BAR; PG8_MMA(0, 0, At, B0); PG8_MMA(0, 1, At, B1); PG8_BAR; PG8_SCHED;
;             PG8_LDA(At, 0, 1); PG8_STAGE(PG8_SB(0, 0), b2, voffB); PG8_STAGE(PG8_SB(0, 1), b2 + hstep, voffB); PG8_STAGE(PG8_SA(0, 0), a2, voffA);
;             PG8_WAIT_V(8); PG8_WAIT_L(0); PG8_BAR; PG8_MMA(1, 0, At, B0); PG8_MMA(1, 1, At, B1); PG8_BAR; PG8_SCHED;
;             PG8_LDB(B0, 1, 0); PG8_LDB(B1, 1, 1); PG8_SCHED; PG8_LDA(At, 1, 0); PG8_STAGE(PG8_SA(0, 1), a2 + hstep, voffA);
;             PG8_WAIT_V(8); PG8_WAIT_L(0); PG8_BAR; PG8_MMA(0, 0, At, B0); PG8_MMA(0, 1, At, B1); PG8_BAR; PG8_SCHED;
;             PG8_LDA(At, 1, 1); PG8_STAGE(PG8_SB(1, 0), b3, voffB); PG8_STAGE(PG8_SB(1, 1), b3 + hstep, voffB); PG8_STAGE(PG8_SA(1, 0), a3, voffA);
;             PG8_WAIT_V(8); PG8_WAIT_L(0); PG8_BAR; PG8_MMA(1, 0, At, B0); PG8_MMA(1, 1, At, B1); PG8_BAR; PG8_SCHED;
.LBB0_950:
	s_add_u32 s14, s14, 0x160080
	s_addc_u32 s15, s15, 0
	s_add_u32 s48, s16, 0x100
	s_addc_u32 s49, s17, 0
	s_mov_b32 s50, -2
	v_add_u32_e32 v248, 0x18000, v175
	v_add_u32_e32 v249, 0x1c000, v175
	ds_read_b128 v[130:133], v177
	ds_read_b128 v[134:137], v177 offset:1024
	ds_read_b128 v[138:141], v177 offset:2048
	ds_read_b128 v[142:145], v177 offset:3072
	ds_read_b128 v[146:149], v178
	ds_read_b128 v[150:153], v178 offset:1024
	ds_read_b128 v[170:173], v178 offset:2048
	ds_read_b128 v[180:183], v178 offset:3072
	s_add_u32 s16, s14, 0xffea0080
	s_addc_u32 s17, s15, -1
	s_cmpk_eq_i32 s50, 0x54
	s_cselect_b32 s19, s5, s17
	s_cselect_b32 s18, s4, s16
	s_cselect_b32 s17, s13, s49
	s_cselect_b32 s16, s12, s48
	s_add_i32 m0, s24, 0xc000
	ds_read_b128 v[190:193], v179
	ds_read_b128 v[194:197], v179 offset:1024
	ds_read_b128 v[198:201], v179 offset:2048
	ds_read_b128 v[202:205], v179 offset:3072
	ds_read_b128 v[206:209], v179 offset:4096
	ds_read_b128 v[216:219], v179 offset:5120
	ds_read_b128 v[220:223], v179 offset:6144
	ds_read_b128 v[224:227], v179 offset:7168
	global_load_lds_dwordx4 v162, s[14:15]
	s_add_i32 m0, s24, 0xe000
	s_nop 0
	global_load_lds_dwordx4 v164, s[14:15]
	s_waitcnt vmcnt(8)
	s_waitcnt lgkmcnt(0)
	s_barrier
	s_setprio 1
	s_waitcnt lgkmcnt(0)
	v_mfma_f32_16x16x32_bf16 v[126:129], v[130:133], v[190:193], 0
	v_mfma_f32_16x16x32_bf16 v[122:125], v[138:141], v[190:193], 0
	v_mfma_f32_16x16x32_bf16 v[110:113], v[130:133], v[198:201], 0
	v_mfma_f32_16x16x32_bf16 v[106:109], v[138:141], v[198:201], 0
	v_mfma_f32_16x16x32_bf16 v[98:101], v[130:133], v[206:209], 0
	v_mfma_f32_16x16x32_bf16 v[90:93], v[138:141], v[206:209], 0
	v_mfma_f32_16x16x32_bf16 v[82:85], v[130:133], v[220:223], 0
	v_mfma_f32_16x16x32_bf16 v[74:77], v[138:141], v[220:223], 0
	v_mfma_f32_16x16x32_bf16 v[126:129], v[134:137], v[194:197], v[126:129]
	v_mfma_f32_16x16x32_bf16 v[122:125], v[142:145], v[194:197], v[122:125]
	v_mfma_f32_16x16x32_bf16 v[110:113], v[134:137], v[202:205], v[110:113]
	v_mfma_f32_16x16x32_bf16 v[106:109], v[142:145], v[202:205], v[106:109]
	v_mfma_f32_16x16x32_bf16 v[98:101], v[134:137], v[216:219], v[98:101]
	v_mfma_f32_16x16x32_bf16 v[90:93], v[142:145], v[216:219], v[90:93]
	v_mfma_f32_16x16x32_bf16 v[82:85], v[134:137], v[224:227], v[82:85]
	v_mfma_f32_16x16x32_bf16 v[74:77], v[142:145], v[224:227], v[74:77]
	s_setprio 0
	s_setprio 1
	v_mfma_f32_16x16x32_bf16 v[118:121], v[146:149], v[190:193], 0
	v_mfma_f32_16x16x32_bf16 v[114:117], v[170:173], v[190:193], 0
	v_mfma_f32_16x16x32_bf16 v[102:105], v[146:149], v[198:201], 0
	v_mfma_f32_16x16x32_bf16 v[94:97], v[170:173], v[198:201], 0
	v_mfma_f32_16x16x32_bf16 v[86:89], v[146:149], v[206:209], 0
	v_mfma_f32_16x16x32_bf16 v[78:81], v[170:173], v[206:209], 0
	v_mfma_f32_16x16x32_bf16 v[70:73], v[146:149], v[220:223], 0
	v_mfma_f32_16x16x32_bf16 v[66:69], v[170:173], v[220:223], 0
	v_mfma_f32_16x16x32_bf16 v[118:121], v[150:153], v[194:197], v[118:121]
	v_mfma_f32_16x16x32_bf16 v[114:117], v[180:183], v[194:197], v[114:117]
	v_mfma_f32_16x16x32_bf16 v[102:105], v[150:153], v[202:205], v[102:105]
	v_mfma_f32_16x16x32_bf16 v[94:97], v[180:183], v[202:205], v[94:97]
	v_mfma_f32_16x16x32_bf16 v[86:89], v[150:153], v[216:219], v[86:89]
	v_mfma_f32_16x16x32_bf16 v[78:81], v[180:183], v[216:219], v[78:81]
	v_mfma_f32_16x16x32_bf16 v[70:73], v[150:153], v[224:227], v[70:73]
	v_mfma_f32_16x16x32_bf16 v[66:69], v[180:183], v[224:227], v[66:69]
	s_setprio 0
	s_barrier
	s_add_i32 s51, s36, s23
	s_mov_b32 m0, s51
	ds_read_b128 v[190:193], v179 offset:16384
	ds_read_b128 v[194:197], v179 offset:17408
	ds_read_b128 v[198:201], v179 offset:18432
	ds_read_b128 v[202:205], v179 offset:19456
	ds_read_b128 v[206:209], v179 offset:20480
	ds_read_b128 v[216:219], v179 offset:21504
	ds_read_b128 v[220:223], v179 offset:22528
	ds_read_b128 v[224:227], v179 offset:23552
	global_load_lds_dwordx4 v156, s[16:17]
	s_add_i32 m0, s51, 0x2000
	s_add_u32 s52, s16, 0x160000
	s_addc_u32 s53, s17, 0
	s_add_i32 s51, s37, s23
	global_load_lds_dwordx4 v160, s[16:17]
	s_mov_b32 m0, s51
	s_nop 0
	global_load_lds_dwordx4 v156, s[52:53]
	s_add_i32 m0, s51, 0x2000
	s_nop 0
	global_load_lds_dwordx4 v160, s[52:53]
	s_mov_b32 m0, s24
	s_nop 0
	global_load_lds_dwordx4 v154, s[18:19]
	s_mov_b32 m0, s25
	s_nop 0
	global_load_lds_dwordx4 v158, s[18:19]
	s_waitcnt vmcnt(8)
	s_waitcnt lgkmcnt(0)
	s_barrier
	s_setprio 1
	s_waitcnt lgkmcnt(0)
	v_mfma_f32_16x16x32_bf16 v[62:65], v[130:133], v[190:193], 0
	v_mfma_f32_16x16x32_bf16 v[58:61], v[138:141], v[190:193], 0
	v_mfma_f32_16x16x32_bf16 v[50:53], v[130:133], v[198:201], 0
	v_mfma_f32_16x16x32_bf16 v[42:45], v[138:141], v[198:201], 0
	v_mfma_f32_16x16x32_bf16 v[34:37], v[130:133], v[206:209], 0
	v_mfma_f32_16x16x32_bf16 v[26:29], v[138:141], v[206:209], 0
	v_mfma_f32_16x16x32_bf16 v[18:21], v[130:133], v[220:223], 0
	v_mfma_f32_16x16x32_bf16 v[10:13], v[138:141], v[220:223], 0
	v_mfma_f32_16x16x32_bf16 v[62:65], v[134:137], v[194:197], v[62:65]
	v_mfma_f32_16x16x32_bf16 v[58:61], v[142:145], v[194:197], v[58:61]
	v_mfma_f32_16x16x32_bf16 v[50:53], v[134:137], v[202:205], v[50:53]
	v_mfma_f32_16x16x32_bf16 v[42:45], v[142:145], v[202:205], v[42:45]
	v_mfma_f32_16x16x32_bf16 v[34:37], v[134:137], v[216:219], v[34:37]
	v_mfma_f32_16x16x32_bf16 v[26:29], v[142:145], v[216:219], v[26:29]
	v_mfma_f32_16x16x32_bf16 v[18:21], v[134:137], v[224:227], v[18:21]
	v_mfma_f32_16x16x32_bf16 v[10:13], v[142:145], v[224:227], v[10:13]
	s_setprio 0
	s_setprio 1
	v_mfma_f32_16x16x32_bf16 v[54:57], v[146:149], v[190:193], 0
	v_mfma_f32_16x16x32_bf16 v[46:49], v[170:173], v[190:193], 0
	v_mfma_f32_16x16x32_bf16 v[38:41], v[146:149], v[198:201], 0
	v_mfma_f32_16x16x32_bf16 v[30:33], v[170:173], v[198:201], 0
	v_mfma_f32_16x16x32_bf16 v[22:25], v[146:149], v[206:209], 0
	v_mfma_f32_16x16x32_bf16 v[14:17], v[170:173], v[206:209], 0
	v_mfma_f32_16x16x32_bf16 v[6:9], v[146:149], v[220:223], 0
	v_mfma_f32_16x16x32_bf16 v[2:5], v[170:173], v[220:223], 0
	v_mfma_f32_16x16x32_bf16 v[54:57], v[150:153], v[194:197], v[54:57]
	v_mfma_f32_16x16x32_bf16 v[46:49], v[180:183], v[194:197], v[46:49]
	v_mfma_f32_16x16x32_bf16 v[38:41], v[150:153], v[202:205], v[38:41]
	v_mfma_f32_16x16x32_bf16 v[30:33], v[180:183], v[202:205], v[30:33]
	v_mfma_f32_16x16x32_bf16 v[22:25], v[150:153], v[216:219], v[22:25]
	v_mfma_f32_16x16x32_bf16 v[14:17], v[180:183], v[216:219], v[14:17]
	v_mfma_f32_16x16x32_bf16 v[6:9], v[150:153], v[224:227], v[6:9]
	v_mfma_f32_16x16x32_bf16 v[2:5], v[180:183], v[224:227], v[2:5]
	s_setprio 0
	s_barrier
; #define PG8_STAGE(bufoff, gbase, voff) do { _Pragma("unroll") for (int _i = 0; _i < 2; ++_i) \
;         __builtin_amdgcn_global_load_lds((const unsigned*)((const char*)(gbase) + (voff)[_i]), (PG8_LAS unsigned*)(lds + (bufoff) + ldsw + _i * 8192), 16, 0, 0); } while (0)
; #define PG8_LDA(dst, b, h) do { _Pragma("unroll") for (int m = 0; m < 4; ++m) _Pragma("unroll") for (int k = 0; k < 2; ++k) dst[m][k] = *(const PG8_LAS bf16x8*)(lds + PG8_SA(b, h) + aoff + m * 2048 + k * 1024); } while (0)
; #define PG8_LDB(dst, b, h) do { _Pragma("unroll") for (int n = 0; n < 2; ++n) _Pragma("unroll") for (int k = 0; k < 2; ++k) dst[n][k] = *(const PG8_LAS bf16x8*)(lds + PG8_SB(b, h) + boff + n * 2048 + k * 1024); } while (0)
; #define PG8_WAIT_V(n) asm volatile("s_waitcnt vmcnt(" #n ")" ::: "memory")
; #define PG8_WAIT_L(n) asm volatile("s_waitcnt lgkmcnt(" #n ")" ::: "memory")
; #define PG8_BAR __builtin_amdgcn_s_barrier()
; #define PG8_SCHED __builtin_amdgcn_sched_barrier(0)
; template <class Epi, class Sched, bool ALIGN_EPI = false, bool SP2 = false>
; __device__ __forceinline__ void gemm_phase(PG8_LAS unsigned char* lds, const Gemm g, const Sched& S, const Epi& E) {
;     ...
;             PG8_LDB(B0, 1, 0); PG8_LDB(B1, 1, 1); PG8_SCHED; PG8_LDA(At, 1, 0); PG8_STAGE(PG8_SA(0, 1), a2 + hstep, voffA);
;             PG8_WAIT_V(8); PG8_WAIT_L(0); PG8_BAR; PG8_MMA(0, 0, At, B0); PG8_MMA(0, 1, At, B1); PG8_BAR; PG8_SCHED;
;             PG8_LDA(At, 1, 1); PG8_STAGE(PG8_SB(1, 0), b3, voffB); PG8_STAGE(PG8_SB(1, 1), b3 + hstep, voffB); PG8_STAGE(PG8_SA(1, 0), a3, voffA);
;             PG8_WAIT_V(8); PG8_WAIT_L(0); PG8_BAR; PG8_MMA(1, 0, At, B0); PG8_MMA(1, 1, At, B1); PG8_BAR; PG8_SCHED;
	s_add_i32 s51, 0, 0x18000
	s_add_i32 s52, 0, 0x1c000
	ds_read_b128 v[130:133], v248
	ds_read_b128 v[134:137], v248 offset:1024
	ds_read_b128 v[138:141], v248 offset:2048
	ds_read_b128 v[142:145], v248 offset:3072
	ds_read_b128 v[146:149], v249
	ds_read_b128 v[150:153], v249 offset:1024
	ds_read_b128 v[170:173], v249 offset:2048
	ds_read_b128 v[180:183], v249 offset:3072
	s_add_u32 s18, s18, 0x160000
	s_addc_u32 s19, s19, 0
	s_mov_b32 m0, s26
	ds_read_b128 v[190:193], v179 offset:32768
	ds_read_b128 v[194:197], v179 offset:33792
	ds_read_b128 v[198:201], v179 offset:34816
	ds_read_b128 v[202:205], v179 offset:35840
	ds_read_b128 v[206:209], v179 offset:36864
	ds_read_b128 v[216:219], v179 offset:37888
	ds_read_b128 v[220:223], v179 offset:38912
	ds_read_b128 v[224:227], v179 offset:39936
	global_load_lds_dwordx4 v154, s[18:19]
	s_mov_b32 m0, s27
	s_nop 0
	global_load_lds_dwordx4 v158, s[18:19]
	s_waitcnt vmcnt(8)
	s_waitcnt lgkmcnt(0)
	s_barrier
	s_setprio 1
	s_waitcnt lgkmcnt(0)
	v_mfma_f32_16x16x32_bf16 v[126:129], v[130:133], v[190:193], v[126:129]
	v_mfma_f32_16x16x32_bf16 v[122:125], v[138:141], v[190:193], v[122:125]
	v_mfma_f32_16x16x32_bf16 v[110:113], v[130:133], v[198:201], v[110:113]
	v_mfma_f32_16x16x32_bf16 v[106:109], v[138:141], v[198:201], v[106:109]
	v_mfma_f32_16x16x32_bf16 v[98:101], v[130:133], v[206:209], v[98:101]
	v_mfma_f32_16x16x32_bf16 v[90:93], v[138:141], v[206:209], v[90:93]
	v_mfma_f32_16x16x32_bf16 v[82:85], v[130:133], v[220:223], v[82:85]
	v_mfma_f32_16x16x32_bf16 v[74:77], v[138:141], v[220:223], v[74:77]
	v_mfma_f32_16x16x32_bf16 v[126:129], v[134:137], v[194:197], v[126:129]
	v_mfma_f32_16x16x32_bf16 v[122:125], v[142:145], v[194:197], v[122:125]
	v_mfma_f32_16x16x32_bf16 v[110:113], v[134:137], v[202:205], v[110:113]
	v_mfma_f32_16x16x32_bf16 v[106:109], v[142:145], v[202:205], v[106:109]
	v_mfma_f32_16x16x32_bf16 v[98:101], v[134:137], v[216:219], v[98:101]
	v_mfma_f32_16x16x32_bf16 v[90:93], v[142:145], v[216:219], v[90:93]
	v_mfma_f32_16x16x32_bf16 v[82:85], v[134:137], v[224:227], v[82:85]
	v_mfma_f32_16x16x32_bf16 v[74:77], v[142:145], v[224:227], v[74:77]
	s_setprio 0
	s_setprio 1
	v_mfma_f32_16x16x32_bf16 v[118:121], v[146:149], v[190:193], v[118:121]
	v_mfma_f32_16x16x32_bf16 v[114:117], v[170:173], v[190:193], v[114:117]
	v_mfma_f32_16x16x32_bf16 v[102:105], v[146:149], v[198:201], v[102:105]
	v_mfma_f32_16x16x32_bf16 v[94:97], v[170:173], v[198:201], v[94:97]
	v_mfma_f32_16x16x32_bf16 v[86:89], v[146:149], v[206:209], v[86:89]
	v_mfma_f32_16x16x32_bf16 v[78:81], v[170:173], v[206:209], v[78:81]
	v_mfma_f32_16x16x32_bf16 v[70:73], v[146:149], v[220:223], v[70:73]
	v_mfma_f32_16x16x32_bf16 v[66:69], v[170:173], v[220:223], v[66:69]
	v_mfma_f32_16x16x32_bf16 v[118:121], v[150:153], v[194:197], v[118:121]
	v_mfma_f32_16x16x32_bf16 v[114:117], v[180:183], v[194:197], v[114:117]
	v_mfma_f32_16x16x32_bf16 v[102:105], v[150:153], v[202:205], v[102:105]
	v_mfma_f32_16x16x32_bf16 v[94:97], v[180:183], v[202:205], v[94:97]
	v_mfma_f32_16x16x32_bf16 v[86:89], v[150:153], v[216:219], v[86:89]
	v_mfma_f32_16x16x32_bf16 v[78:81], v[180:183], v[216:219], v[78:81]
	v_mfma_f32_16x16x32_bf16 v[70:73], v[150:153], v[224:227], v[70:73]
	v_mfma_f32_16x16x32_bf16 v[66:69], v[180:183], v[224:227], v[66:69]
	s_setprio 0
	s_barrier
	s_add_u32 s98, s16, 0x80
	s_addc_u32 s99, s17, 0
	s_add_u32 s100, s18, 0xffea0080
	s_addc_u32 s101, s19, -1
	s_add_i32 s18, s51, s23
	s_mov_b32 m0, s18
	ds_read_b128 v[190:193], v179 offset:49152
	ds_read_b128 v[194:197], v179 offset:50176
	ds_read_b128 v[198:201], v179 offset:51200
	ds_read_b128 v[202:205], v179 offset:52224
	ds_read_b128 v[206:209], v179 offset:53248
	ds_read_b128 v[216:219], v179 offset:54272
	ds_read_b128 v[220:223], v179 offset:55296
	ds_read_b128 v[224:227], v179 offset:56320
	global_load_lds_dwordx4 v156, s[98:99]
	s_add_i32 m0, s18, 0x2000
	s_add_u32 s16, s16, 0x160080
	s_addc_u32 s17, s17, 0
	s_add_i32 s18, s52, s23
	global_load_lds_dwordx4 v160, s[98:99]
	s_mov_b32 m0, s18
	s_nop 0
	global_load_lds_dwordx4 v156, s[16:17]
	s_add_i32 m0, s18, 0x2000
	s_nop 0
	global_load_lds_dwordx4 v160, s[16:17]
	s_mov_b32 m0, s33
	s_nop 0
	global_load_lds_dwordx4 v154, s[100:101]
	s_mov_b32 m0, s34
	s_nop 0
	global_load_lds_dwordx4 v158, s[100:101]
	s_waitcnt vmcnt(8)
	s_waitcnt lgkmcnt(0)
	s_barrier
	s_setprio 1
	s_waitcnt lgkmcnt(0)
	v_mfma_f32_16x16x32_bf16 v[62:65], v[130:133], v[190:193], v[62:65]
	v_mfma_f32_16x16x32_bf16 v[58:61], v[138:141], v[190:193], v[58:61]
	v_mfma_f32_16x16x32_bf16 v[50:53], v[130:133], v[198:201], v[50:53]
	v_mfma_f32_16x16x32_bf16 v[42:45], v[138:141], v[198:201], v[42:45]
	v_mfma_f32_16x16x32_bf16 v[34:37], v[130:133], v[206:209], v[34:37]
	v_mfma_f32_16x16x32_bf16 v[26:29], v[138:141], v[206:209], v[26:29]
	v_mfma_f32_16x16x32_bf16 v[18:21], v[130:133], v[220:223], v[18:21]
	v_mfma_f32_16x16x32_bf16 v[10:13], v[138:141], v[220:223], v[10:13]
	v_mfma_f32_16x16x32_bf16 v[62:65], v[134:137], v[194:197], v[62:65]
	v_mfma_f32_16x16x32_bf16 v[58:61], v[142:145], v[194:197], v[58:61]
	v_mfma_f32_16x16x32_bf16 v[50:53], v[134:137], v[202:205], v[50:53]
	v_mfma_f32_16x16x32_bf16 v[42:45], v[142:145], v[202:205], v[42:45]
	v_mfma_f32_16x16x32_bf16 v[34:37], v[134:137], v[216:219], v[34:37]
	v_mfma_f32_16x16x32_bf16 v[26:29], v[142:145], v[216:219], v[26:29]
	v_mfma_f32_16x16x32_bf16 v[18:21], v[134:137], v[224:227], v[18:21]
	v_mfma_f32_16x16x32_bf16 v[10:13], v[142:145], v[224:227], v[10:13]
	s_setprio 0
	s_setprio 1
	v_mfma_f32_16x16x32_bf16 v[54:57], v[146:149], v[190:193], v[54:57]
	v_mfma_f32_16x16x32_bf16 v[46:49], v[170:173], v[190:193], v[46:49]
	v_mfma_f32_16x16x32_bf16 v[38:41], v[146:149], v[198:201], v[38:41]
	v_mfma_f32_16x16x32_bf16 v[30:33], v[170:173], v[198:201], v[30:33]
	v_mfma_f32_16x16x32_bf16 v[22:25], v[146:149], v[206:209], v[22:25]
	v_mfma_f32_16x16x32_bf16 v[14:17], v[170:173], v[206:209], v[14:17]
	v_mfma_f32_16x16x32_bf16 v[6:9], v[146:149], v[220:223], v[6:9]
	v_mfma_f32_16x16x32_bf16 v[2:5], v[170:173], v[220:223], v[2:5]
	v_mfma_f32_16x16x32_bf16 v[54:57], v[150:153], v[194:197], v[54:57]
	v_mfma_f32_16x16x32_bf16 v[46:49], v[180:183], v[194:197], v[46:49]
	v_mfma_f32_16x16x32_bf16 v[38:41], v[150:153], v[202:205], v[38:41]
	v_mfma_f32_16x16x32_bf16 v[30:33], v[180:183], v[202:205], v[30:33]
	v_mfma_f32_16x16x32_bf16 v[22:25], v[150:153], v[216:219], v[22:25]
	v_mfma_f32_16x16x32_bf16 v[14:17], v[180:183], v[216:219], v[14:17]
	v_mfma_f32_16x16x32_bf16 v[6:9], v[150:153], v[224:227], v[6:9]
	v_mfma_f32_16x16x32_bf16 v[2:5], v[180:183], v[224:227], v[2:5]
	s_setprio 0
	s_barrier
	s_add_i32 s50, s50, 2
	s_add_u32 s14, s14, 0x100
	s_addc_u32 s15, s15, 0
	s_add_u32 s48, s48, 0x100
	s_addc_u32 s49, s49, 0
	s_cmpk_gt_u32 s50, 0x55

; #define PG8_STAGE(bufoff, gbase, voff) do { _Pragma("unroll") for (int _i = 0; _i < 2; ++_i) \
;         __builtin_amdgcn_global_load_lds((const unsigned*)((const char*)(gbase) + (voff)[_i]), (PG8_LAS unsigned*)(lds + (bufoff) + ldsw + _i * 8192), 16, 0, 0); } while (0)
; #define PG8_LDA(dst, b, h) do { _Pragma("unroll") for (int m = 0; m < 4; ++m) _Pragma("unroll") for (int k = 0; k < 2; ++k) dst[m][k] = *(const PG8_LAS bf16x8*)(lds + PG8_SA(b, h) + aoff + m * 2048 + k * 1024); } while (0)
; template <class Epi, class Sched, bool ALIGN_EPI = false, bool SP2 = false>
; __device__ __forceinline__ void gemm_phase(PG8_LAS unsigned char* lds, const Gemm g, const Sched& S, const Epi& E) {
;     ...
;         const bool has_next = S.next(ui + 1, nxt);
;         const char* nA = has_next ? (const char*)g.A + (size_t)nxt.pm * tstep : cA; const char* nB = has_next ? (const char*)g.Bt + (size_t)nxt.pn * tstep : cB;
;         for (int t = 0; t < nt; t += 2) {
;             const bool last = (t == nt - 2);
;             const char* a1 = cA + (size_t)(t + 1) * kstep;
;             const char* a2 = last ? nA : cA + (size_t)(t + 2) * kstep; const char* b2 = last ? nB : cB + (size_t)(t + 2) * kstep;
;             const char* a3 = a2 + kstep; const char* b3 = b2 + kstep;
;             if (last && has_next) S.a_ready(nxt);
;             if constexpr (SP2) {
;             PG8_LDB(B0, 0, 0); PG8_LDB(B1, 0, 1); PG8_SCHED; PG8_LDA(At, 0, 0); PG8_STAGE(PG8_SA(1, 1), a1 + hstep, voffA);
;             PG8_WAIT_V(8); PG8_WAIT_L(0); PG8_BAR; PG8_MMA(0, 0, At, B0); PG8_MMA(0, 1, At, B1); PG8_BAR; PG8_SCHED;
;             PG8_LDA(At, 0, 1); PG8_STAGE(PG8_SB(0, 0), b2, voffB); PG8_STAGE(PG8_SB(0, 1), b2 + hstep, voffB); PG8_STAGE(PG8_SA(0, 0), a2, voffA);
;             PG8_WAIT_V(8); PG8_WAIT_L(0); PG8_BAR; PG8_MMA(1, 0, At, B0); PG8_MMA(1, 1, At, B1); PG8_BAR; PG8_SCHED;
;             PG8_LDB(B0, 1, 0); PG8_LDB(B1, 1, 1); PG8_SCHED; PG8_LDA(At, 1, 0); PG8_STAGE(PG8_SA(0, 1), a2 + hstep, voffA);
;             PG8_WAIT_V(8); PG8_WAIT_L(0); PG8_BAR; PG8_MMA(0, 0, At, B0); PG8_MMA(0, 1, At, B1); PG8_BAR; PG8_SCHED;
;             PG8_LDA(At, 1, 1); PG8_STAGE(PG8_SB(1, 0), b3, voffB); PG8_STAGE(PG8_SB(1, 1), b3 + hstep, voffB); PG8_STAGE(PG8_SA(1, 0), a3, voffA);
;             PG8_WAIT_V(8); PG8_WAIT_L(0); PG8_BAR; PG8_MMA(1, 0, At, B0); PG8_MMA(1, 1, At, B1); PG8_BAR; PG8_SCHED;
.LBB0_1075:
	s_ashr_i32 s23, s22, 31
	s_lshl_b64 s[24:25], s[22:23], 20
	s_add_u32 s24, s70, s24
	s_addc_u32 s25, s71, s25
	s_and_b64 s[26:27], s[2:3], exec
	s_cselect_b32 s23, s25, s31
	s_cselect_b32 s29, s24, s30
	s_ashr_i32 s21, s20, 31
	s_lshl_b64 s[26:27], s[20:21], 20
	s_add_u32 s26, s33, s26
	s_addc_u32 s27, s38, s27
	s_and_b64 s[36:37], s[2:3], exec
	s_cselect_b32 s21, s27, s35
	s_cselect_b32 s55, s26, s34
	s_add_u32 s30, s30, 0x80080
	s_addc_u32 s31, s31, 0
	s_add_u32 s56, s34, 0x100
	s_addc_u32 s57, s35, 0
	s_mov_b32 s58, -2
	v_add_u32_e32 v248, 0x18000, v155
	v_add_u32_e32 v249, 0x1c000, v155
	ds_read_b128 v[148:151], v157
	ds_read_b128 v[160:163], v157 offset:1024
	ds_read_b128 v[164:167], v157 offset:2048
	ds_read_b128 v[168:171], v157 offset:3072
	ds_read_b128 v[172:175], v158
	ds_read_b128 v[176:179], v158 offset:1024
	ds_read_b128 v[180:183], v158 offset:2048
	ds_read_b128 v[190:193], v158 offset:3072
	s_add_u32 s34, s30, 0xfff80080
	s_addc_u32 s35, s31, -1
	s_cmp_eq_u32 s58, 28
	s_cselect_b32 s37, s23, s35
	s_cselect_b32 s36, s29, s34
	s_cselect_b32 s35, s21, s57
	s_cselect_b32 s34, s55, s56
	s_add_i32 m0, s42, 0xc000
	ds_read_b128 v[194:197], v159
	ds_read_b128 v[198:201], v159 offset:1024
	ds_read_b128 v[202:205], v159 offset:2048
	ds_read_b128 v[206:209], v159 offset:3072
	ds_read_b128 v[216:219], v159 offset:4096
	ds_read_b128 v[220:223], v159 offset:5120
	ds_read_b128 v[224:227], v159 offset:6144
	ds_read_b128 v[228:231], v159 offset:7168
	global_load_lds_dwordx4 v140, s[30:31]
	s_add_i32 m0, s42, 0xe000
	s_nop 0
	global_load_lds_dwordx4 v142, s[30:31]
	s_waitcnt vmcnt(8)
	s_waitcnt lgkmcnt(0)
	s_barrier
	s_setprio 1
	s_waitcnt lgkmcnt(0)
	v_mfma_f32_16x16x32_bf16 v[126:129], v[148:151], v[194:197], 0
	v_mfma_f32_16x16x32_bf16 v[122:125], v[164:167], v[194:197], 0
	v_mfma_f32_16x16x32_bf16 v[118:121], v[148:151], v[202:205], 0
	v_mfma_f32_16x16x32_bf16 v[110:113], v[164:167], v[202:205], 0
	v_mfma_f32_16x16x32_bf16 v[102:105], v[148:151], v[216:219], 0
	v_mfma_f32_16x16x32_bf16 v[94:97], v[164:167], v[216:219], 0
	v_mfma_f32_16x16x32_bf16 v[86:89], v[148:151], v[224:227], 0
	v_mfma_f32_16x16x32_bf16 v[78:81], v[164:167], v[224:227], 0
	v_mfma_f32_16x16x32_bf16 v[126:129], v[160:163], v[198:201], v[126:129]
	v_mfma_f32_16x16x32_bf16 v[122:125], v[168:171], v[198:201], v[122:125]
	v_mfma_f32_16x16x32_bf16 v[118:121], v[160:163], v[206:209], v[118:121]
	v_mfma_f32_16x16x32_bf16 v[110:113], v[168:171], v[206:209], v[110:113]
	v_mfma_f32_16x16x32_bf16 v[102:105], v[160:163], v[220:223], v[102:105]
	v_mfma_f32_16x16x32_bf16 v[94:97], v[168:171], v[220:223], v[94:97]
	v_mfma_f32_16x16x32_bf16 v[86:89], v[160:163], v[228:231], v[86:89]
	v_mfma_f32_16x16x32_bf16 v[78:81], v[168:171], v[228:231], v[78:81]
	s_setprio 0
	s_setprio 1
	v_mfma_f32_16x16x32_bf16 v[114:117], v[172:175], v[194:197], 0
	v_mfma_f32_16x16x32_bf16 v[106:109], v[180:183], v[194:197], 0
	v_mfma_f32_16x16x32_bf16 v[98:101], v[172:175], v[202:205], 0
	v_mfma_f32_16x16x32_bf16 v[90:93], v[180:183], v[202:205], 0
	v_mfma_f32_16x16x32_bf16 v[82:85], v[172:175], v[216:219], 0
	v_mfma_f32_16x16x32_bf16 v[74:77], v[180:183], v[216:219], 0
	v_mfma_f32_16x16x32_bf16 v[70:73], v[172:175], v[224:227], 0
	v_mfma_f32_16x16x32_bf16 v[66:69], v[180:183], v[224:227], 0
	v_mfma_f32_16x16x32_bf16 v[114:117], v[176:179], v[198:201], v[114:117]
	v_mfma_f32_16x16x32_bf16 v[106:109], v[190:193], v[198:201], v[106:109]
	v_mfma_f32_16x16x32_bf16 v[98:101], v[176:179], v[206:209], v[98:101]
	v_mfma_f32_16x16x32_bf16 v[90:93], v[190:193], v[206:209], v[90:93]
	v_mfma_f32_16x16x32_bf16 v[82:85], v[176:179], v[220:223], v[82:85]
	v_mfma_f32_16x16x32_bf16 v[74:77], v[190:193], v[220:223], v[74:77]
	v_mfma_f32_16x16x32_bf16 v[70:73], v[176:179], v[228:231], v[70:73]
	v_mfma_f32_16x16x32_bf16 v[66:69], v[190:193], v[228:231], v[66:69]
	s_setprio 0
	s_barrier
	s_add_i32 s59, s51, s39
	s_mov_b32 m0, s59
	ds_read_b128 v[194:197], v159 offset:16384
	ds_read_b128 v[198:201], v159 offset:17408
	ds_read_b128 v[202:205], v159 offset:18432
	ds_read_b128 v[206:209], v159 offset:19456
	ds_read_b128 v[216:219], v159 offset:20480
	ds_read_b128 v[220:223], v159 offset:21504
	ds_read_b128 v[224:227], v159 offset:22528
	ds_read_b128 v[228:231], v159 offset:23552
	global_load_lds_dwordx4 v134, s[34:35]
	s_add_i32 m0, s59, 0x2000
	s_add_u32 s60, s34, 0x80000
	s_addc_u32 s61, s35, 0
	s_add_i32 s59, s52, s39
	global_load_lds_dwordx4 v130, s[34:35]
	s_mov_b32 m0, s59
	s_nop 0
	global_load_lds_dwordx4 v134, s[60:61]
	s_add_i32 m0, s59, 0x2000
	s_nop 0
	global_load_lds_dwordx4 v130, s[60:61]
	s_mov_b32 m0, s42
	s_nop 0
	global_load_lds_dwordx4 v136, s[36:37]
	s_mov_b32 m0, s43
	s_nop 0
	global_load_lds_dwordx4 v132, s[36:37]
	s_waitcnt vmcnt(8)
	s_waitcnt lgkmcnt(0)
	s_barrier
; #define PG8_STAGE(bufoff, gbase, voff) do { _Pragma("unroll") for (int _i = 0; _i < 2; ++_i) \
;         __builtin_amdgcn_global_load_lds((const unsigned*)((const char*)(gbase) + (voff)[_i]), (PG8_LAS unsigned*)(lds + (bufoff) + ldsw + _i * 8192), 16, 0, 0); } while (0)
; #define PG8_LDA(dst, b, h) do { _Pragma("unroll") for (int m = 0; m < 4; ++m) _Pragma("unroll") for (int k = 0; k < 2; ++k) dst[m][k] = *(const PG8_LAS bf16x8*)(lds + PG8_SA(b, h) + aoff + m * 2048 + k * 1024); } while (0)
; #define PG8_LDB(dst, b, h) do { _Pragma("unroll") for (int n = 0; n < 2; ++n) _Pragma("unroll") for (int k = 0; k < 2; ++k) dst[n][k] = *(const PG8_LAS bf16x8*)(lds + PG8_SB(b, h) + boff + n * 2048 + k * 1024); } while (0)
; #define PG8_WAIT_V(n) asm volatile("s_waitcnt vmcnt(" #n ")" ::: "memory")
; #define PG8_WAIT_L(n) asm volatile("s_waitcnt lgkmcnt(" #n ")" ::: "memory")
; #define PG8_BAR __builtin_amdgcn_s_barrier()
; #define PG8_SCHED __builtin_amdgcn_sched_barrier(0)
; template <class Epi, class Sched, bool ALIGN_EPI = false, bool SP2 = false>
; __device__ __forceinline__ void gemm_phase(PG8_LAS unsigned char* lds, const Gemm g, const Sched& S, const Epi& E) {
;     ...
;             PG8_WAIT_V(8); PG8_WAIT_L(0); PG8_BAR; PG8_MMA(1, 0, At, B0); PG8_MMA(1, 1, At, B1); PG8_BAR; PG8_SCHED;
;             PG8_LDB(B0, 1, 0); PG8_LDB(B1, 1, 1); PG8_SCHED; PG8_LDA(At, 1, 0); PG8_STAGE(PG8_SA(0, 1), a2 + hstep, voffA);
;             PG8_WAIT_V(8); PG8_WAIT_L(0); PG8_BAR; PG8_MMA(0, 0, At, B0); PG8_MMA(0, 1, At, B1); PG8_BAR; PG8_SCHED;
	s_setprio 1
	s_waitcnt lgkmcnt(0)
	v_mfma_f32_16x16x32_bf16 v[62:65], v[148:151], v[194:197], 0
	v_mfma_f32_16x16x32_bf16 v[58:61], v[164:167], v[194:197], 0
	v_mfma_f32_16x16x32_bf16 v[54:57], v[148:151], v[202:205], 0
	v_mfma_f32_16x16x32_bf16 v[46:49], v[164:167], v[202:205], 0
	v_mfma_f32_16x16x32_bf16 v[38:41], v[148:151], v[216:219], 0
	v_mfma_f32_16x16x32_bf16 v[30:33], v[164:167], v[216:219], 0
	v_mfma_f32_16x16x32_bf16 v[22:25], v[148:151], v[224:227], 0
	v_mfma_f32_16x16x32_bf16 v[14:17], v[164:167], v[224:227], 0
	v_mfma_f32_16x16x32_bf16 v[62:65], v[160:163], v[198:201], v[62:65]
	v_mfma_f32_16x16x32_bf16 v[58:61], v[168:171], v[198:201], v[58:61]
	v_mfma_f32_16x16x32_bf16 v[54:57], v[160:163], v[206:209], v[54:57]
	v_mfma_f32_16x16x32_bf16 v[46:49], v[168:171], v[206:209], v[46:49]
	v_mfma_f32_16x16x32_bf16 v[38:41], v[160:163], v[220:223], v[38:41]
	v_mfma_f32_16x16x32_bf16 v[30:33], v[168:171], v[220:223], v[30:33]
	v_mfma_f32_16x16x32_bf16 v[22:25], v[160:163], v[228:231], v[22:25]
	v_mfma_f32_16x16x32_bf16 v[14:17], v[168:171], v[228:231], v[14:17]
	s_setprio 0
	s_setprio 1
	v_mfma_f32_16x16x32_bf16 v[50:53], v[172:175], v[194:197], 0
	v_mfma_f32_16x16x32_bf16 v[42:45], v[180:183], v[194:197], 0
	v_mfma_f32_16x16x32_bf16 v[34:37], v[172:175], v[202:205], 0
	v_mfma_f32_16x16x32_bf16 v[26:29], v[180:183], v[202:205], 0
	v_mfma_f32_16x16x32_bf16 v[18:21], v[172:175], v[216:219], 0
	v_mfma_f32_16x16x32_bf16 v[10:13], v[180:183], v[216:219], 0
	v_mfma_f32_16x16x32_bf16 v[6:9], v[172:175], v[224:227], 0
	v_mfma_f32_16x16x32_bf16 v[2:5], v[180:183], v[224:227], 0
	v_mfma_f32_16x16x32_bf16 v[50:53], v[176:179], v[198:201], v[50:53]
	v_mfma_f32_16x16x32_bf16 v[42:45], v[190:193], v[198:201], v[42:45]
	v_mfma_f32_16x16x32_bf16 v[34:37], v[176:179], v[206:209], v[34:37]
	v_mfma_f32_16x16x32_bf16 v[26:29], v[190:193], v[206:209], v[26:29]
	v_mfma_f32_16x16x32_bf16 v[18:21], v[176:179], v[220:223], v[18:21]
	v_mfma_f32_16x16x32_bf16 v[10:13], v[190:193], v[220:223], v[10:13]
	v_mfma_f32_16x16x32_bf16 v[6:9], v[176:179], v[228:231], v[6:9]
	v_mfma_f32_16x16x32_bf16 v[2:5], v[190:193], v[228:231], v[2:5]
	s_setprio 0
	s_barrier
	s_add_i32 s59, 0, 0x18000
	s_add_i32 s60, 0, 0x1c000
	ds_read_b128 v[148:151], v248
	ds_read_b128 v[160:163], v248 offset:1024
	ds_read_b128 v[164:167], v248 offset:2048
	ds_read_b128 v[168:171], v248 offset:3072
	ds_read_b128 v[172:175], v249
	ds_read_b128 v[176:179], v249 offset:1024
	ds_read_b128 v[180:183], v249 offset:2048
	ds_read_b128 v[190:193], v249 offset:3072
	s_add_u32 s36, s36, 0x80000
	s_addc_u32 s37, s37, 0
	s_mov_b32 m0, s44
	ds_read_b128 v[194:197], v159 offset:32768
	ds_read_b128 v[198:201], v159 offset:33792
	ds_read_b128 v[202:205], v159 offset:34816
	ds_read_b128 v[206:209], v159 offset:35840
	ds_read_b128 v[216:219], v159 offset:36864
	ds_read_b128 v[220:223], v159 offset:37888
	ds_read_b128 v[224:227], v159 offset:38912
	ds_read_b128 v[228:231], v159 offset:39936
	global_load_lds_dwordx4 v136, s[36:37]
	s_mov_b32 m0, s45
	s_nop 0
	global_load_lds_dwordx4 v132, s[36:37]
	s_waitcnt vmcnt(8)
	s_waitcnt lgkmcnt(0)
	s_barrier
	s_setprio 1
	s_waitcnt lgkmcnt(0)
	v_mfma_f32_16x16x32_bf16 v[126:129], v[148:151], v[194:197], v[126:129]
	v_mfma_f32_16x16x32_bf16 v[122:125], v[164:167], v[194:197], v[122:125]
	v_mfma_f32_16x16x32_bf16 v[118:121], v[148:151], v[202:205], v[118:121]
	v_mfma_f32_16x16x32_bf16 v[110:113], v[164:167], v[202:205], v[110:113]
	v_mfma_f32_16x16x32_bf16 v[102:105], v[148:151], v[216:219], v[102:105]
	v_mfma_f32_16x16x32_bf16 v[94:97], v[164:167], v[216:219], v[94:97]
	v_mfma_f32_16x16x32_bf16 v[86:89], v[148:151], v[224:227], v[86:89]
	v_mfma_f32_16x16x32_bf16 v[78:81], v[164:167], v[224:227], v[78:81]
	v_mfma_f32_16x16x32_bf16 v[126:129], v[160:163], v[198:201], v[126:129]
	v_mfma_f32_16x16x32_bf16 v[122:125], v[168:171], v[198:201], v[122:125]
	v_mfma_f32_16x16x32_bf16 v[118:121], v[160:163], v[206:209], v[118:121]
	v_mfma_f32_16x16x32_bf16 v[110:113], v[168:171], v[206:209], v[110:113]
	v_mfma_f32_16x16x32_bf16 v[102:105], v[160:163], v[220:223], v[102:105]
	v_mfma_f32_16x16x32_bf16 v[94:97], v[168:171], v[220:223], v[94:97]
	v_mfma_f32_16x16x32_bf16 v[86:89], v[160:163], v[228:231], v[86:89]
	v_mfma_f32_16x16x32_bf16 v[78:81], v[168:171], v[228:231], v[78:81]
	s_setprio 0
	s_setprio 1
	v_mfma_f32_16x16x32_bf16 v[114:117], v[172:175], v[194:197], v[114:117]
	v_mfma_f32_16x16x32_bf16 v[106:109], v[180:183], v[194:197], v[106:109]
	v_mfma_f32_16x16x32_bf16 v[98:101], v[172:175], v[202:205], v[98:101]
	v_mfma_f32_16x16x32_bf16 v[90:93], v[180:183], v[202:205], v[90:93]
	v_mfma_f32_16x16x32_bf16 v[82:85], v[172:175], v[216:219], v[82:85]
	v_mfma_f32_16x16x32_bf16 v[74:77], v[180:183], v[216:219], v[74:77]
	v_mfma_f32_16x16x32_bf16 v[70:73], v[172:175], v[224:227], v[70:73]
	v_mfma_f32_16x16x32_bf16 v[66:69], v[180:183], v[224:227], v[66:69]
	v_mfma_f32_16x16x32_bf16 v[114:117], v[176:179], v[198:201], v[114:117]
	v_mfma_f32_16x16x32_bf16 v[106:109], v[190:193], v[198:201], v[106:109]
	v_mfma_f32_16x16x32_bf16 v[98:101], v[176:179], v[206:209], v[98:101]
	v_mfma_f32_16x16x32_bf16 v[90:93], v[190:193], v[206:209], v[90:93]
	v_mfma_f32_16x16x32_bf16 v[82:85], v[176:179], v[220:223], v[82:85]
	v_mfma_f32_16x16x32_bf16 v[74:77], v[190:193], v[220:223], v[74:77]
	v_mfma_f32_16x16x32_bf16 v[70:73], v[176:179], v[228:231], v[70:73]
	v_mfma_f32_16x16x32_bf16 v[66:69], v[190:193], v[228:231], v[66:69]
	s_setprio 0
	s_barrier
; #define PG8_STAGE(bufoff, gbase, voff) do { _Pragma("unroll") for (int _i = 0; _i < 2; ++_i) \
;         __builtin_amdgcn_global_load_lds((const unsigned*)((const char*)(gbase) + (voff)[_i]), (PG8_LAS unsigned*)(lds + (bufoff) + ldsw + _i * 8192), 16, 0, 0); } while (0)
; #define PG8_LDA(dst, b, h) do { _Pragma("unroll") for (int m = 0; m < 4; ++m) _Pragma("unroll") for (int k = 0; k < 2; ++k) dst[m][k] = *(const PG8_LAS bf16x8*)(lds + PG8_SA(b, h) + aoff + m * 2048 + k * 1024); } while (0)
; #define PG8_LDB(dst, b, h) do { _Pragma("unroll") for (int n = 0; n < 2; ++n) _Pragma("unroll") for (int k = 0; k < 2; ++k) dst[n][k] = *(const PG8_LAS bf16x8*)(lds + PG8_SB(b, h) + boff + n * 2048 + k * 1024); } while (0)
; #define PG8_WAIT_V(n) asm volatile("s_waitcnt vmcnt(" #n ")" ::: "memory")
; #define PG8_WAIT_L(n) asm volatile("s_waitcnt lgkmcnt(" #n ")" ::: "memory")
; #define PG8_BAR __builtin_amdgcn_s_barrier()
; #define PG8_SCHED __builtin_amdgcn_sched_barrier(0)
; template <class Epi, class Sched, bool ALIGN_EPI = false, bool SP2 = false>
; __device__ __forceinline__ void gemm_phase(PG8_LAS unsigned char* lds, const Gemm g, const Sched& S, const Epi& E) {
;     ...
;         for (int t = 0; t < nt; t += 2) {
;     ...
;             PG8_LDB(B0, 1, 0); PG8_LDB(B1, 1, 1); PG8_SCHED; PG8_LDA(At, 1, 0); PG8_STAGE(PG8_SA(0, 1), a2 + hstep, voffA);
;             PG8_WAIT_V(8); PG8_WAIT_L(0); PG8_BAR; PG8_MMA(0, 0, At, B0); PG8_MMA(0, 1, At, B1); PG8_BAR; PG8_SCHED;
;             PG8_LDA(At, 1, 1); PG8_STAGE(PG8_SB(1, 0), b3, voffB); PG8_STAGE(PG8_SB(1, 1), b3 + hstep, voffB); PG8_STAGE(PG8_SA(1, 0), a3, voffA);
;             PG8_WAIT_V(8); PG8_WAIT_L(0); PG8_BAR; PG8_MMA(1, 0, At, B0); PG8_MMA(1, 1, At, B1); PG8_BAR; PG8_SCHED;
	s_add_u32 s98, s34, 0x80
	s_addc_u32 s99, s35, 0
	s_add_u32 s100, s36, 0xfff80080
	s_addc_u32 s101, s37, -1
	s_add_i32 s36, s59, s39
	s_mov_b32 m0, s36
	ds_read_b128 v[194:197], v159 offset:49152
	ds_read_b128 v[198:201], v159 offset:50176
	ds_read_b128 v[202:205], v159 offset:51200
	ds_read_b128 v[206:209], v159 offset:52224
	ds_read_b128 v[216:219], v159 offset:53248
	ds_read_b128 v[220:223], v159 offset:54272
	ds_read_b128 v[224:227], v159 offset:55296
	ds_read_b128 v[228:231], v159 offset:56320
	global_load_lds_dwordx4 v134, s[98:99]
	s_add_i32 m0, s36, 0x2000
	s_add_u32 s34, s34, 0x80080
	s_addc_u32 s35, s35, 0
	s_add_i32 s36, s60, s39
	global_load_lds_dwordx4 v130, s[98:99]
	s_mov_b32 m0, s36
	s_nop 0
	global_load_lds_dwordx4 v134, s[34:35]
	s_add_i32 m0, s36, 0x2000
	s_nop 0
	global_load_lds_dwordx4 v130, s[34:35]
	s_mov_b32 m0, s48
	s_nop 0
	global_load_lds_dwordx4 v136, s[100:101]
	s_mov_b32 m0, s49
	s_nop 0
	global_load_lds_dwordx4 v132, s[100:101]
	s_waitcnt vmcnt(8)
	s_waitcnt lgkmcnt(0)
	s_barrier
	s_setprio 1
	s_waitcnt lgkmcnt(0)
	v_mfma_f32_16x16x32_bf16 v[62:65], v[148:151], v[194:197], v[62:65]
	v_mfma_f32_16x16x32_bf16 v[58:61], v[164:167], v[194:197], v[58:61]
	v_mfma_f32_16x16x32_bf16 v[54:57], v[148:151], v[202:205], v[54:57]
	v_mfma_f32_16x16x32_bf16 v[46:49], v[164:167], v[202:205], v[46:49]
	v_mfma_f32_16x16x32_bf16 v[38:41], v[148:151], v[216:219], v[38:41]
	v_mfma_f32_16x16x32_bf16 v[30:33], v[164:167], v[216:219], v[30:33]
	v_mfma_f32_16x16x32_bf16 v[22:25], v[148:151], v[224:227], v[22:25]
	v_mfma_f32_16x16x32_bf16 v[14:17], v[164:167], v[224:227], v[14:17]
	v_mfma_f32_16x16x32_bf16 v[62:65], v[160:163], v[198:201], v[62:65]
	v_mfma_f32_16x16x32_bf16 v[58:61], v[168:171], v[198:201], v[58:61]
	v_mfma_f32_16x16x32_bf16 v[54:57], v[160:163], v[206:209], v[54:57]
	v_mfma_f32_16x16x32_bf16 v[46:49], v[168:171], v[206:209], v[46:49]
	v_mfma_f32_16x16x32_bf16 v[38:41], v[160:163], v[220:223], v[38:41]
	v_mfma_f32_16x16x32_bf16 v[30:33], v[168:171], v[220:223], v[30:33]
	v_mfma_f32_16x16x32_bf16 v[22:25], v[160:163], v[228:231], v[22:25]
	v_mfma_f32_16x16x32_bf16 v[14:17], v[168:171], v[228:231], v[14:17]
	s_setprio 0
	s_setprio 1
	v_mfma_f32_16x16x32_bf16 v[50:53], v[172:175], v[194:197], v[50:53]
	v_mfma_f32_16x16x32_bf16 v[42:45], v[180:183], v[194:197], v[42:45]
	v_mfma_f32_16x16x32_bf16 v[34:37], v[172:175], v[202:205], v[34:37]
	v_mfma_f32_16x16x32_bf16 v[26:29], v[180:183], v[202:205], v[26:29]
	v_mfma_f32_16x16x32_bf16 v[18:21], v[172:175], v[216:219], v[18:21]
	v_mfma_f32_16x16x32_bf16 v[10:13], v[180:183], v[216:219], v[10:13]
	v_mfma_f32_16x16x32_bf16 v[6:9], v[172:175], v[224:227], v[6:9]
	v_mfma_f32_16x16x32_bf16 v[2:5], v[180:183], v[224:227], v[2:5]
	v_mfma_f32_16x16x32_bf16 v[50:53], v[176:179], v[198:201], v[50:53]
	v_mfma_f32_16x16x32_bf16 v[42:45], v[190:193], v[198:201], v[42:45]
	v_mfma_f32_16x16x32_bf16 v[34:37], v[176:179], v[206:209], v[34:37]
	v_mfma_f32_16x16x32_bf16 v[26:29], v[190:193], v[206:209], v[26:29]
	v_mfma_f32_16x16x32_bf16 v[18:21], v[176:179], v[220:223], v[18:21]
	v_mfma_f32_16x16x32_bf16 v[10:13], v[190:193], v[220:223], v[10:13]
	v_mfma_f32_16x16x32_bf16 v[6:9], v[176:179], v[228:231], v[6:9]
	v_mfma_f32_16x16x32_bf16 v[2:5], v[190:193], v[228:231], v[2:5]
	s_setprio 0
	s_barrier
	s_add_i32 s58, s58, 2
	s_add_u32 s30, s30, 0x100
	s_addc_u32 s31, s31, 0
	s_add_u32 s56, s56, 0x100
	s_addc_u32 s57, s57, 0
	s_cmp_gt_u32 s58, 29

; #define PG8_STAGE(bufoff, gbase, voff) do { _Pragma("unroll") for (int _i = 0; _i < 2; ++_i) \
;         __builtin_amdgcn_global_load_lds((const unsigned*)((const char*)(gbase) + (voff)[_i]), (PG8_LAS unsigned*)(lds + (bufoff) + ldsw + _i * 8192), 16, 0, 0); } while (0)
; #define PG8_LDA(dst, b, h) do { _Pragma("unroll") for (int m = 0; m < 4; ++m) _Pragma("unroll") for (int k = 0; k < 2; ++k) dst[m][k] = *(const PG8_LAS bf16x8*)(lds + PG8_SA(b, h) + aoff + m * 2048 + k * 1024); } while (0)
; template <class Epi, class Sched, bool ALIGN_EPI = false, bool SP2 = false>
; __device__ __forceinline__ void gemm_phase(PG8_LAS unsigned char* lds, const Gemm g, const Sched& S, const Epi& E) {
;     ...
;         const bool has_next = S.next(ui + 1, nxt);
;         const char* nA = has_next ? (const char*)g.A + (size_t)nxt.pm * tstep : cA; const char* nB = has_next ? (const char*)g.Bt + (size_t)nxt.pn * tstep : cB;
;         for (int t = 0; t < nt; t += 2) {
;             const bool last = (t == nt - 2);
;             const char* a1 = cA + (size_t)(t + 1) * kstep;
;             const char* a2 = last ? nA : cA + (size_t)(t + 2) * kstep; const char* b2 = last ? nB : cB + (size_t)(t + 2) * kstep;
;             const char* a3 = a2 + kstep; const char* b3 = b2 + kstep;
;             if (last && has_next) S.a_ready(nxt);
;             if constexpr (SP2) {
;             PG8_LDB(B0, 0, 0); PG8_LDB(B1, 0, 1); PG8_SCHED; PG8_LDA(At, 0, 0); PG8_STAGE(PG8_SA(1, 1), a1 + hstep, voffA);
;             PG8_WAIT_V(8); PG8_WAIT_L(0); PG8_BAR; PG8_MMA(0, 0, At, B0); PG8_MMA(0, 1, At, B1); PG8_BAR; PG8_SCHED;
;             PG8_LDA(At, 0, 1); PG8_STAGE(PG8_SB(0, 0), b2, voffB); PG8_STAGE(PG8_SB(0, 1), b2 + hstep, voffB); PG8_STAGE(PG8_SA(0, 0), a2, voffA);
;             PG8_WAIT_V(8); PG8_WAIT_L(0); PG8_BAR; PG8_MMA(1, 0, At, B0); PG8_MMA(1, 1, At, B1); PG8_BAR; PG8_SCHED;
;             PG8_LDB(B0, 1, 0); PG8_LDB(B1, 1, 1); PG8_SCHED; PG8_LDA(At, 1, 0); PG8_STAGE(PG8_SA(0, 1), a2 + hstep, voffA);
;             PG8_WAIT_V(8); PG8_WAIT_L(0); PG8_BAR; PG8_MMA(0, 0, At, B0); PG8_MMA(0, 1, At, B1); PG8_BAR; PG8_SCHED;
;             PG8_LDA(At, 1, 1); PG8_STAGE(PG8_SB(1, 0), b3, voffB); PG8_STAGE(PG8_SB(1, 1), b3 + hstep, voffB); PG8_STAGE(PG8_SA(1, 0), a3, voffA);
;             PG8_WAIT_V(8); PG8_WAIT_L(0); PG8_BAR; PG8_MMA(1, 0, At, B0); PG8_MMA(1, 1, At, B1); PG8_BAR; PG8_SCHED;
.LBB0_1455:
	s_ashr_i32 s13, s12, 31
	s_lshl_b64 s[14:15], s[12:13], 20
	v_readlane_b32 s16, v247, 17
	v_readlane_b32 s17, v247, 18
	s_add_u32 s14, s16, s14
	s_addc_u32 s15, s17, s15
	s_and_b64 s[16:17], s[2:3], exec
	s_cselect_b32 s13, s15, s21
	s_cselect_b32 s50, s14, s20
	s_ashr_i32 s11, s10, 31
	s_lshl_b64 s[16:17], s[10:11], 20
	s_add_u32 s16, s27, s16
	s_addc_u32 s17, s28, s17
	s_and_b64 s[24:25], s[2:3], exec
	s_cselect_b32 s11, s17, s23
	s_cselect_b32 s51, s16, s22
	s_add_u32 s20, s20, 0x80080
	s_addc_u32 s21, s21, 0
	s_add_u32 s52, s22, 0x100
	s_addc_u32 s53, s23, 0
	s_mov_b32 s54, -2
	v_add_u32_e32 v248, 0x18000, v174
	v_add_u32_e32 v249, 0x1c000, v174
	ds_read_b128 v[130:133], v176
	ds_read_b128 v[134:137], v176 offset:1024
	ds_read_b128 v[138:141], v176 offset:2048
	ds_read_b128 v[142:145], v176 offset:3072
	ds_read_b128 v[146:149], v177
	ds_read_b128 v[150:153], v177 offset:1024
	ds_read_b128 v[170:173], v177 offset:2048
	ds_read_b128 v[180:183], v177 offset:3072
	s_add_u32 s22, s20, 0xfff80080
	s_addc_u32 s23, s21, -1
	s_cmp_eq_u32 s54, 28
	s_cselect_b32 s25, s13, s23
	s_cselect_b32 s24, s50, s22
	s_cselect_b32 s23, s11, s53
	s_cselect_b32 s22, s51, s52
	s_add_i32 m0, s19, 0xc000
	ds_read_b128 v[188:191], v178
	ds_read_b128 v[192:195], v178 offset:1024
	ds_read_b128 v[196:199], v178 offset:2048
	ds_read_b128 v[200:203], v178 offset:3072
	ds_read_b128 v[204:207], v178 offset:4096
	ds_read_b128 v[214:217], v178 offset:5120
	ds_read_b128 v[218:221], v178 offset:6144
	ds_read_b128 v[222:225], v178 offset:7168
	global_load_lds_dwordx4 v162, s[20:21]
	s_add_i32 m0, s19, 0xe000
	s_nop 0
	global_load_lds_dwordx4 v164, s[20:21]
	s_waitcnt vmcnt(8)
	s_waitcnt lgkmcnt(0)
	s_barrier
	s_setprio 1
	s_waitcnt lgkmcnt(0)
	v_mfma_f32_16x16x32_bf16 v[126:129], v[130:133], v[188:191], 0
	v_mfma_f32_16x16x32_bf16 v[122:125], v[138:141], v[188:191], 0
	v_mfma_f32_16x16x32_bf16 v[110:113], v[130:133], v[196:199], 0
	v_mfma_f32_16x16x32_bf16 v[106:109], v[138:141], v[196:199], 0
	v_mfma_f32_16x16x32_bf16 v[98:101], v[130:133], v[204:207], 0
	v_mfma_f32_16x16x32_bf16 v[90:93], v[138:141], v[204:207], 0
	v_mfma_f32_16x16x32_bf16 v[82:85], v[130:133], v[218:221], 0
	v_mfma_f32_16x16x32_bf16 v[74:77], v[138:141], v[218:221], 0
	v_mfma_f32_16x16x32_bf16 v[126:129], v[134:137], v[192:195], v[126:129]
	v_mfma_f32_16x16x32_bf16 v[122:125], v[142:145], v[192:195], v[122:125]
	v_mfma_f32_16x16x32_bf16 v[110:113], v[134:137], v[200:203], v[110:113]
	v_mfma_f32_16x16x32_bf16 v[106:109], v[142:145], v[200:203], v[106:109]
	v_mfma_f32_16x16x32_bf16 v[98:101], v[134:137], v[214:217], v[98:101]
	v_mfma_f32_16x16x32_bf16 v[90:93], v[142:145], v[214:217], v[90:93]
	v_mfma_f32_16x16x32_bf16 v[82:85], v[134:137], v[222:225], v[82:85]
	v_mfma_f32_16x16x32_bf16 v[74:77], v[142:145], v[222:225], v[74:77]
	s_setprio 0
	s_setprio 1
	v_mfma_f32_16x16x32_bf16 v[118:121], v[146:149], v[188:191], 0
	v_mfma_f32_16x16x32_bf16 v[114:117], v[170:173], v[188:191], 0
	v_mfma_f32_16x16x32_bf16 v[102:105], v[146:149], v[196:199], 0
	v_mfma_f32_16x16x32_bf16 v[94:97], v[170:173], v[196:199], 0
	v_mfma_f32_16x16x32_bf16 v[86:89], v[146:149], v[204:207], 0
	v_mfma_f32_16x16x32_bf16 v[78:81], v[170:173], v[204:207], 0
	v_mfma_f32_16x16x32_bf16 v[70:73], v[146:149], v[218:221], 0
	v_mfma_f32_16x16x32_bf16 v[66:69], v[170:173], v[218:221], 0
	v_mfma_f32_16x16x32_bf16 v[118:121], v[150:153], v[192:195], v[118:121]
	v_mfma_f32_16x16x32_bf16 v[114:117], v[180:183], v[192:195], v[114:117]
	v_mfma_f32_16x16x32_bf16 v[102:105], v[150:153], v[200:203], v[102:105]
	v_mfma_f32_16x16x32_bf16 v[94:97], v[180:183], v[200:203], v[94:97]
	v_mfma_f32_16x16x32_bf16 v[86:89], v[150:153], v[214:217], v[86:89]
	v_mfma_f32_16x16x32_bf16 v[78:81], v[180:183], v[214:217], v[78:81]
	v_mfma_f32_16x16x32_bf16 v[70:73], v[150:153], v[222:225], v[70:73]
	v_mfma_f32_16x16x32_bf16 v[66:69], v[180:183], v[222:225], v[66:69]
	s_setprio 0
	s_barrier
	s_add_i32 s55, s42, s29
	s_mov_b32 m0, s55
	ds_read_b128 v[188:191], v178 offset:16384
	ds_read_b128 v[192:195], v178 offset:17408
	ds_read_b128 v[196:199], v178 offset:18432
	ds_read_b128 v[200:203], v178 offset:19456
	ds_read_b128 v[204:207], v178 offset:20480
	ds_read_b128 v[214:217], v178 offset:21504
	ds_read_b128 v[218:221], v178 offset:22528
	ds_read_b128 v[222:225], v178 offset:23552
	global_load_lds_dwordx4 v156, s[22:23]
	s_add_i32 m0, s55, 0x2000
	s_add_u32 s56, s22, 0x80000
	s_addc_u32 s57, s23, 0
	s_add_i32 s55, s43, s29
	global_load_lds_dwordx4 v160, s[22:23]
	s_mov_b32 m0, s55
	s_nop 0
	global_load_lds_dwordx4 v156, s[56:57]
	s_add_i32 m0, s55, 0x2000
	s_nop 0
	global_load_lds_dwordx4 v160, s[56:57]
	s_mov_b32 m0, s19
	s_nop 0
	global_load_lds_dwordx4 v154, s[24:25]
	s_mov_b32 m0, s30
	s_nop 0
	global_load_lds_dwordx4 v158, s[24:25]
	s_waitcnt vmcnt(8)
	s_waitcnt lgkmcnt(0)
	s_barrier
; #define PG8_STAGE(bufoff, gbase, voff) do { _Pragma("unroll") for (int _i = 0; _i < 2; ++_i) \
;         __builtin_amdgcn_global_load_lds((const unsigned*)((const char*)(gbase) + (voff)[_i]), (PG8_LAS unsigned*)(lds + (bufoff) + ldsw + _i * 8192), 16, 0, 0); } while (0)
; #define PG8_LDA(dst, b, h) do { _Pragma("unroll") for (int m = 0; m < 4; ++m) _Pragma("unroll") for (int k = 0; k < 2; ++k) dst[m][k] = *(const PG8_LAS bf16x8*)(lds + PG8_SA(b, h) + aoff + m * 2048 + k * 1024); } while (0)
; #define PG8_LDB(dst, b, h) do { _Pragma("unroll") for (int n = 0; n < 2; ++n) _Pragma("unroll") for (int k = 0; k < 2; ++k) dst[n][k] = *(const PG8_LAS bf16x8*)(lds + PG8_SB(b, h) + boff + n * 2048 + k * 1024); } while (0)
; #define PG8_WAIT_V(n) asm volatile("s_waitcnt vmcnt(" #n ")" ::: "memory")
; #define PG8_WAIT_L(n) asm volatile("s_waitcnt lgkmcnt(" #n ")" ::: "memory")
; #define PG8_BAR __builtin_amdgcn_s_barrier()
; #define PG8_SCHED __builtin_amdgcn_sched_barrier(0)
; template <class Epi, class Sched, bool ALIGN_EPI = false, bool SP2 = false>
; __device__ __forceinline__ void gemm_phase(PG8_LAS unsigned char* lds, const Gemm g, const Sched& S, const Epi& E) {
;     ...
;             PG8_WAIT_V(8); PG8_WAIT_L(0); PG8_BAR; PG8_MMA(1, 0, At, B0); PG8_MMA(1, 1, At, B1); PG8_BAR; PG8_SCHED;
;             PG8_LDB(B0, 1, 0); PG8_LDB(B1, 1, 1); PG8_SCHED; PG8_LDA(At, 1, 0); PG8_STAGE(PG8_SA(0, 1), a2 + hstep, voffA);
;             PG8_WAIT_V(8); PG8_WAIT_L(0); PG8_BAR; PG8_MMA(0, 0, At, B0); PG8_MMA(0, 1, At, B1); PG8_BAR; PG8_SCHED;
	s_setprio 1
	s_waitcnt lgkmcnt(0)
	v_mfma_f32_16x16x32_bf16 v[62:65], v[130:133], v[188:191], 0
	v_mfma_f32_16x16x32_bf16 v[58:61], v[138:141], v[188:191], 0
	v_mfma_f32_16x16x32_bf16 v[50:53], v[130:133], v[196:199], 0
	v_mfma_f32_16x16x32_bf16 v[42:45], v[138:141], v[196:199], 0
	v_mfma_f32_16x16x32_bf16 v[34:37], v[130:133], v[204:207], 0
	v_mfma_f32_16x16x32_bf16 v[26:29], v[138:141], v[204:207], 0
	v_mfma_f32_16x16x32_bf16 v[18:21], v[130:133], v[218:221], 0
	v_mfma_f32_16x16x32_bf16 v[10:13], v[138:141], v[218:221], 0
	v_mfma_f32_16x16x32_bf16 v[62:65], v[134:137], v[192:195], v[62:65]
	v_mfma_f32_16x16x32_bf16 v[58:61], v[142:145], v[192:195], v[58:61]
	v_mfma_f32_16x16x32_bf16 v[50:53], v[134:137], v[200:203], v[50:53]
	v_mfma_f32_16x16x32_bf16 v[42:45], v[142:145], v[200:203], v[42:45]
	v_mfma_f32_16x16x32_bf16 v[34:37], v[134:137], v[214:217], v[34:37]
	v_mfma_f32_16x16x32_bf16 v[26:29], v[142:145], v[214:217], v[26:29]
	v_mfma_f32_16x16x32_bf16 v[18:21], v[134:137], v[222:225], v[18:21]
	v_mfma_f32_16x16x32_bf16 v[10:13], v[142:145], v[222:225], v[10:13]
	s_setprio 0
	s_setprio 1
	v_mfma_f32_16x16x32_bf16 v[54:57], v[146:149], v[188:191], 0
	v_mfma_f32_16x16x32_bf16 v[46:49], v[170:173], v[188:191], 0
	v_mfma_f32_16x16x32_bf16 v[38:41], v[146:149], v[196:199], 0
	v_mfma_f32_16x16x32_bf16 v[30:33], v[170:173], v[196:199], 0
	v_mfma_f32_16x16x32_bf16 v[22:25], v[146:149], v[204:207], 0
	v_mfma_f32_16x16x32_bf16 v[14:17], v[170:173], v[204:207], 0
	v_mfma_f32_16x16x32_bf16 v[6:9], v[146:149], v[218:221], 0
	v_mfma_f32_16x16x32_bf16 v[2:5], v[170:173], v[218:221], 0
	v_mfma_f32_16x16x32_bf16 v[54:57], v[150:153], v[192:195], v[54:57]
	v_mfma_f32_16x16x32_bf16 v[46:49], v[180:183], v[192:195], v[46:49]
	v_mfma_f32_16x16x32_bf16 v[38:41], v[150:153], v[200:203], v[38:41]
	v_mfma_f32_16x16x32_bf16 v[30:33], v[180:183], v[200:203], v[30:33]
	v_mfma_f32_16x16x32_bf16 v[22:25], v[150:153], v[214:217], v[22:25]
	v_mfma_f32_16x16x32_bf16 v[14:17], v[180:183], v[214:217], v[14:17]
	v_mfma_f32_16x16x32_bf16 v[6:9], v[150:153], v[222:225], v[6:9]
	v_mfma_f32_16x16x32_bf16 v[2:5], v[180:183], v[222:225], v[2:5]
	s_setprio 0
	s_barrier
	s_add_i32 s55, 0, 0x18000
	s_add_i32 s56, 0, 0x1c000
	ds_read_b128 v[130:133], v248
	ds_read_b128 v[134:137], v248 offset:1024
	ds_read_b128 v[138:141], v248 offset:2048
	ds_read_b128 v[142:145], v248 offset:3072
	ds_read_b128 v[146:149], v249
	ds_read_b128 v[150:153], v249 offset:1024
	ds_read_b128 v[170:173], v249 offset:2048
	ds_read_b128 v[180:183], v249 offset:3072
	s_add_u32 s24, s24, 0x80000
	s_addc_u32 s25, s25, 0
	s_mov_b32 m0, s31
	ds_read_b128 v[188:191], v178 offset:32768
	ds_read_b128 v[192:195], v178 offset:33792
	ds_read_b128 v[196:199], v178 offset:34816
	ds_read_b128 v[200:203], v178 offset:35840
	ds_read_b128 v[204:207], v178 offset:36864
	ds_read_b128 v[214:217], v178 offset:37888
	ds_read_b128 v[218:221], v178 offset:38912
	ds_read_b128 v[222:225], v178 offset:39936
	global_load_lds_dwordx4 v154, s[24:25]
	s_mov_b32 m0, s33
	s_nop 0
	global_load_lds_dwordx4 v158, s[24:25]
	s_waitcnt vmcnt(8)
	s_waitcnt lgkmcnt(0)
	s_barrier
	s_setprio 1
	s_waitcnt lgkmcnt(0)
	v_mfma_f32_16x16x32_bf16 v[126:129], v[130:133], v[188:191], v[126:129]
	v_mfma_f32_16x16x32_bf16 v[122:125], v[138:141], v[188:191], v[122:125]
	v_mfma_f32_16x16x32_bf16 v[110:113], v[130:133], v[196:199], v[110:113]
	v_mfma_f32_16x16x32_bf16 v[106:109], v[138:141], v[196:199], v[106:109]
	v_mfma_f32_16x16x32_bf16 v[98:101], v[130:133], v[204:207], v[98:101]
	v_mfma_f32_16x16x32_bf16 v[90:93], v[138:141], v[204:207], v[90:93]
	v_mfma_f32_16x16x32_bf16 v[82:85], v[130:133], v[218:221], v[82:85]
	v_mfma_f32_16x16x32_bf16 v[74:77], v[138:141], v[218:221], v[74:77]
	v_mfma_f32_16x16x32_bf16 v[126:129], v[134:137], v[192:195], v[126:129]
	v_mfma_f32_16x16x32_bf16 v[122:125], v[142:145], v[192:195], v[122:125]
	v_mfma_f32_16x16x32_bf16 v[110:113], v[134:137], v[200:203], v[110:113]
	v_mfma_f32_16x16x32_bf16 v[106:109], v[142:145], v[200:203], v[106:109]
	v_mfma_f32_16x16x32_bf16 v[98:101], v[134:137], v[214:217], v[98:101]
	v_mfma_f32_16x16x32_bf16 v[90:93], v[142:145], v[214:217], v[90:93]
	v_mfma_f32_16x16x32_bf16 v[82:85], v[134:137], v[222:225], v[82:85]
	v_mfma_f32_16x16x32_bf16 v[74:77], v[142:145], v[222:225], v[74:77]
	s_setprio 0
	s_setprio 1
	v_mfma_f32_16x16x32_bf16 v[118:121], v[146:149], v[188:191], v[118:121]
	v_mfma_f32_16x16x32_bf16 v[114:117], v[170:173], v[188:191], v[114:117]
	v_mfma_f32_16x16x32_bf16 v[102:105], v[146:149], v[196:199], v[102:105]
	v_mfma_f32_16x16x32_bf16 v[94:97], v[170:173], v[196:199], v[94:97]
	v_mfma_f32_16x16x32_bf16 v[86:89], v[146:149], v[204:207], v[86:89]
	v_mfma_f32_16x16x32_bf16 v[78:81], v[170:173], v[204:207], v[78:81]
	v_mfma_f32_16x16x32_bf16 v[70:73], v[146:149], v[218:221], v[70:73]
	v_mfma_f32_16x16x32_bf16 v[66:69], v[170:173], v[218:221], v[66:69]
	v_mfma_f32_16x16x32_bf16 v[118:121], v[150:153], v[192:195], v[118:121]
	v_mfma_f32_16x16x32_bf16 v[114:117], v[180:183], v[192:195], v[114:117]
	v_mfma_f32_16x16x32_bf16 v[102:105], v[150:153], v[200:203], v[102:105]
	v_mfma_f32_16x16x32_bf16 v[94:97], v[180:183], v[200:203], v[94:97]
	v_mfma_f32_16x16x32_bf16 v[86:89], v[150:153], v[214:217], v[86:89]
	v_mfma_f32_16x16x32_bf16 v[78:81], v[180:183], v[214:217], v[78:81]
	v_mfma_f32_16x16x32_bf16 v[70:73], v[150:153], v[222:225], v[70:73]
	v_mfma_f32_16x16x32_bf16 v[66:69], v[180:183], v[222:225], v[66:69]
	s_setprio 0
	s_barrier
; #define PG8_STAGE(bufoff, gbase, voff) do { _Pragma("unroll") for (int _i = 0; _i < 2; ++_i) \
;         __builtin_amdgcn_global_load_lds((const unsigned*)((const char*)(gbase) + (voff)[_i]), (PG8_LAS unsigned*)(lds + (bufoff) + ldsw + _i * 8192), 16, 0, 0); } while (0)
; #define PG8_LDA(dst, b, h) do { _Pragma("unroll") for (int m = 0; m < 4; ++m) _Pragma("unroll") for (int k = 0; k < 2; ++k) dst[m][k] = *(const PG8_LAS bf16x8*)(lds + PG8_SA(b, h) + aoff + m * 2048 + k * 1024); } while (0)
; #define PG8_LDB(dst, b, h) do { _Pragma("unroll") for (int n = 0; n < 2; ++n) _Pragma("unroll") for (int k = 0; k < 2; ++k) dst[n][k] = *(const PG8_LAS bf16x8*)(lds + PG8_SB(b, h) + boff + n * 2048 + k * 1024); } while (0)
; #define PG8_WAIT_V(n) asm volatile("s_waitcnt vmcnt(" #n ")" ::: "memory")
; #define PG8_WAIT_L(n) asm volatile("s_waitcnt lgkmcnt(" #n ")" ::: "memory")
; #define PG8_BAR __builtin_amdgcn_s_barrier()
; #define PG8_SCHED __builtin_amdgcn_sched_barrier(0)
; template <class Epi, class Sched, bool ALIGN_EPI = false, bool SP2 = false>
; __device__ __forceinline__ void gemm_phase(PG8_LAS unsigned char* lds, const Gemm g, const Sched& S, const Epi& E) {
;     ...
;         for (int t = 0; t < nt; t += 2) {
;     ...
;             PG8_LDB(B0, 1, 0); PG8_LDB(B1, 1, 1); PG8_SCHED; PG8_LDA(At, 1, 0); PG8_STAGE(PG8_SA(0, 1), a2 + hstep, voffA);
;             PG8_WAIT_V(8); PG8_WAIT_L(0); PG8_BAR; PG8_MMA(0, 0, At, B0); PG8_MMA(0, 1, At, B1); PG8_BAR; PG8_SCHED;
;             PG8_LDA(At, 1, 1); PG8_STAGE(PG8_SB(1, 0), b3, voffB); PG8_STAGE(PG8_SB(1, 1), b3 + hstep, voffB); PG8_STAGE(PG8_SA(1, 0), a3, voffA);
;             PG8_WAIT_V(8); PG8_WAIT_L(0); PG8_BAR; PG8_MMA(1, 0, At, B0); PG8_MMA(1, 1, At, B1); PG8_BAR; PG8_SCHED;
	s_add_u32 s98, s22, 0x80
	s_addc_u32 s99, s23, 0
	s_add_u32 s100, s24, 0xfff80080
	s_addc_u32 s101, s25, -1
	s_add_i32 s24, s55, s29
	s_mov_b32 m0, s24
	ds_read_b128 v[188:191], v178 offset:49152
	ds_read_b128 v[192:195], v178 offset:50176
	ds_read_b128 v[196:199], v178 offset:51200
	ds_read_b128 v[200:203], v178 offset:52224
	ds_read_b128 v[204:207], v178 offset:53248
	ds_read_b128 v[214:217], v178 offset:54272
	ds_read_b128 v[218:221], v178 offset:55296
	ds_read_b128 v[222:225], v178 offset:56320
	global_load_lds_dwordx4 v156, s[98:99]
	s_add_i32 m0, s24, 0x2000
	s_add_u32 s22, s22, 0x80080
	s_addc_u32 s23, s23, 0
	s_add_i32 s24, s56, s29
	global_load_lds_dwordx4 v160, s[98:99]
	s_mov_b32 m0, s24
	s_nop 0
	global_load_lds_dwordx4 v156, s[22:23]
	s_add_i32 m0, s24, 0x2000
	s_nop 0
	global_load_lds_dwordx4 v160, s[22:23]
	s_mov_b32 m0, s38
	s_nop 0
	global_load_lds_dwordx4 v154, s[100:101]
	s_mov_b32 m0, s39
	s_nop 0
	global_load_lds_dwordx4 v158, s[100:101]
	s_waitcnt vmcnt(8)
	s_waitcnt lgkmcnt(0)
	s_barrier
	s_setprio 1
	s_waitcnt lgkmcnt(0)
	v_mfma_f32_16x16x32_bf16 v[62:65], v[130:133], v[188:191], v[62:65]
	v_mfma_f32_16x16x32_bf16 v[58:61], v[138:141], v[188:191], v[58:61]
	v_mfma_f32_16x16x32_bf16 v[50:53], v[130:133], v[196:199], v[50:53]
	v_mfma_f32_16x16x32_bf16 v[42:45], v[138:141], v[196:199], v[42:45]
	v_mfma_f32_16x16x32_bf16 v[34:37], v[130:133], v[204:207], v[34:37]
	v_mfma_f32_16x16x32_bf16 v[26:29], v[138:141], v[204:207], v[26:29]
	v_mfma_f32_16x16x32_bf16 v[18:21], v[130:133], v[218:221], v[18:21]
	v_mfma_f32_16x16x32_bf16 v[10:13], v[138:141], v[218:221], v[10:13]
	v_mfma_f32_16x16x32_bf16 v[62:65], v[134:137], v[192:195], v[62:65]
	v_mfma_f32_16x16x32_bf16 v[58:61], v[142:145], v[192:195], v[58:61]
	v_mfma_f32_16x16x32_bf16 v[50:53], v[134:137], v[200:203], v[50:53]
	v_mfma_f32_16x16x32_bf16 v[42:45], v[142:145], v[200:203], v[42:45]
	v_mfma_f32_16x16x32_bf16 v[34:37], v[134:137], v[214:217], v[34:37]
	v_mfma_f32_16x16x32_bf16 v[26:29], v[142:145], v[214:217], v[26:29]
	v_mfma_f32_16x16x32_bf16 v[18:21], v[134:137], v[222:225], v[18:21]
	v_mfma_f32_16x16x32_bf16 v[10:13], v[142:145], v[222:225], v[10:13]
	s_setprio 0
	s_setprio 1
	v_mfma_f32_16x16x32_bf16 v[54:57], v[146:149], v[188:191], v[54:57]
	v_mfma_f32_16x16x32_bf16 v[46:49], v[170:173], v[188:191], v[46:49]
	v_mfma_f32_16x16x32_bf16 v[38:41], v[146:149], v[196:199], v[38:41]
	v_mfma_f32_16x16x32_bf16 v[30:33], v[170:173], v[196:199], v[30:33]
	v_mfma_f32_16x16x32_bf16 v[22:25], v[146:149], v[204:207], v[22:25]
	v_mfma_f32_16x16x32_bf16 v[14:17], v[170:173], v[204:207], v[14:17]
	v_mfma_f32_16x16x32_bf16 v[6:9], v[146:149], v[218:221], v[6:9]
	v_mfma_f32_16x16x32_bf16 v[2:5], v[170:173], v[218:221], v[2:5]
	v_mfma_f32_16x16x32_bf16 v[54:57], v[150:153], v[192:195], v[54:57]
	v_mfma_f32_16x16x32_bf16 v[46:49], v[180:183], v[192:195], v[46:49]
	v_mfma_f32_16x16x32_bf16 v[38:41], v[150:153], v[200:203], v[38:41]
	v_mfma_f32_16x16x32_bf16 v[30:33], v[180:183], v[200:203], v[30:33]
	v_mfma_f32_16x16x32_bf16 v[22:25], v[150:153], v[214:217], v[22:25]
	v_mfma_f32_16x16x32_bf16 v[14:17], v[180:183], v[214:217], v[14:17]
	v_mfma_f32_16x16x32_bf16 v[6:9], v[150:153], v[222:225], v[6:9]
	v_mfma_f32_16x16x32_bf16 v[2:5], v[180:183], v[222:225], v[2:5]
	s_setprio 0
	s_barrier
	s_add_i32 s54, s54, 2
	s_add_u32 s20, s20, 0x100
	s_addc_u32 s21, s21, 0
	s_add_u32 s52, s52, 0x100
	s_addc_u32 s53, s53, 0
	s_cmp_gt_u32 s54, 29

; #define PG8_STAGE(bufoff, gbase, voff) do { _Pragma("unroll") for (int _i = 0; _i < 2; ++_i) \
;         __builtin_amdgcn_global_load_lds((const unsigned*)((const char*)(gbase) + (voff)[_i]), (PG8_LAS unsigned*)(lds + (bufoff) + ldsw + _i * 8192), 16, 0, 0); } while (0)
; #define PG8_LDA(dst, b, h) do { _Pragma("unroll") for (int m = 0; m < 4; ++m) _Pragma("unroll") for (int k = 0; k < 2; ++k) dst[m][k] = *(const PG8_LAS bf16x8*)(lds + PG8_SA(b, h) + aoff + m * 2048 + k * 1024); } while (0)
; #define PG8_BAR __builtin_amdgcn_s_barrier()
; template <class Epi, class Sched, bool ALIGN_EPI = false, bool SP2 = false>
; __device__ __forceinline__ void gemm_phase(PG8_LAS unsigned char* lds, const Gemm g, const Sched& S, const Epi& E) {
;     ...
;         const char* nA = has_next ? (const char*)g.A + (size_t)nxt.pm * tstep : cA; const char* nB = has_next ? (const char*)g.Bt + (size_t)nxt.pn * tstep : cB;
;         for (int t = 0; t < nt; t += 2) {
;             const bool last = (t == nt - 2);
;             const char* a1 = cA + (size_t)(t + 1) * kstep;
;             const char* a2 = last ? nA : cA + (size_t)(t + 2) * kstep; const char* b2 = last ? nB : cB + (size_t)(t + 2) * kstep;
;             const char* a3 = a2 + kstep; const char* b3 = b2 + kstep;
;             if (last && has_next) S.a_ready(nxt);
;             if constexpr (SP2) {
;             PG8_LDB(B0, 0, 0); PG8_LDB(B1, 0, 1); PG8_SCHED; PG8_LDA(At, 0, 0); PG8_STAGE(PG8_SA(1, 1), a1 + hstep, voffA);
;             PG8_WAIT_V(8); PG8_WAIT_L(0); PG8_BAR; PG8_MMA(0, 0, At, B0); PG8_MMA(0, 1, At, B1); PG8_BAR; PG8_SCHED;
;             PG8_LDA(At, 0, 1); PG8_STAGE(PG8_SB(0, 0), b2, voffB); PG8_STAGE(PG8_SB(0, 1), b2 + hstep, voffB); PG8_STAGE(PG8_SA(0, 0), a2, voffA);
;             PG8_WAIT_V(8); PG8_WAIT_L(0); PG8_BAR; PG8_MMA(1, 0, At, B0); PG8_MMA(1, 1, At, B1); PG8_BAR; PG8_SCHED;
;             PG8_LDB(B0, 1, 0); PG8_LDB(B1, 1, 1); PG8_SCHED; PG8_LDA(At, 1, 0); PG8_STAGE(PG8_SA(0, 1), a2 + hstep, voffA);
;             PG8_WAIT_V(8); PG8_WAIT_L(0); PG8_BAR; PG8_MMA(0, 0, At, B0); PG8_MMA(0, 1, At, B1); PG8_BAR; PG8_SCHED;
;             PG8_LDA(At, 1, 1); PG8_STAGE(PG8_SB(1, 0), b3, voffB); PG8_STAGE(PG8_SB(1, 1), b3 + hstep, voffB); PG8_STAGE(PG8_SA(1, 0), a3, voffA);
;             PG8_WAIT_V(8); PG8_WAIT_L(0); PG8_BAR; PG8_MMA(1, 0, At, B0); PG8_MMA(1, 1, At, B1); PG8_BAR; PG8_SCHED;
.LBB0_1882:
	s_ashr_i32 s15, s14, 31
	s_lshl_b64 s[18:19], s[14:15], 19
	s_add_u32 s18, s8, s18
	s_addc_u32 s19, s9, s19
	s_and_b64 s[20:21], s[0:1], exec
	s_cselect_b32 s15, s19, s27
	s_cselect_b32 s49, s18, s26
	s_ashr_i32 s17, s16, 31
	s_lshl_b64 s[20:21], s[16:17], 19
	s_add_u32 s20, s33, s20
	s_addc_u32 s21, s34, s21
	s_and_b64 s[30:31], s[0:1], exec
	s_cselect_b32 s17, s21, s29
	s_cselect_b32 s50, s20, s28
	s_add_u32 s26, s26, 0x40080
	s_addc_u32 s27, s27, 0
	s_add_u32 s51, s28, 0x100
	s_addc_u32 s52, s29, 0
	s_mov_b32 s53, -2
	v_add_u32_e32 v248, 0x18000, v188
	v_add_u32_e32 v249, 0x1c000, v188
	ds_read_b128 v[26:29], v190
	ds_read_b128 v[30:33], v190 offset:1024
	ds_read_b128 v[18:21], v190 offset:2048
	ds_read_b128 v[22:25], v190 offset:3072
	ds_read_b128 v[10:13], v191
	ds_read_b128 v[14:17], v191 offset:1024
	ds_read_b128 v[2:5], v191 offset:2048
	ds_read_b128 v[6:9], v191 offset:3072
	s_add_u32 s28, s26, 0xfffc0080
	s_addc_u32 s29, s27, -1
	s_cmp_eq_u32 s53, 12
	s_cselect_b32 s31, s15, s29
	s_cselect_b32 s30, s49, s28
	s_cselect_b32 s29, s17, s52
	s_cselect_b32 s28, s50, s51
	s_add_i32 m0, s23, 0xc000
	ds_read_b128 v[176:179], v192
	ds_read_b128 v[180:183], v192 offset:1024
	ds_read_b128 v[194:197], v192 offset:2048
	ds_read_b128 v[198:201], v192 offset:3072
	ds_read_b128 v[202:205], v192 offset:4096
	ds_read_b128 v[206:209], v192 offset:5120
	ds_read_b128 v[214:217], v192 offset:6144
	ds_read_b128 v[218:221], v192 offset:7168
	global_load_lds_dwordx4 v170, s[26:27]
	s_add_i32 m0, s23, 0xe000
	s_nop 0
	global_load_lds_dwordx4 v172, s[26:27]
	s_waitcnt vmcnt(8)
	s_waitcnt lgkmcnt(0)
	s_barrier
	s_setprio 1
	s_waitcnt lgkmcnt(0)
	v_mfma_scale_f32_16x16x128_f8f6f4 v[158:161], v[26:33], v[176:183], 0, v1, v184 op_sel_hi:[0,0,0]
	v_mfma_scale_f32_16x16x128_f8f6f4 v[154:157], v[18:25], v[176:183], 0, v1, v184 op_sel_hi:[0,0,0]
	v_mfma_scale_f32_16x16x128_f8f6f4 v[142:145], v[26:33], v[194:201], 0, v1, v184 op_sel_hi:[0,0,0]
	v_mfma_scale_f32_16x16x128_f8f6f4 v[138:141], v[18:25], v[194:201], 0, v1, v184 op_sel_hi:[0,0,0]
	v_mfma_scale_f32_16x16x128_f8f6f4 v[126:129], v[26:33], v[202:209], 0, v1, v184 op_sel_hi:[0,0,0]
	v_mfma_scale_f32_16x16x128_f8f6f4 v[122:125], v[18:25], v[202:209], 0, v1, v184 op_sel_hi:[0,0,0]
	v_mfma_scale_f32_16x16x128_f8f6f4 v[110:113], v[26:33], v[214:221], 0, v1, v184 op_sel_hi:[0,0,0]
	v_mfma_scale_f32_16x16x128_f8f6f4 v[106:109], v[18:25], v[214:221], 0, v1, v184 op_sel_hi:[0,0,0]
	s_setprio 0
	s_setprio 1
	v_mfma_scale_f32_16x16x128_f8f6f4 v[150:153], v[10:17], v[176:183], 0, v1, v184 op_sel_hi:[0,0,0]
	v_mfma_scale_f32_16x16x128_f8f6f4 v[146:149], v[2:9], v[176:183], 0, v1, v184 op_sel_hi:[0,0,0]
	v_mfma_scale_f32_16x16x128_f8f6f4 v[134:137], v[10:17], v[194:201], 0, v1, v184 op_sel_hi:[0,0,0]
	v_mfma_scale_f32_16x16x128_f8f6f4 v[130:133], v[2:9], v[194:201], 0, v1, v184 op_sel_hi:[0,0,0]
	v_mfma_scale_f32_16x16x128_f8f6f4 v[118:121], v[10:17], v[202:209], 0, v1, v184 op_sel_hi:[0,0,0]
	v_mfma_scale_f32_16x16x128_f8f6f4 v[114:117], v[2:9], v[202:209], 0, v1, v184 op_sel_hi:[0,0,0]
	v_mfma_scale_f32_16x16x128_f8f6f4 v[102:105], v[10:17], v[214:221], 0, v1, v184 op_sel_hi:[0,0,0]
	v_mfma_scale_f32_16x16x128_f8f6f4 v[98:101], v[2:9], v[214:221], 0, v1, v184 op_sel_hi:[0,0,0]
	s_setprio 0
	s_barrier
	s_add_i32 s54, s45, s35
	s_mov_b32 m0, s54
	ds_read_b128 v[194:197], v192 offset:16384
	ds_read_b128 v[198:201], v192 offset:17408
	ds_read_b128 v[202:205], v192 offset:18432
	ds_read_b128 v[206:209], v192 offset:19456
	ds_read_b128 v[214:217], v192 offset:20480
	ds_read_b128 v[218:221], v192 offset:21504
	ds_read_b128 v[222:225], v192 offset:22528
	ds_read_b128 v[226:229], v192 offset:23552
	global_load_lds_dwordx4 v166, s[28:29]
	s_add_i32 m0, s54, 0x2000
	s_add_u32 s54, s28, 0x40000
	s_addc_u32 s55, s29, 0
	s_add_i32 s56, s46, s35
	global_load_lds_dwordx4 v162, s[28:29]
	s_mov_b32 m0, s56
	s_nop 0
	global_load_lds_dwordx4 v166, s[54:55]
	s_add_i32 m0, s56, 0x2000
	s_nop 0
	global_load_lds_dwordx4 v162, s[54:55]
	s_mov_b32 m0, s23
	s_nop 0
	global_load_lds_dwordx4 v168, s[30:31]
	s_mov_b32 m0, s25
	s_nop 0
	global_load_lds_dwordx4 v164, s[30:31]
	s_waitcnt vmcnt(8)
	s_waitcnt lgkmcnt(0)
	s_barrier
	s_setprio 1
	s_waitcnt lgkmcnt(0)
	v_mfma_scale_f32_16x16x128_f8f6f4 v[94:97], v[26:33], v[194:201], 0, v1, v184 op_sel_hi:[0,0,0]
	v_mfma_scale_f32_16x16x128_f8f6f4 v[90:93], v[18:25], v[194:201], 0, v1, v184 op_sel_hi:[0,0,0]
	v_mfma_scale_f32_16x16x128_f8f6f4 v[78:81], v[26:33], v[202:209], 0, v1, v184 op_sel_hi:[0,0,0]
	v_mfma_scale_f32_16x16x128_f8f6f4 v[74:77], v[18:25], v[202:209], 0, v1, v184 op_sel_hi:[0,0,0]
	v_mfma_scale_f32_16x16x128_f8f6f4 v[62:65], v[26:33], v[214:221], 0, v1, v184 op_sel_hi:[0,0,0]
	v_mfma_scale_f32_16x16x128_f8f6f4 v[58:61], v[18:25], v[214:221], 0, v1, v184 op_sel_hi:[0,0,0]
	v_mfma_scale_f32_16x16x128_f8f6f4 v[46:49], v[26:33], v[222:229], 0, v1, v184 op_sel_hi:[0,0,0]
	v_mfma_scale_f32_16x16x128_f8f6f4 v[42:45], v[18:25], v[222:229], 0, v1, v184 op_sel_hi:[0,0,0]
	s_setprio 0
	s_setprio 1
	v_mfma_scale_f32_16x16x128_f8f6f4 v[86:89], v[10:17], v[194:201], 0, v1, v184 op_sel_hi:[0,0,0]
	v_mfma_scale_f32_16x16x128_f8f6f4 v[82:85], v[2:9], v[194:201], 0, v1, v184 op_sel_hi:[0,0,0]
	v_mfma_scale_f32_16x16x128_f8f6f4 v[70:73], v[10:17], v[202:209], 0, v1, v184 op_sel_hi:[0,0,0]
	v_mfma_scale_f32_16x16x128_f8f6f4 v[66:69], v[2:9], v[202:209], 0, v1, v184 op_sel_hi:[0,0,0]
	v_mfma_scale_f32_16x16x128_f8f6f4 v[54:57], v[10:17], v[214:221], 0, v1, v184 op_sel_hi:[0,0,0]
	v_mfma_scale_f32_16x16x128_f8f6f4 v[50:53], v[2:9], v[214:221], 0, v1, v184 op_sel_hi:[0,0,0]
	v_mfma_scale_f32_16x16x128_f8f6f4 v[38:41], v[10:17], v[222:229], 0, v1, v184 op_sel_hi:[0,0,0]
	v_mfma_scale_f32_16x16x128_f8f6f4 v[34:37], v[2:9], v[222:229], 0, v1, v184 op_sel_hi:[0,0,0]
	s_setprio 0
	s_barrier
; #define PG8_STAGE(bufoff, gbase, voff) do { _Pragma("unroll") for (int _i = 0; _i < 2; ++_i) \
;         __builtin_amdgcn_global_load_lds((const unsigned*)((const char*)(gbase) + (voff)[_i]), (PG8_LAS unsigned*)(lds + (bufoff) + ldsw + _i * 8192), 16, 0, 0); } while (0)
; #define PG8_LDA(dst, b, h) do { _Pragma("unroll") for (int m = 0; m < 4; ++m) _Pragma("unroll") for (int k = 0; k < 2; ++k) dst[m][k] = *(const PG8_LAS bf16x8*)(lds + PG8_SA(b, h) + aoff + m * 2048 + k * 1024); } while (0)
; #define PG8_LDB(dst, b, h) do { _Pragma("unroll") for (int n = 0; n < 2; ++n) _Pragma("unroll") for (int k = 0; k < 2; ++k) dst[n][k] = *(const PG8_LAS bf16x8*)(lds + PG8_SB(b, h) + boff + n * 2048 + k * 1024); } while (0)
; #define PG8_WAIT_V(n) asm volatile("s_waitcnt vmcnt(" #n ")" ::: "memory")
; #define PG8_WAIT_L(n) asm volatile("s_waitcnt lgkmcnt(" #n ")" ::: "memory")
; #define PG8_BAR __builtin_amdgcn_s_barrier()
; #define PG8_SCHED __builtin_amdgcn_sched_barrier(0)
; template <class Epi, class Sched, bool ALIGN_EPI = false, bool SP2 = false>
; __device__ __forceinline__ void gemm_phase(PG8_LAS unsigned char* lds, const Gemm g, const Sched& S, const Epi& E) {
;     ...
;             PG8_LDB(B0, 1, 0); PG8_LDB(B1, 1, 1); PG8_SCHED; PG8_LDA(At, 1, 0); PG8_STAGE(PG8_SA(0, 1), a2 + hstep, voffA);
;             PG8_WAIT_V(8); PG8_WAIT_L(0); PG8_BAR; PG8_MMA(0, 0, At, B0); PG8_MMA(0, 1, At, B1); PG8_BAR; PG8_SCHED;
;             PG8_LDA(At, 1, 1); PG8_STAGE(PG8_SB(1, 0), b3, voffB); PG8_STAGE(PG8_SB(1, 1), b3 + hstep, voffB); PG8_STAGE(PG8_SA(1, 0), a3, voffA);
;             PG8_WAIT_V(8); PG8_WAIT_L(0); PG8_BAR; PG8_MMA(1, 0, At, B0); PG8_MMA(1, 1, At, B1); PG8_BAR; PG8_SCHED;
	s_add_i32 s54, 0, 0x18000
	s_add_i32 s55, 0, 0x1c000
	ds_read_b128 v[2:5], v248
	ds_read_b128 v[6:9], v248 offset:1024
	ds_read_b128 v[10:13], v248 offset:2048
	ds_read_b128 v[14:17], v248 offset:3072
	ds_read_b128 v[18:21], v249
	ds_read_b128 v[22:25], v249 offset:1024
	ds_read_b128 v[26:29], v249 offset:2048
	ds_read_b128 v[30:33], v249 offset:3072
	s_add_u32 s30, s30, 0x40000
	s_addc_u32 s31, s31, 0
	s_mov_b32 m0, s39
	ds_read_b128 v[194:197], v192 offset:32768
	ds_read_b128 v[198:201], v192 offset:33792
	ds_read_b128 v[202:205], v192 offset:34816
	ds_read_b128 v[206:209], v192 offset:35840
	ds_read_b128 v[214:217], v192 offset:36864
	ds_read_b128 v[218:221], v192 offset:37888
	ds_read_b128 v[222:225], v192 offset:38912
	ds_read_b128 v[226:229], v192 offset:39936
	global_load_lds_dwordx4 v168, s[30:31]
	s_mov_b32 m0, s40
	s_nop 0
	global_load_lds_dwordx4 v164, s[30:31]
	s_waitcnt vmcnt(8)
	s_waitcnt lgkmcnt(0)
	s_barrier
	s_setprio 1
	s_waitcnt lgkmcnt(0)
	v_mfma_scale_f32_16x16x128_f8f6f4 v[158:161], v[2:9], v[194:201], v[158:161], v1, v184 op_sel_hi:[0,0,0]
	v_mfma_scale_f32_16x16x128_f8f6f4 v[154:157], v[10:17], v[194:201], v[154:157], v1, v184 op_sel_hi:[0,0,0]
	v_mfma_scale_f32_16x16x128_f8f6f4 v[142:145], v[2:9], v[202:209], v[142:145], v1, v184 op_sel_hi:[0,0,0]
	v_mfma_scale_f32_16x16x128_f8f6f4 v[138:141], v[10:17], v[202:209], v[138:141], v1, v184 op_sel_hi:[0,0,0]
	v_mfma_scale_f32_16x16x128_f8f6f4 v[126:129], v[2:9], v[214:221], v[126:129], v1, v184 op_sel_hi:[0,0,0]
	v_mfma_scale_f32_16x16x128_f8f6f4 v[122:125], v[10:17], v[214:221], v[122:125], v1, v184 op_sel_hi:[0,0,0]
	v_mfma_scale_f32_16x16x128_f8f6f4 v[110:113], v[2:9], v[222:229], v[110:113], v1, v184 op_sel_hi:[0,0,0]
	v_mfma_scale_f32_16x16x128_f8f6f4 v[106:109], v[10:17], v[222:229], v[106:109], v1, v184 op_sel_hi:[0,0,0]
	s_setprio 0
	s_setprio 1
	v_mfma_scale_f32_16x16x128_f8f6f4 v[150:153], v[18:25], v[194:201], v[150:153], v1, v184 op_sel_hi:[0,0,0]
	v_mfma_scale_f32_16x16x128_f8f6f4 v[146:149], v[26:33], v[194:201], v[146:149], v1, v184 op_sel_hi:[0,0,0]
	v_mfma_scale_f32_16x16x128_f8f6f4 v[134:137], v[18:25], v[202:209], v[134:137], v1, v184 op_sel_hi:[0,0,0]
	v_mfma_scale_f32_16x16x128_f8f6f4 v[130:133], v[26:33], v[202:209], v[130:133], v1, v184 op_sel_hi:[0,0,0]
	v_mfma_scale_f32_16x16x128_f8f6f4 v[118:121], v[18:25], v[214:221], v[118:121], v1, v184 op_sel_hi:[0,0,0]
	v_mfma_scale_f32_16x16x128_f8f6f4 v[114:117], v[26:33], v[214:221], v[114:117], v1, v184 op_sel_hi:[0,0,0]
	v_mfma_scale_f32_16x16x128_f8f6f4 v[102:105], v[18:25], v[222:229], v[102:105], v1, v184 op_sel_hi:[0,0,0]
	v_mfma_scale_f32_16x16x128_f8f6f4 v[98:101], v[26:33], v[222:229], v[98:101], v1, v184 op_sel_hi:[0,0,0]
	s_setprio 0
	s_barrier
	s_add_u32 s98, s28, 0x80
	s_addc_u32 s99, s29, 0
	s_add_u32 s100, s30, 0xfffc0080
	s_addc_u32 s101, s31, -1
	s_add_i32 s30, s54, s35
	s_mov_b32 m0, s30
	ds_read_b128 v[194:197], v192 offset:49152
	ds_read_b128 v[198:201], v192 offset:50176
	ds_read_b128 v[202:205], v192 offset:51200
	ds_read_b128 v[206:209], v192 offset:52224
	ds_read_b128 v[214:217], v192 offset:53248
	ds_read_b128 v[218:221], v192 offset:54272
	ds_read_b128 v[222:225], v192 offset:55296
	ds_read_b128 v[226:229], v192 offset:56320
	global_load_lds_dwordx4 v166, s[98:99]
	s_add_i32 m0, s30, 0x2000
	s_add_u32 s28, s28, 0x40080
	s_addc_u32 s29, s29, 0
	s_add_i32 s30, s55, s35
	global_load_lds_dwordx4 v162, s[98:99]
	s_mov_b32 m0, s30
	s_nop 0
	global_load_lds_dwordx4 v166, s[28:29]
	s_add_i32 m0, s30, 0x2000
	s_nop 0
	global_load_lds_dwordx4 v162, s[28:29]
	s_mov_b32 m0, s41
	s_nop 0
	global_load_lds_dwordx4 v168, s[100:101]
	s_mov_b32 m0, s42
	s_nop 0
	global_load_lds_dwordx4 v164, s[100:101]
	s_waitcnt vmcnt(8)
	s_waitcnt lgkmcnt(0)
	s_barrier
	s_setprio 1
	s_waitcnt lgkmcnt(0)
	v_mfma_scale_f32_16x16x128_f8f6f4 v[94:97], v[2:9], v[194:201], v[94:97], v1, v184 op_sel_hi:[0,0,0]
	v_mfma_scale_f32_16x16x128_f8f6f4 v[90:93], v[10:17], v[194:201], v[90:93], v1, v184 op_sel_hi:[0,0,0]
	v_mfma_scale_f32_16x16x128_f8f6f4 v[78:81], v[2:9], v[202:209], v[78:81], v1, v184 op_sel_hi:[0,0,0]
	v_mfma_scale_f32_16x16x128_f8f6f4 v[74:77], v[10:17], v[202:209], v[74:77], v1, v184 op_sel_hi:[0,0,0]
	v_mfma_scale_f32_16x16x128_f8f6f4 v[62:65], v[2:9], v[214:221], v[62:65], v1, v184 op_sel_hi:[0,0,0]
	v_mfma_scale_f32_16x16x128_f8f6f4 v[58:61], v[10:17], v[214:221], v[58:61], v1, v184 op_sel_hi:[0,0,0]
	v_mfma_scale_f32_16x16x128_f8f6f4 v[46:49], v[2:9], v[222:229], v[46:49], v1, v184 op_sel_hi:[0,0,0]
	v_mfma_scale_f32_16x16x128_f8f6f4 v[42:45], v[10:17], v[222:229], v[42:45], v1, v184 op_sel_hi:[0,0,0]
	s_setprio 0
	s_setprio 1
	v_mfma_scale_f32_16x16x128_f8f6f4 v[86:89], v[18:25], v[194:201], v[86:89], v1, v184 op_sel_hi:[0,0,0]
	v_mfma_scale_f32_16x16x128_f8f6f4 v[82:85], v[26:33], v[194:201], v[82:85], v1, v184 op_sel_hi:[0,0,0]
	v_mfma_scale_f32_16x16x128_f8f6f4 v[70:73], v[18:25], v[202:209], v[70:73], v1, v184 op_sel_hi:[0,0,0]
	v_mfma_scale_f32_16x16x128_f8f6f4 v[66:69], v[26:33], v[202:209], v[66:69], v1, v184 op_sel_hi:[0,0,0]
	v_mfma_scale_f32_16x16x128_f8f6f4 v[54:57], v[18:25], v[214:221], v[54:57], v1, v184 op_sel_hi:[0,0,0]
	v_mfma_scale_f32_16x16x128_f8f6f4 v[50:53], v[26:33], v[214:221], v[50:53], v1, v184 op_sel_hi:[0,0,0]
	v_mfma_scale_f32_16x16x128_f8f6f4 v[38:41], v[18:25], v[222:229], v[38:41], v1, v184 op_sel_hi:[0,0,0]
	v_mfma_scale_f32_16x16x128_f8f6f4 v[34:37], v[26:33], v[222:229], v[34:37], v1, v184 op_sel_hi:[0,0,0]
	s_setprio 0
	s_barrier
	s_add_i32 s53, s53, 2
	s_add_u32 s26, s26, 0x100
	s_addc_u32 s27, s27, 0
	s_add_u32 s51, s51, 0x100
	s_addc_u32 s52, s52, 0
	s_cmp_gt_u32 s53, 13

; #define PG8_STAGE(bufoff, gbase, voff) do { _Pragma("unroll") for (int _i = 0; _i < 2; ++_i) \
;         __builtin_amdgcn_global_load_lds((const unsigned*)((const char*)(gbase) + (voff)[_i]), (PG8_LAS unsigned*)(lds + (bufoff) + ldsw + _i * 8192), 16, 0, 0); } while (0)
; #define PG8_LDA(dst, b, h) do { _Pragma("unroll") for (int m = 0; m < 4; ++m) _Pragma("unroll") for (int k = 0; k < 2; ++k) dst[m][k] = *(const PG8_LAS bf16x8*)(lds + PG8_SA(b, h) + aoff + m * 2048 + k * 1024); } while (0)
; #define PG8_BAR __builtin_amdgcn_s_barrier()
; template <class Epi, class Sched, bool ALIGN_EPI = false, bool SP2 = false>
; __device__ __forceinline__ void gemm_phase(PG8_LAS unsigned char* lds, const Gemm g, const Sched& S, const Epi& E) {
;     ...
;         const char* nA = has_next ? (const char*)g.A + (size_t)nxt.pm * tstep : cA; const char* nB = has_next ? (const char*)g.Bt + (size_t)nxt.pn * tstep : cB;
;         for (int t = 0; t < nt; t += 2) {
;             const bool last = (t == nt - 2);
;             const char* a1 = cA + (size_t)(t + 1) * kstep;
;             const char* a2 = last ? nA : cA + (size_t)(t + 2) * kstep; const char* b2 = last ? nB : cB + (size_t)(t + 2) * kstep;
;             const char* a3 = a2 + kstep; const char* b3 = b2 + kstep;
;             if (last && has_next) S.a_ready(nxt);
;             if constexpr (SP2) {
;             PG8_LDB(B0, 0, 0); PG8_LDB(B1, 0, 1); PG8_SCHED; PG8_LDA(At, 0, 0); PG8_STAGE(PG8_SA(1, 1), a1 + hstep, voffA);
;             PG8_WAIT_V(8); PG8_WAIT_L(0); PG8_BAR; PG8_MMA(0, 0, At, B0); PG8_MMA(0, 1, At, B1); PG8_BAR; PG8_SCHED;
;             PG8_LDA(At, 0, 1); PG8_STAGE(PG8_SB(0, 0), b2, voffB); PG8_STAGE(PG8_SB(0, 1), b2 + hstep, voffB); PG8_STAGE(PG8_SA(0, 0), a2, voffA);
;             PG8_WAIT_V(8); PG8_WAIT_L(0); PG8_BAR; PG8_MMA(1, 0, At, B0); PG8_MMA(1, 1, At, B1); PG8_BAR; PG8_SCHED;
;             PG8_LDB(B0, 1, 0); PG8_LDB(B1, 1, 1); PG8_SCHED; PG8_LDA(At, 1, 0); PG8_STAGE(PG8_SA(0, 1), a2 + hstep, voffA);
;             PG8_WAIT_V(8); PG8_WAIT_L(0); PG8_BAR; PG8_MMA(0, 0, At, B0); PG8_MMA(0, 1, At, B1); PG8_BAR; PG8_SCHED;
;             PG8_LDA(At, 1, 1); PG8_STAGE(PG8_SB(1, 0), b3, voffB); PG8_STAGE(PG8_SB(1, 1), b3 + hstep, voffB); PG8_STAGE(PG8_SA(1, 0), a3, voffA);
;             PG8_WAIT_V(8); PG8_WAIT_L(0); PG8_BAR; PG8_MMA(1, 0, At, B0); PG8_MMA(1, 1, At, B1); PG8_BAR; PG8_SCHED;
.LBB0_2053:
	s_add_u32 s26, s26, 0xe0080
	s_addc_u32 s27, s27, 0
	s_add_u32 s58, s28, 0x100
	s_addc_u32 s59, s29, 0
	s_mov_b32 s60, -2
	v_add_u32_e32 v248, 0x18000, v195
	v_add_u32_e32 v249, 0x1c000, v195
	ds_read_b128 v[26:29], v197
	ds_read_b128 v[30:33], v197 offset:1024
	ds_read_b128 v[18:21], v197 offset:2048
	ds_read_b128 v[22:25], v197 offset:3072
	ds_read_b128 v[10:13], v198
	ds_read_b128 v[14:17], v198 offset:1024
	ds_read_b128 v[2:5], v198 offset:2048
	ds_read_b128 v[6:9], v198 offset:3072
	s_add_u32 s28, s26, 0xfff20080
	s_addc_u32 s29, s27, -1
	s_cmp_eq_u32 s60, 52
	s_cselect_b32 s31, s5, s29
	s_cselect_b32 s30, s4, s28
	s_cselect_b32 s29, s25, s59
	s_cselect_b32 s28, s24, s58
	s_add_i32 m0, s36, 0xc000
	ds_read_b128 v[176:179], v199
	ds_read_b128 v[180:183], v199 offset:1024
	ds_read_b128 v[200:203], v199 offset:2048
	ds_read_b128 v[204:207], v199 offset:3072
	ds_read_b128 v[214:217], v199 offset:4096
	ds_read_b128 v[218:221], v199 offset:5120
	ds_read_b128 v[222:225], v199 offset:6144
	ds_read_b128 v[226:229], v199 offset:7168
	global_load_lds_dwordx4 v170, s[26:27]
	s_add_i32 m0, s36, 0xe000
	s_nop 0
	global_load_lds_dwordx4 v172, s[26:27]
	s_waitcnt vmcnt(8)
	s_waitcnt lgkmcnt(0)
	s_barrier
	s_setprio 1
	s_waitcnt lgkmcnt(0)
	v_mfma_scale_f32_16x16x128_f8f6f4 v[158:161], v[26:33], v[176:183], 0, v192, v193 op_sel_hi:[0,0,0]
	v_mfma_scale_f32_16x16x128_f8f6f4 v[154:157], v[18:25], v[176:183], 0, v192, v193 op_sel_hi:[0,0,0]
	v_mfma_scale_f32_16x16x128_f8f6f4 v[150:153], v[26:33], v[200:207], 0, v192, v193 op_sel_hi:[0,0,0]
	v_mfma_scale_f32_16x16x128_f8f6f4 v[142:145], v[18:25], v[200:207], 0, v192, v193 op_sel_hi:[0,0,0]
	v_mfma_scale_f32_16x16x128_f8f6f4 v[134:137], v[26:33], v[214:221], 0, v192, v193 op_sel_hi:[0,0,0]
	v_mfma_scale_f32_16x16x128_f8f6f4 v[126:129], v[18:25], v[214:221], 0, v192, v193 op_sel_hi:[0,0,0]
	v_mfma_scale_f32_16x16x128_f8f6f4 v[118:121], v[26:33], v[222:229], 0, v192, v193 op_sel_hi:[0,0,0]
	v_mfma_scale_f32_16x16x128_f8f6f4 v[110:113], v[18:25], v[222:229], 0, v192, v193 op_sel_hi:[0,0,0]
	s_setprio 0
	s_setprio 1
	v_mfma_scale_f32_16x16x128_f8f6f4 v[146:149], v[10:17], v[176:183], 0, v192, v193 op_sel_hi:[0,0,0]
	v_mfma_scale_f32_16x16x128_f8f6f4 v[138:141], v[2:9], v[176:183], 0, v192, v193 op_sel_hi:[0,0,0]
	v_mfma_scale_f32_16x16x128_f8f6f4 v[130:133], v[10:17], v[200:207], 0, v192, v193 op_sel_hi:[0,0,0]
	v_mfma_scale_f32_16x16x128_f8f6f4 v[122:125], v[2:9], v[200:207], 0, v192, v193 op_sel_hi:[0,0,0]
	v_mfma_scale_f32_16x16x128_f8f6f4 v[114:117], v[10:17], v[214:221], 0, v192, v193 op_sel_hi:[0,0,0]
	v_mfma_scale_f32_16x16x128_f8f6f4 v[106:109], v[2:9], v[214:221], 0, v192, v193 op_sel_hi:[0,0,0]
	v_mfma_scale_f32_16x16x128_f8f6f4 v[102:105], v[10:17], v[222:229], 0, v192, v193 op_sel_hi:[0,0,0]
	v_mfma_scale_f32_16x16x128_f8f6f4 v[98:101], v[2:9], v[222:229], 0, v192, v193 op_sel_hi:[0,0,0]
	s_setprio 0
	s_barrier
	s_add_i32 s61, s44, s34
	s_mov_b32 m0, s61
	ds_read_b128 v[200:203], v199 offset:16384
	ds_read_b128 v[204:207], v199 offset:17408
	ds_read_b128 v[214:217], v199 offset:18432
	ds_read_b128 v[218:221], v199 offset:19456
	ds_read_b128 v[222:225], v199 offset:20480
	ds_read_b128 v[226:229], v199 offset:21504
	ds_read_b128 v[230:233], v199 offset:22528
	ds_read_b128 v[234:237], v199 offset:23552
	global_load_lds_dwordx4 v164, s[28:29]
	s_add_i32 m0, s61, 0x2000
	s_add_u32 s62, s28, 0xe0000
	s_addc_u32 s63, s29, 0
	s_add_i32 s61, s45, s34
	global_load_lds_dwordx4 v168, s[28:29]
	s_mov_b32 m0, s61
	s_nop 0
	global_load_lds_dwordx4 v164, s[62:63]
	s_add_i32 m0, s61, 0x2000
	s_nop 0
	global_load_lds_dwordx4 v168, s[62:63]
	s_mov_b32 m0, s36
	s_nop 0
	global_load_lds_dwordx4 v162, s[30:31]
	s_mov_b32 m0, s37
	s_nop 0
	global_load_lds_dwordx4 v166, s[30:31]
	s_waitcnt vmcnt(8)
	s_waitcnt lgkmcnt(0)
	s_barrier
	s_setprio 1
	s_waitcnt lgkmcnt(0)
	v_mfma_scale_f32_16x16x128_f8f6f4 v[94:97], v[26:33], v[200:207], 0, v192, v193 op_sel_hi:[0,0,0]
	v_mfma_scale_f32_16x16x128_f8f6f4 v[90:93], v[18:25], v[200:207], 0, v192, v193 op_sel_hi:[0,0,0]
	v_mfma_scale_f32_16x16x128_f8f6f4 v[86:89], v[26:33], v[214:221], 0, v192, v193 op_sel_hi:[0,0,0]
	v_mfma_scale_f32_16x16x128_f8f6f4 v[78:81], v[18:25], v[214:221], 0, v192, v193 op_sel_hi:[0,0,0]
	v_mfma_scale_f32_16x16x128_f8f6f4 v[70:73], v[26:33], v[222:229], 0, v192, v193 op_sel_hi:[0,0,0]
	v_mfma_scale_f32_16x16x128_f8f6f4 v[62:65], v[18:25], v[222:229], 0, v192, v193 op_sel_hi:[0,0,0]
	v_mfma_scale_f32_16x16x128_f8f6f4 v[54:57], v[26:33], v[230:237], 0, v192, v193 op_sel_hi:[0,0,0]
	v_mfma_scale_f32_16x16x128_f8f6f4 v[46:49], v[18:25], v[230:237], 0, v192, v193 op_sel_hi:[0,0,0]
	s_setprio 0
	s_setprio 1
	v_mfma_scale_f32_16x16x128_f8f6f4 v[82:85], v[10:17], v[200:207], 0, v192, v193 op_sel_hi:[0,0,0]
	v_mfma_scale_f32_16x16x128_f8f6f4 v[74:77], v[2:9], v[200:207], 0, v192, v193 op_sel_hi:[0,0,0]
	v_mfma_scale_f32_16x16x128_f8f6f4 v[66:69], v[10:17], v[214:221], 0, v192, v193 op_sel_hi:[0,0,0]
	v_mfma_scale_f32_16x16x128_f8f6f4 v[58:61], v[2:9], v[214:221], 0, v192, v193 op_sel_hi:[0,0,0]
	v_mfma_scale_f32_16x16x128_f8f6f4 v[50:53], v[10:17], v[222:229], 0, v192, v193 op_sel_hi:[0,0,0]
	v_mfma_scale_f32_16x16x128_f8f6f4 v[42:45], v[2:9], v[222:229], 0, v192, v193 op_sel_hi:[0,0,0]
	v_mfma_scale_f32_16x16x128_f8f6f4 v[38:41], v[10:17], v[230:237], 0, v192, v193 op_sel_hi:[0,0,0]
	v_mfma_scale_f32_16x16x128_f8f6f4 v[34:37], v[2:9], v[230:237], 0, v192, v193 op_sel_hi:[0,0,0]
	s_setprio 0
	s_barrier
; #define PG8_STAGE(bufoff, gbase, voff) do { _Pragma("unroll") for (int _i = 0; _i < 2; ++_i) \
;         __builtin_amdgcn_global_load_lds((const unsigned*)((const char*)(gbase) + (voff)[_i]), (PG8_LAS unsigned*)(lds + (bufoff) + ldsw + _i * 8192), 16, 0, 0); } while (0)
; #define PG8_LDA(dst, b, h) do { _Pragma("unroll") for (int m = 0; m < 4; ++m) _Pragma("unroll") for (int k = 0; k < 2; ++k) dst[m][k] = *(const PG8_LAS bf16x8*)(lds + PG8_SA(b, h) + aoff + m * 2048 + k * 1024); } while (0)
; #define PG8_LDB(dst, b, h) do { _Pragma("unroll") for (int n = 0; n < 2; ++n) _Pragma("unroll") for (int k = 0; k < 2; ++k) dst[n][k] = *(const PG8_LAS bf16x8*)(lds + PG8_SB(b, h) + boff + n * 2048 + k * 1024); } while (0)
; #define PG8_WAIT_V(n) asm volatile("s_waitcnt vmcnt(" #n ")" ::: "memory")
; #define PG8_WAIT_L(n) asm volatile("s_waitcnt lgkmcnt(" #n ")" ::: "memory")
; #define PG8_BAR __builtin_amdgcn_s_barrier()
; #define PG8_SCHED __builtin_amdgcn_sched_barrier(0)
; template <class Epi, class Sched, bool ALIGN_EPI = false, bool SP2 = false>
; __device__ __forceinline__ void gemm_phase(PG8_LAS unsigned char* lds, const Gemm g, const Sched& S, const Epi& E) {
;     ...
;             PG8_LDB(B0, 1, 0); PG8_LDB(B1, 1, 1); PG8_SCHED; PG8_LDA(At, 1, 0); PG8_STAGE(PG8_SA(0, 1), a2 + hstep, voffA);
;             PG8_WAIT_V(8); PG8_WAIT_L(0); PG8_BAR; PG8_MMA(0, 0, At, B0); PG8_MMA(0, 1, At, B1); PG8_BAR; PG8_SCHED;
;             PG8_LDA(At, 1, 1); PG8_STAGE(PG8_SB(1, 0), b3, voffB); PG8_STAGE(PG8_SB(1, 1), b3 + hstep, voffB); PG8_STAGE(PG8_SA(1, 0), a3, voffA);
;             PG8_WAIT_V(8); PG8_WAIT_L(0); PG8_BAR; PG8_MMA(1, 0, At, B0); PG8_MMA(1, 1, At, B1); PG8_BAR; PG8_SCHED;
	s_add_i32 s61, 0, 0x18000
	s_add_i32 s62, 0, 0x1c000
	ds_read_b128 v[2:5], v248
	ds_read_b128 v[6:9], v248 offset:1024
	ds_read_b128 v[10:13], v248 offset:2048
	ds_read_b128 v[14:17], v248 offset:3072
	ds_read_b128 v[18:21], v249
	ds_read_b128 v[22:25], v249 offset:1024
	ds_read_b128 v[26:29], v249 offset:2048
	ds_read_b128 v[30:33], v249 offset:3072
	s_add_u32 s30, s30, 0xe0000
	s_addc_u32 s31, s31, 0
	s_mov_b32 m0, s38
	ds_read_b128 v[200:203], v199 offset:32768
	ds_read_b128 v[204:207], v199 offset:33792
	ds_read_b128 v[214:217], v199 offset:34816
	ds_read_b128 v[218:221], v199 offset:35840
	ds_read_b128 v[222:225], v199 offset:36864
	ds_read_b128 v[226:229], v199 offset:37888
	ds_read_b128 v[230:233], v199 offset:38912
	ds_read_b128 v[234:237], v199 offset:39936
	global_load_lds_dwordx4 v162, s[30:31]
	s_mov_b32 m0, s39
	s_nop 0
	global_load_lds_dwordx4 v166, s[30:31]
	s_waitcnt vmcnt(8)
	s_waitcnt lgkmcnt(0)
	s_barrier
	s_setprio 1
	s_waitcnt lgkmcnt(0)
	v_mfma_scale_f32_16x16x128_f8f6f4 v[158:161], v[2:9], v[200:207], v[158:161], v192, v193 op_sel_hi:[0,0,0]
	v_mfma_scale_f32_16x16x128_f8f6f4 v[154:157], v[10:17], v[200:207], v[154:157], v192, v193 op_sel_hi:[0,0,0]
	v_mfma_scale_f32_16x16x128_f8f6f4 v[150:153], v[2:9], v[214:221], v[150:153], v192, v193 op_sel_hi:[0,0,0]
	v_mfma_scale_f32_16x16x128_f8f6f4 v[142:145], v[10:17], v[214:221], v[142:145], v192, v193 op_sel_hi:[0,0,0]
	v_mfma_scale_f32_16x16x128_f8f6f4 v[134:137], v[2:9], v[222:229], v[134:137], v192, v193 op_sel_hi:[0,0,0]
	v_mfma_scale_f32_16x16x128_f8f6f4 v[126:129], v[10:17], v[222:229], v[126:129], v192, v193 op_sel_hi:[0,0,0]
	v_mfma_scale_f32_16x16x128_f8f6f4 v[118:121], v[2:9], v[230:237], v[118:121], v192, v193 op_sel_hi:[0,0,0]
	v_mfma_scale_f32_16x16x128_f8f6f4 v[110:113], v[10:17], v[230:237], v[110:113], v192, v193 op_sel_hi:[0,0,0]
	s_setprio 0
	s_setprio 1
	v_mfma_scale_f32_16x16x128_f8f6f4 v[146:149], v[18:25], v[200:207], v[146:149], v192, v193 op_sel_hi:[0,0,0]
	v_mfma_scale_f32_16x16x128_f8f6f4 v[138:141], v[26:33], v[200:207], v[138:141], v192, v193 op_sel_hi:[0,0,0]
	v_mfma_scale_f32_16x16x128_f8f6f4 v[130:133], v[18:25], v[214:221], v[130:133], v192, v193 op_sel_hi:[0,0,0]
	v_mfma_scale_f32_16x16x128_f8f6f4 v[122:125], v[26:33], v[214:221], v[122:125], v192, v193 op_sel_hi:[0,0,0]
	v_mfma_scale_f32_16x16x128_f8f6f4 v[114:117], v[18:25], v[222:229], v[114:117], v192, v193 op_sel_hi:[0,0,0]
	v_mfma_scale_f32_16x16x128_f8f6f4 v[106:109], v[26:33], v[222:229], v[106:109], v192, v193 op_sel_hi:[0,0,0]
	v_mfma_scale_f32_16x16x128_f8f6f4 v[102:105], v[18:25], v[230:237], v[102:105], v192, v193 op_sel_hi:[0,0,0]
	v_mfma_scale_f32_16x16x128_f8f6f4 v[98:101], v[26:33], v[230:237], v[98:101], v192, v193 op_sel_hi:[0,0,0]
	s_setprio 0
	s_barrier
	s_add_u32 s98, s28, 0x80
	s_addc_u32 s99, s29, 0
	s_add_u32 s100, s30, 0xfff20080
	s_addc_u32 s101, s31, -1
	s_add_i32 s30, s61, s34
	s_mov_b32 m0, s30
	ds_read_b128 v[200:203], v199 offset:49152
	ds_read_b128 v[204:207], v199 offset:50176
	ds_read_b128 v[214:217], v199 offset:51200
	ds_read_b128 v[218:221], v199 offset:52224
	ds_read_b128 v[222:225], v199 offset:53248
	ds_read_b128 v[226:229], v199 offset:54272
	ds_read_b128 v[230:233], v199 offset:55296
	ds_read_b128 v[234:237], v199 offset:56320
	global_load_lds_dwordx4 v164, s[98:99]
	s_add_i32 m0, s30, 0x2000
	s_add_u32 s28, s28, 0xe0080
	s_addc_u32 s29, s29, 0
	s_add_i32 s30, s62, s34
	global_load_lds_dwordx4 v168, s[98:99]
	s_mov_b32 m0, s30
	s_nop 0
	global_load_lds_dwordx4 v164, s[28:29]
	s_add_i32 m0, s30, 0x2000
	s_nop 0
	global_load_lds_dwordx4 v168, s[28:29]
	s_mov_b32 m0, s41
	s_nop 0
	global_load_lds_dwordx4 v162, s[100:101]
	s_mov_b32 m0, s42
	s_nop 0
	global_load_lds_dwordx4 v166, s[100:101]
	s_waitcnt vmcnt(8)
	s_waitcnt lgkmcnt(0)
	s_barrier
	s_setprio 1
	s_waitcnt lgkmcnt(0)
	v_mfma_scale_f32_16x16x128_f8f6f4 v[94:97], v[2:9], v[200:207], v[94:97], v192, v193 op_sel_hi:[0,0,0]
	v_mfma_scale_f32_16x16x128_f8f6f4 v[90:93], v[10:17], v[200:207], v[90:93], v192, v193 op_sel_hi:[0,0,0]
	v_mfma_scale_f32_16x16x128_f8f6f4 v[86:89], v[2:9], v[214:221], v[86:89], v192, v193 op_sel_hi:[0,0,0]
	v_mfma_scale_f32_16x16x128_f8f6f4 v[78:81], v[10:17], v[214:221], v[78:81], v192, v193 op_sel_hi:[0,0,0]
	v_mfma_scale_f32_16x16x128_f8f6f4 v[70:73], v[2:9], v[222:229], v[70:73], v192, v193 op_sel_hi:[0,0,0]
	v_mfma_scale_f32_16x16x128_f8f6f4 v[62:65], v[10:17], v[222:229], v[62:65], v192, v193 op_sel_hi:[0,0,0]
	v_mfma_scale_f32_16x16x128_f8f6f4 v[54:57], v[2:9], v[230:237], v[54:57], v192, v193 op_sel_hi:[0,0,0]
	v_mfma_scale_f32_16x16x128_f8f6f4 v[46:49], v[10:17], v[230:237], v[46:49], v192, v193 op_sel_hi:[0,0,0]
	s_setprio 0
	s_setprio 1
	v_mfma_scale_f32_16x16x128_f8f6f4 v[82:85], v[18:25], v[200:207], v[82:85], v192, v193 op_sel_hi:[0,0,0]
	v_mfma_scale_f32_16x16x128_f8f6f4 v[74:77], v[26:33], v[200:207], v[74:77], v192, v193 op_sel_hi:[0,0,0]
	v_mfma_scale_f32_16x16x128_f8f6f4 v[66:69], v[18:25], v[214:221], v[66:69], v192, v193 op_sel_hi:[0,0,0]
	v_mfma_scale_f32_16x16x128_f8f6f4 v[58:61], v[26:33], v[214:221], v[58:61], v192, v193 op_sel_hi:[0,0,0]
	v_mfma_scale_f32_16x16x128_f8f6f4 v[50:53], v[18:25], v[222:229], v[50:53], v192, v193 op_sel_hi:[0,0,0]
	v_mfma_scale_f32_16x16x128_f8f6f4 v[42:45], v[26:33], v[222:229], v[42:45], v192, v193 op_sel_hi:[0,0,0]
	v_mfma_scale_f32_16x16x128_f8f6f4 v[38:41], v[18:25], v[230:237], v[38:41], v192, v193 op_sel_hi:[0,0,0]
	v_mfma_scale_f32_16x16x128_f8f6f4 v[34:37], v[26:33], v[230:237], v[34:37], v192, v193 op_sel_hi:[0,0,0]
	s_setprio 0
	s_barrier
	s_add_i32 s60, s60, 2
	s_add_u32 s26, s26, 0x100
	s_addc_u32 s27, s27, 0
	s_add_u32 s58, s58, 0x100
	s_addc_u32 s59, s59, 0
	s_cmp_gt_u32 s60, 53

; #define PG8_STAGE(bufoff, gbase, voff) do { _Pragma("unroll") for (int _i = 0; _i < 2; ++_i) \
;         __builtin_amdgcn_global_load_lds((const unsigned*)((const char*)(gbase) + (voff)[_i]), (PG8_LAS unsigned*)(lds + (bufoff) + ldsw + _i * 8192), 16, 0, 0); } while (0)
; #define PG8_LDA(dst, b, h) do { _Pragma("unroll") for (int m = 0; m < 4; ++m) _Pragma("unroll") for (int k = 0; k < 2; ++k) dst[m][k] = *(const PG8_LAS bf16x8*)(lds + PG8_SA(b, h) + aoff + m * 2048 + k * 1024); } while (0)
; #define PG8_BAR __builtin_amdgcn_s_barrier()
; template <class Epi, class Sched, bool ALIGN_EPI = false, bool SP2 = false>
; __device__ __forceinline__ void gemm_phase(PG8_LAS unsigned char* lds, const Gemm g, const Sched& S, const Epi& E) {
;     ...
;         const char* nA = has_next ? (const char*)g.A + (size_t)nxt.pm * tstep : cA; const char* nB = has_next ? (const char*)g.Bt + (size_t)nxt.pn * tstep : cB;
;         for (int t = 0; t < nt; t += 2) {
;             const bool last = (t == nt - 2);
;             const char* a1 = cA + (size_t)(t + 1) * kstep;
;             const char* a2 = last ? nA : cA + (size_t)(t + 2) * kstep; const char* b2 = last ? nB : cB + (size_t)(t + 2) * kstep;
;             const char* a3 = a2 + kstep; const char* b3 = b2 + kstep;
;             if (last && has_next) S.a_ready(nxt);
;             if constexpr (SP2) {
;             PG8_LDB(B0, 0, 0); PG8_LDB(B1, 0, 1); PG8_SCHED; PG8_LDA(At, 0, 0); PG8_STAGE(PG8_SA(1, 1), a1 + hstep, voffA);
;             PG8_WAIT_V(8); PG8_WAIT_L(0); PG8_BAR; PG8_MMA(0, 0, At, B0); PG8_MMA(0, 1, At, B1); PG8_BAR; PG8_SCHED;
;             PG8_LDA(At, 0, 1); PG8_STAGE(PG8_SB(0, 0), b2, voffB); PG8_STAGE(PG8_SB(0, 1), b2 + hstep, voffB); PG8_STAGE(PG8_SA(0, 0), a2, voffA);
;             PG8_WAIT_V(8); PG8_WAIT_L(0); PG8_BAR; PG8_MMA(1, 0, At, B0); PG8_MMA(1, 1, At, B1); PG8_BAR; PG8_SCHED;
;             PG8_LDB(B0, 1, 0); PG8_LDB(B1, 1, 1); PG8_SCHED; PG8_LDA(At, 1, 0); PG8_STAGE(PG8_SA(0, 1), a2 + hstep, voffA);
;             PG8_WAIT_V(8); PG8_WAIT_L(0); PG8_BAR; PG8_MMA(0, 0, At, B0); PG8_MMA(0, 1, At, B1); PG8_BAR; PG8_SCHED;
;             PG8_LDA(At, 1, 1); PG8_STAGE(PG8_SB(1, 0), b3, voffB); PG8_STAGE(PG8_SB(1, 1), b3 + hstep, voffB); PG8_STAGE(PG8_SA(1, 0), a3, voffA);
;             PG8_WAIT_V(8); PG8_WAIT_L(0); PG8_BAR; PG8_MMA(1, 0, At, B0); PG8_MMA(1, 1, At, B1); PG8_BAR; PG8_SCHED;
.LBB0_2132:
	s_add_u32 s24, s24, 0xe0080
	s_addc_u32 s25, s25, 0
	s_add_u32 s56, s26, 0x100
	s_addc_u32 s57, s27, 0
	s_mov_b32 s58, -2
	v_add_u32_e32 v248, 0x18000, v190
	v_add_u32_e32 v249, 0x1c000, v190
	ds_read_b128 v[26:29], v1
	ds_read_b128 v[30:33], v1 offset:1024
	ds_read_b128 v[18:21], v1 offset:2048
	ds_read_b128 v[22:25], v1 offset:3072
	ds_read_b128 v[10:13], v184
	ds_read_b128 v[14:17], v184 offset:1024
	ds_read_b128 v[2:5], v184 offset:2048
	ds_read_b128 v[6:9], v184 offset:3072
	s_add_u32 s26, s24, 0xfff20080
	s_addc_u32 s27, s25, -1
	s_cmp_eq_u32 s58, 52
	s_cselect_b32 s29, s3, s27
	s_cselect_b32 s28, s2, s26
	s_cselect_b32 s27, s23, s57
	s_cselect_b32 s26, s22, s56
	s_add_i32 m0, s34, 0xc000
	ds_read_b128 v[176:179], v188
	ds_read_b128 v[180:183], v188 offset:1024
	ds_read_b128 v[194:197], v188 offset:2048
	ds_read_b128 v[198:201], v188 offset:3072
	ds_read_b128 v[202:205], v188 offset:4096
	ds_read_b128 v[206:209], v188 offset:5120
	ds_read_b128 v[210:213], v188 offset:6144
	ds_read_b128 v[214:217], v188 offset:7168
	global_load_lds_dwordx4 v170, s[24:25]
	s_add_i32 m0, s34, 0xe000
	s_nop 0
	global_load_lds_dwordx4 v172, s[24:25]
	s_waitcnt vmcnt(8)
	s_waitcnt lgkmcnt(0)
	s_barrier
	s_setprio 1
	s_waitcnt lgkmcnt(0)
	v_mfma_scale_f32_16x16x128_f8f6f4 v[158:161], v[26:33], v[176:183], 0, v187, v192 op_sel_hi:[0,0,0]
	v_mfma_scale_f32_16x16x128_f8f6f4 v[154:157], v[18:25], v[176:183], 0, v187, v192 op_sel_hi:[0,0,0]
	v_mfma_scale_f32_16x16x128_f8f6f4 v[150:153], v[26:33], v[194:201], 0, v187, v192 op_sel_hi:[0,0,0]
	v_mfma_scale_f32_16x16x128_f8f6f4 v[142:145], v[18:25], v[194:201], 0, v187, v192 op_sel_hi:[0,0,0]
	v_mfma_scale_f32_16x16x128_f8f6f4 v[134:137], v[26:33], v[202:209], 0, v187, v192 op_sel_hi:[0,0,0]
	v_mfma_scale_f32_16x16x128_f8f6f4 v[126:129], v[18:25], v[202:209], 0, v187, v192 op_sel_hi:[0,0,0]
	v_mfma_scale_f32_16x16x128_f8f6f4 v[118:121], v[26:33], v[210:217], 0, v187, v192 op_sel_hi:[0,0,0]
	v_mfma_scale_f32_16x16x128_f8f6f4 v[110:113], v[18:25], v[210:217], 0, v187, v192 op_sel_hi:[0,0,0]
	s_setprio 0
	s_setprio 1
	v_mfma_scale_f32_16x16x128_f8f6f4 v[146:149], v[10:17], v[176:183], 0, v187, v192 op_sel_hi:[0,0,0]
	v_mfma_scale_f32_16x16x128_f8f6f4 v[138:141], v[2:9], v[176:183], 0, v187, v192 op_sel_hi:[0,0,0]
	v_mfma_scale_f32_16x16x128_f8f6f4 v[130:133], v[10:17], v[194:201], 0, v187, v192 op_sel_hi:[0,0,0]
	v_mfma_scale_f32_16x16x128_f8f6f4 v[122:125], v[2:9], v[194:201], 0, v187, v192 op_sel_hi:[0,0,0]
	v_mfma_scale_f32_16x16x128_f8f6f4 v[114:117], v[10:17], v[202:209], 0, v187, v192 op_sel_hi:[0,0,0]
	v_mfma_scale_f32_16x16x128_f8f6f4 v[106:109], v[2:9], v[202:209], 0, v187, v192 op_sel_hi:[0,0,0]
	v_mfma_scale_f32_16x16x128_f8f6f4 v[102:105], v[10:17], v[210:217], 0, v187, v192 op_sel_hi:[0,0,0]
	v_mfma_scale_f32_16x16x128_f8f6f4 v[98:101], v[2:9], v[210:217], 0, v187, v192 op_sel_hi:[0,0,0]
	s_setprio 0
	s_barrier
	s_add_i32 s59, s42, s31
	s_mov_b32 m0, s59
	ds_read_b128 v[194:197], v188 offset:16384
	ds_read_b128 v[198:201], v188 offset:17408
	ds_read_b128 v[202:205], v188 offset:18432
	ds_read_b128 v[206:209], v188 offset:19456
	ds_read_b128 v[210:213], v188 offset:20480
	ds_read_b128 v[214:217], v188 offset:21504
	ds_read_b128 v[218:221], v188 offset:22528
	ds_read_b128 v[222:225], v188 offset:23552
	global_load_lds_dwordx4 v164, s[26:27]
	s_add_i32 m0, s59, 0x2000
	s_add_u32 s60, s26, 0xe0000
	s_addc_u32 s61, s27, 0
	s_add_i32 s59, s43, s31
	global_load_lds_dwordx4 v168, s[26:27]
	s_mov_b32 m0, s59
	s_nop 0
	global_load_lds_dwordx4 v164, s[60:61]
	s_add_i32 m0, s59, 0x2000
	s_nop 0
	global_load_lds_dwordx4 v168, s[60:61]
	s_mov_b32 m0, s34
	s_nop 0
	global_load_lds_dwordx4 v162, s[28:29]
	s_mov_b32 m0, s35
	s_nop 0
	global_load_lds_dwordx4 v166, s[28:29]
	s_waitcnt vmcnt(8)
	s_waitcnt lgkmcnt(0)
	s_barrier
	s_setprio 1
	s_waitcnt lgkmcnt(0)
	v_mfma_scale_f32_16x16x128_f8f6f4 v[94:97], v[26:33], v[194:201], 0, v187, v192 op_sel_hi:[0,0,0]
	v_mfma_scale_f32_16x16x128_f8f6f4 v[90:93], v[18:25], v[194:201], 0, v187, v192 op_sel_hi:[0,0,0]
	v_mfma_scale_f32_16x16x128_f8f6f4 v[86:89], v[26:33], v[202:209], 0, v187, v192 op_sel_hi:[0,0,0]
	v_mfma_scale_f32_16x16x128_f8f6f4 v[78:81], v[18:25], v[202:209], 0, v187, v192 op_sel_hi:[0,0,0]
	v_mfma_scale_f32_16x16x128_f8f6f4 v[70:73], v[26:33], v[210:217], 0, v187, v192 op_sel_hi:[0,0,0]
	v_mfma_scale_f32_16x16x128_f8f6f4 v[62:65], v[18:25], v[210:217], 0, v187, v192 op_sel_hi:[0,0,0]
	v_mfma_scale_f32_16x16x128_f8f6f4 v[54:57], v[26:33], v[218:225], 0, v187, v192 op_sel_hi:[0,0,0]
	v_mfma_scale_f32_16x16x128_f8f6f4 v[46:49], v[18:25], v[218:225], 0, v187, v192 op_sel_hi:[0,0,0]
	s_setprio 0
	s_setprio 1
	v_mfma_scale_f32_16x16x128_f8f6f4 v[82:85], v[10:17], v[194:201], 0, v187, v192 op_sel_hi:[0,0,0]
	v_mfma_scale_f32_16x16x128_f8f6f4 v[74:77], v[2:9], v[194:201], 0, v187, v192 op_sel_hi:[0,0,0]
	v_mfma_scale_f32_16x16x128_f8f6f4 v[66:69], v[10:17], v[202:209], 0, v187, v192 op_sel_hi:[0,0,0]
	v_mfma_scale_f32_16x16x128_f8f6f4 v[58:61], v[2:9], v[202:209], 0, v187, v192 op_sel_hi:[0,0,0]
	v_mfma_scale_f32_16x16x128_f8f6f4 v[50:53], v[10:17], v[210:217], 0, v187, v192 op_sel_hi:[0,0,0]
	v_mfma_scale_f32_16x16x128_f8f6f4 v[42:45], v[2:9], v[210:217], 0, v187, v192 op_sel_hi:[0,0,0]
	v_mfma_scale_f32_16x16x128_f8f6f4 v[38:41], v[10:17], v[218:225], 0, v187, v192 op_sel_hi:[0,0,0]
	v_mfma_scale_f32_16x16x128_f8f6f4 v[34:37], v[2:9], v[218:225], 0, v187, v192 op_sel_hi:[0,0,0]
	s_setprio 0
	s_barrier
; #define PG8_STAGE(bufoff, gbase, voff) do { _Pragma("unroll") for (int _i = 0; _i < 2; ++_i) \
;         __builtin_amdgcn_global_load_lds((const unsigned*)((const char*)(gbase) + (voff)[_i]), (PG8_LAS unsigned*)(lds + (bufoff) + ldsw + _i * 8192), 16, 0, 0); } while (0)
; #define PG8_LDA(dst, b, h) do { _Pragma("unroll") for (int m = 0; m < 4; ++m) _Pragma("unroll") for (int k = 0; k < 2; ++k) dst[m][k] = *(const PG8_LAS bf16x8*)(lds + PG8_SA(b, h) + aoff + m * 2048 + k * 1024); } while (0)
; #define PG8_LDB(dst, b, h) do { _Pragma("unroll") for (int n = 0; n < 2; ++n) _Pragma("unroll") for (int k = 0; k < 2; ++k) dst[n][k] = *(const PG8_LAS bf16x8*)(lds + PG8_SB(b, h) + boff + n * 2048 + k * 1024); } while (0)
; #define PG8_WAIT_V(n) asm volatile("s_waitcnt vmcnt(" #n ")" ::: "memory")
; #define PG8_WAIT_L(n) asm volatile("s_waitcnt lgkmcnt(" #n ")" ::: "memory")
; #define PG8_BAR __builtin_amdgcn_s_barrier()
; #define PG8_SCHED __builtin_amdgcn_sched_barrier(0)
; template <class Epi, class Sched, bool ALIGN_EPI = false, bool SP2 = false>
; __device__ __forceinline__ void gemm_phase(PG8_LAS unsigned char* lds, const Gemm g, const Sched& S, const Epi& E) {
;     ...
;             PG8_LDB(B0, 1, 0); PG8_LDB(B1, 1, 1); PG8_SCHED; PG8_LDA(At, 1, 0); PG8_STAGE(PG8_SA(0, 1), a2 + hstep, voffA);
;             PG8_WAIT_V(8); PG8_WAIT_L(0); PG8_BAR; PG8_MMA(0, 0, At, B0); PG8_MMA(0, 1, At, B1); PG8_BAR; PG8_SCHED;
;             PG8_LDA(At, 1, 1); PG8_STAGE(PG8_SB(1, 0), b3, voffB); PG8_STAGE(PG8_SB(1, 1), b3 + hstep, voffB); PG8_STAGE(PG8_SA(1, 0), a3, voffA);
;             PG8_WAIT_V(8); PG8_WAIT_L(0); PG8_BAR; PG8_MMA(1, 0, At, B0); PG8_MMA(1, 1, At, B1); PG8_BAR; PG8_SCHED;
	s_add_i32 s59, 0, 0x18000
	s_add_i32 s60, 0, 0x1c000
	ds_read_b128 v[2:5], v248
	ds_read_b128 v[6:9], v248 offset:1024
	ds_read_b128 v[10:13], v248 offset:2048
	ds_read_b128 v[14:17], v248 offset:3072
	ds_read_b128 v[18:21], v249
	ds_read_b128 v[22:25], v249 offset:1024
	ds_read_b128 v[26:29], v249 offset:2048
	ds_read_b128 v[30:33], v249 offset:3072
	s_add_u32 s28, s28, 0xe0000
	s_addc_u32 s29, s29, 0
	s_mov_b32 m0, s36
	ds_read_b128 v[194:197], v188 offset:32768
	ds_read_b128 v[198:201], v188 offset:33792
	ds_read_b128 v[202:205], v188 offset:34816
	ds_read_b128 v[206:209], v188 offset:35840
	ds_read_b128 v[210:213], v188 offset:36864
	ds_read_b128 v[214:217], v188 offset:37888
	ds_read_b128 v[218:221], v188 offset:38912
	ds_read_b128 v[222:225], v188 offset:39936
	global_load_lds_dwordx4 v162, s[28:29]
	s_mov_b32 m0, s37
	s_nop 0
	global_load_lds_dwordx4 v166, s[28:29]
	s_waitcnt vmcnt(8)
	s_waitcnt lgkmcnt(0)
	s_barrier
	s_setprio 1
	s_waitcnt lgkmcnt(0)
	v_mfma_scale_f32_16x16x128_f8f6f4 v[158:161], v[2:9], v[194:201], v[158:161], v187, v192 op_sel_hi:[0,0,0]
	v_mfma_scale_f32_16x16x128_f8f6f4 v[154:157], v[10:17], v[194:201], v[154:157], v187, v192 op_sel_hi:[0,0,0]
	v_mfma_scale_f32_16x16x128_f8f6f4 v[150:153], v[2:9], v[202:209], v[150:153], v187, v192 op_sel_hi:[0,0,0]
	v_mfma_scale_f32_16x16x128_f8f6f4 v[142:145], v[10:17], v[202:209], v[142:145], v187, v192 op_sel_hi:[0,0,0]
	v_mfma_scale_f32_16x16x128_f8f6f4 v[134:137], v[2:9], v[210:217], v[134:137], v187, v192 op_sel_hi:[0,0,0]
	v_mfma_scale_f32_16x16x128_f8f6f4 v[126:129], v[10:17], v[210:217], v[126:129], v187, v192 op_sel_hi:[0,0,0]
	v_mfma_scale_f32_16x16x128_f8f6f4 v[118:121], v[2:9], v[218:225], v[118:121], v187, v192 op_sel_hi:[0,0,0]
	v_mfma_scale_f32_16x16x128_f8f6f4 v[110:113], v[10:17], v[218:225], v[110:113], v187, v192 op_sel_hi:[0,0,0]
	s_setprio 0
	s_setprio 1
	v_mfma_scale_f32_16x16x128_f8f6f4 v[146:149], v[18:25], v[194:201], v[146:149], v187, v192 op_sel_hi:[0,0,0]
	v_mfma_scale_f32_16x16x128_f8f6f4 v[138:141], v[26:33], v[194:201], v[138:141], v187, v192 op_sel_hi:[0,0,0]
	v_mfma_scale_f32_16x16x128_f8f6f4 v[130:133], v[18:25], v[202:209], v[130:133], v187, v192 op_sel_hi:[0,0,0]
	v_mfma_scale_f32_16x16x128_f8f6f4 v[122:125], v[26:33], v[202:209], v[122:125], v187, v192 op_sel_hi:[0,0,0]
	v_mfma_scale_f32_16x16x128_f8f6f4 v[114:117], v[18:25], v[210:217], v[114:117], v187, v192 op_sel_hi:[0,0,0]
	v_mfma_scale_f32_16x16x128_f8f6f4 v[106:109], v[26:33], v[210:217], v[106:109], v187, v192 op_sel_hi:[0,0,0]
	v_mfma_scale_f32_16x16x128_f8f6f4 v[102:105], v[18:25], v[218:225], v[102:105], v187, v192 op_sel_hi:[0,0,0]
	v_mfma_scale_f32_16x16x128_f8f6f4 v[98:101], v[26:33], v[218:225], v[98:101], v187, v192 op_sel_hi:[0,0,0]
	s_setprio 0
	s_barrier
	s_add_u32 s98, s26, 0x80
	s_addc_u32 s99, s27, 0
	s_add_u32 s100, s28, 0xfff20080
	s_addc_u32 s101, s29, -1
	s_add_i32 s28, s59, s31
	s_mov_b32 m0, s28
	ds_read_b128 v[194:197], v188 offset:49152
	ds_read_b128 v[198:201], v188 offset:50176
	ds_read_b128 v[202:205], v188 offset:51200
	ds_read_b128 v[206:209], v188 offset:52224
	ds_read_b128 v[210:213], v188 offset:53248
	ds_read_b128 v[214:217], v188 offset:54272
	ds_read_b128 v[218:221], v188 offset:55296
	ds_read_b128 v[222:225], v188 offset:56320
	global_load_lds_dwordx4 v164, s[98:99]
	s_add_i32 m0, s28, 0x2000
	s_add_u32 s26, s26, 0xe0080
	s_addc_u32 s27, s27, 0
	s_add_i32 s28, s60, s31
	global_load_lds_dwordx4 v168, s[98:99]
	s_mov_b32 m0, s28
	s_nop 0
	global_load_lds_dwordx4 v164, s[26:27]
	s_add_i32 m0, s28, 0x2000
	s_nop 0
	global_load_lds_dwordx4 v168, s[26:27]
	s_mov_b32 m0, s39
	s_nop 0
	global_load_lds_dwordx4 v162, s[100:101]
	s_mov_b32 m0, s40
	s_nop 0
	global_load_lds_dwordx4 v166, s[100:101]
	s_waitcnt vmcnt(8)
	s_waitcnt lgkmcnt(0)
	s_barrier
	s_setprio 1
	s_waitcnt lgkmcnt(0)
	v_mfma_scale_f32_16x16x128_f8f6f4 v[94:97], v[2:9], v[194:201], v[94:97], v187, v192 op_sel_hi:[0,0,0]
	v_mfma_scale_f32_16x16x128_f8f6f4 v[90:93], v[10:17], v[194:201], v[90:93], v187, v192 op_sel_hi:[0,0,0]
	v_mfma_scale_f32_16x16x128_f8f6f4 v[86:89], v[2:9], v[202:209], v[86:89], v187, v192 op_sel_hi:[0,0,0]
	v_mfma_scale_f32_16x16x128_f8f6f4 v[78:81], v[10:17], v[202:209], v[78:81], v187, v192 op_sel_hi:[0,0,0]
	v_mfma_scale_f32_16x16x128_f8f6f4 v[70:73], v[2:9], v[210:217], v[70:73], v187, v192 op_sel_hi:[0,0,0]
	v_mfma_scale_f32_16x16x128_f8f6f4 v[62:65], v[10:17], v[210:217], v[62:65], v187, v192 op_sel_hi:[0,0,0]
	v_mfma_scale_f32_16x16x128_f8f6f4 v[54:57], v[2:9], v[218:225], v[54:57], v187, v192 op_sel_hi:[0,0,0]
	v_mfma_scale_f32_16x16x128_f8f6f4 v[46:49], v[10:17], v[218:225], v[46:49], v187, v192 op_sel_hi:[0,0,0]
	s_setprio 0
	s_setprio 1
	v_mfma_scale_f32_16x16x128_f8f6f4 v[82:85], v[18:25], v[194:201], v[82:85], v187, v192 op_sel_hi:[0,0,0]
	v_mfma_scale_f32_16x16x128_f8f6f4 v[74:77], v[26:33], v[194:201], v[74:77], v187, v192 op_sel_hi:[0,0,0]
	v_mfma_scale_f32_16x16x128_f8f6f4 v[66:69], v[18:25], v[202:209], v[66:69], v187, v192 op_sel_hi:[0,0,0]
	v_mfma_scale_f32_16x16x128_f8f6f4 v[58:61], v[26:33], v[202:209], v[58:61], v187, v192 op_sel_hi:[0,0,0]
	v_mfma_scale_f32_16x16x128_f8f6f4 v[50:53], v[18:25], v[210:217], v[50:53], v187, v192 op_sel_hi:[0,0,0]
	v_mfma_scale_f32_16x16x128_f8f6f4 v[42:45], v[26:33], v[210:217], v[42:45], v187, v192 op_sel_hi:[0,0,0]
	v_mfma_scale_f32_16x16x128_f8f6f4 v[38:41], v[18:25], v[218:225], v[38:41], v187, v192 op_sel_hi:[0,0,0]
	v_mfma_scale_f32_16x16x128_f8f6f4 v[34:37], v[26:33], v[218:225], v[34:37], v187, v192 op_sel_hi:[0,0,0]
	s_setprio 0
	s_barrier
	s_add_i32 s58, s58, 2
	s_add_u32 s24, s24, 0x100
	s_addc_u32 s25, s25, 0
	s_add_u32 s56, s56, 0x100
	s_addc_u32 s57, s57, 0
	s_cmp_gt_u32 s58, 53
